# v59 + 18 wave-wide f32 sum ladders (ds_bpermute xor butterfly with lgkmcnt waits) replaced by DPP quad_perm/row_mirror adds and permlane16/32 swaps; bit-identical
# baseline (speedup 1.0000x reference)
.LBB0_103:
	s_add_i32 s16, s25, s40
	s_ashr_i32 s17, s16, 31
	s_lshl_b64 s[10:11], s[16:17], 12
	s_waitcnt lgkmcnt(0)
	v_lshl_add_u64 v[16:17], v[38:39], 0, s[10:11]
	global_load_dwordx4 v[78:81], v[16:17], off nt
	global_load_dwordx4 v[82:85], v[16:17], off offset:1024 nt
	global_load_dwordx4 v[86:89], v[16:17], off offset:2048 nt
	global_load_dwordx4 v[90:93], v[16:17], off offset:3072 nt
	s_lshl_b64 s[10:11], s[16:17], 10
	v_lshl_add_u64 v[126:127], v[40:41], 0, s[10:11]
	s_add_i32 s18, s16, 1
	s_ashr_i32 s19, s18, 31
	s_lshl_b64 s[20:21], s[18:19], 12
	v_lshl_add_u64 v[24:25], v[38:39], 0, s[20:21]
	ds_read_b128 v[94:97], v70
	ds_read_b128 v[98:101], v70 offset:1024
	ds_read_b128 v[102:105], v70 offset:2048
	ds_read_b128 v[106:109], v70 offset:3072
	ds_read_b128 v[110:113], v70 offset:7168
	ds_read_b128 v[114:117], v70 offset:6144
	ds_read_b128 v[118:121], v70 offset:5120
	ds_read_b128 v[122:125], v70 offset:4096
	v_mov_b32_e32 v45, 0
	v_mov_b32_e32 v77, 0
	v_mov_b32_e32 v144, 0
	v_mov_b32_e32 v145, 0
	s_waitcnt vmcnt(3)
	v_pk_fma_f32 v[16:17], v[78:79], v[78:79], 0 op_sel_hi:[1,1,0]
	s_nop 0
	v_pk_fma_f32 v[16:17], v[80:81], v[80:81], v[16:17]
	s_waitcnt vmcnt(2)
	v_pk_fma_f32 v[16:17], v[82:83], v[82:83], v[16:17]
	s_nop 0
	v_pk_fma_f32 v[16:17], v[84:85], v[84:85], v[16:17]
	s_waitcnt vmcnt(1)
	v_pk_fma_f32 v[16:17], v[86:87], v[86:87], v[16:17]
	s_nop 0
	v_pk_fma_f32 v[16:17], v[88:89], v[88:89], v[16:17]
	s_waitcnt vmcnt(0)
	v_pk_fma_f32 v[16:17], v[90:91], v[90:91], v[16:17]
	s_nop 0
	v_pk_fma_f32 v[16:17], v[92:93], v[92:93], v[16:17]
	s_nop 0
	v_add_f32_e32 v16, v16, v17
	s_waitcnt lgkmcnt(0)
	s_nop 1
	v_add_f32_dpp v16, v16, v16 quad_perm:[1,0,3,2] row_mask:0xf bank_mask:0xf
	s_waitcnt lgkmcnt(0)
	s_nop 1
	v_add_f32_dpp v16, v16, v16 quad_perm:[2,3,0,1] row_mask:0xf bank_mask:0xf
	s_waitcnt lgkmcnt(0)
	s_nop 1
	v_add_f32_dpp v16, v16, v16 row_half_mirror row_mask:0xf bank_mask:0xf
	s_waitcnt lgkmcnt(0)
	s_nop 1
	v_add_f32_dpp v16, v16, v16 row_mirror row_mask:0xf bank_mask:0xf
	s_waitcnt lgkmcnt(0)
	v_mov_b32_e32 v17, v16
	s_nop 1
	v_permlane16_swap_b32_e32 v16, v17
	v_add_f32_e32 v16, v16, v17
	s_waitcnt lgkmcnt(0)
	v_mov_b32_e32 v17, v16
	s_nop 1
	v_permlane32_swap_b32_e32 v16, v17
	v_add_f32_e32 v16, v16, v17
	v_fmamk_f32 v16, v16, 0x3a800000, v35
	v_mul_f32_e32 v17, 0x4f800000, v16
	v_cmp_gt_f32_e32 vcc, s28, v16
	s_nop 1
	v_cndmask_b32_e32 v26, v16, v17, vcc
	v_sqrt_f32_e32 v27, v26
	global_load_dwordx4 v[20:23], v[24:25], off nt
	global_load_dwordx4 v[16:19], v[24:25], off offset:1024 nt
	v_add_u32_e32 v28, -1, v27
	v_add_u32_e32 v29, 1, v27
	v_fma_f32 v30, -v28, v27, v26
	v_fma_f32 v31, -v29, v27, v26
	v_cmp_ge_f32_e64 s[10:11], 0, v30
	s_nop 1
	v_cndmask_b32_e64 v27, v27, v28, s[10:11]
	v_cmp_lt_f32_e64 s[10:11], 0, v31
	s_nop 1
	v_cndmask_b32_e64 v27, v27, v29, s[10:11]
	v_mul_f32_e32 v28, 0x37800000, v27
	v_cndmask_b32_e32 v27, v27, v28, vcc
	v_cmp_class_f32_e32 vcc, v26, v71
	s_nop 1
	v_cndmask_b32_e32 v128, v27, v26, vcc
	global_load_dwordx4 v[28:31], v[24:25], off offset:2048 nt
	s_nop 0
	global_load_dwordx4 v[24:27], v[24:25], off offset:3072 nt
	v_div_scale_f32 v129, s[10:11], v128, v128, 1.0
	v_rcp_f32_e32 v130, v129
	v_div_scale_f32 v131, vcc, 1.0, v128, 1.0
	v_fma_f32 v132, -v129, v130, 1.0
	v_fmac_f32_e32 v130, v132, v130
	v_mul_f32_e32 v132, v131, v130
	v_fma_f32 v133, -v129, v132, v131
	v_fmac_f32_e32 v132, v133, v130
	v_fma_f32 v129, -v129, v132, v131
	v_div_fmas_f32 v129, v129, v130, v132
	v_div_fixup_f32 v128, v129, v128, 1.0
	v_pk_mul_f32 v[78:79], v[78:79], v[128:129] op_sel_hi:[1,0]
	v_pk_mul_f32 v[82:83], v[82:83], v[128:129] op_sel_hi:[1,0]
	v_pk_fma_f32 v[130:131], v[50:51], v[78:79], v[0:1]
	v_pk_mul_f32 v[86:87], v[86:87], v[128:129] op_sel_hi:[1,0]
	v_pk_fma_f32 v[134:135], v[54:55], v[82:83], v[4:5]
	v_mul_f32_e32 v82, 0x41000000, v130
	v_mul_f32_e32 v83, 0x41000000, v131
	v_pk_mul_f32 v[80:81], v[80:81], v[128:129] op_sel_hi:[1,0]
	v_pk_mul_f32 v[90:91], v[90:91], v[128:129] op_sel_hi:[1,0]
	v_pk_fma_f32 v[138:139], v[58:59], v[86:87], v[8:9]
	v_mul_f32_e32 v86, 0x41000000, v134
	v_mul_f32_e32 v87, 0x41000000, v135
	v_med3_f32 v82, v82, s29, v73
	v_med3_f32 v83, v83, s29, v73
	v_pk_mul_f32 v[84:85], v[84:85], v[128:129] op_sel_hi:[1,0]
	v_pk_mul_f32 v[88:89], v[88:89], v[128:129] op_sel_hi:[1,0]
	v_pk_mul_f32 v[92:93], v[92:93], v[128:129] op_sel_hi:[1,0]
	v_pk_fma_f32 v[128:129], v[48:49], v[80:81], v[2:3]
	v_pk_fma_f32 v[142:143], v[62:63], v[90:91], v[12:13]
	v_mul_f32_e32 v90, 0x41000000, v138
	v_mul_f32_e32 v91, 0x41000000, v139
	v_pk_fma_f32 v[80:81], v[130:131], v[122:123], 0 op_sel_hi:[1,1,0]
	v_med3_f32 v86, v86, s29, v73
	v_med3_f32 v87, v87, s29, v73
	v_cvt_pk_fp8_f32 v45, v82, v83
	v_mul_f32_e32 v146, 0x41000000, v142
	v_mul_f32_e32 v147, 0x41000000, v143
	v_pk_fma_f32 v[78:79], v[130:131], v[94:95], 0 op_sel_hi:[1,1,0]
	v_med3_f32 v90, v90, s29, v73
	v_med3_f32 v91, v91, s29, v73
	v_pk_fma_f32 v[80:81], v[128:129], v[124:125], v[80:81]
	v_cvt_pk_fp8_f32 v77, v86, v87
	v_pk_fma_f32 v[132:133], v[52:53], v[84:85], v[6:7]
	v_mul_f32_e32 v84, 0x41000000, v128
	v_mul_f32_e32 v85, 0x41000000, v129
	v_med3_f32 v94, v146, s29, v73
	v_med3_f32 v95, v147, s29, v73
	v_pk_fma_f32 v[78:79], v[128:129], v[96:97], v[78:79]
	v_cvt_pk_fp8_f32 v144, v90, v91
	v_pk_fma_f32 v[80:81], v[134:135], v[118:119], v[80:81]
	v_pk_fma_f32 v[136:137], v[56:57], v[88:89], v[10:11]
	v_mul_f32_e32 v88, 0x41000000, v132
	v_mul_f32_e32 v89, 0x41000000, v133
	v_med3_f32 v84, v84, s29, v73
	v_med3_f32 v85, v85, s29, v73
	v_cvt_pk_fp8_f32 v145, v94, v95
	v_pk_fma_f32 v[78:79], v[134:135], v[98:99], v[78:79]
	v_pk_fma_f32 v[80:81], v[132:133], v[120:121], v[80:81]
	v_pk_fma_f32 v[140:141], v[60:61], v[92:93], v[14:15]
	v_mul_f32_e32 v92, 0x41000000, v136
	v_mul_f32_e32 v93, 0x41000000, v137
	v_med3_f32 v88, v88, s29, v73
	v_med3_f32 v89, v89, s29, v73
	v_pk_fma_f32 v[78:79], v[132:133], v[100:101], v[78:79]
	v_pk_fma_f32 v[80:81], v[138:139], v[114:115], v[80:81]
	v_cvt_pk_fp8_f32 v45, v84, v85 op_sel:[0,0,1]
	v_mul_f32_e32 v148, 0x41000000, v140
	v_mul_f32_e32 v149, 0x41000000, v141
	v_med3_f32 v92, v92, s29, v73
	v_med3_f32 v93, v93, s29, v73
	v_pk_fma_f32 v[78:79], v[138:139], v[102:103], v[78:79]
	v_pk_fma_f32 v[80:81], v[136:137], v[116:117], v[80:81]
	v_cvt_pk_fp8_f32 v77, v88, v89 op_sel:[0,0,1]
	v_med3_f32 v122, v148, s29, v73
	v_med3_f32 v123, v149, s29, v73
	v_pk_fma_f32 v[78:79], v[136:137], v[104:105], v[78:79]
	v_cvt_pk_fp8_f32 v144, v92, v93 op_sel:[0,0,1]
	v_pk_fma_f32 v[80:81], v[142:143], v[110:111], v[80:81]
	v_cvt_pk_fp8_f32 v145, v122, v123 op_sel:[0,0,1]
	v_pk_fma_f32 v[78:79], v[142:143], v[106:107], v[78:79]
	v_pk_fma_f32 v[80:81], v[140:141], v[112:113], v[80:81]
	v_pk_fma_f32 v[78:79], v[140:141], v[108:109], v[78:79]
	global_store_dword v[126:127], v45, off
	global_store_dword v[126:127], v77, off offset:256
	global_store_dword v[126:127], v144, off offset:512
	global_store_dword v[126:127], v145, off offset:768
	v_add_f32_e32 v45, v80, v81
	v_add_f32_e32 v94, v78, v79
	ds_read_b128 v[78:81], v70 offset:8192
	ds_read_b128 v[82:85], v70 offset:9216
	ds_read_b128 v[86:89], v70 offset:10240
	ds_read_b128 v[90:93], v70 offset:11264
	s_waitcnt lgkmcnt(3)
	v_pk_fma_f32 v[78:79], v[130:131], v[78:79], 0 op_sel_hi:[1,1,0]
	s_nop 0
	v_pk_fma_f32 v[78:79], v[128:129], v[80:81], v[78:79]
	s_waitcnt lgkmcnt(2)
	v_pk_fma_f32 v[78:79], v[134:135], v[82:83], v[78:79]
	s_nop 0
	v_pk_fma_f32 v[78:79], v[132:133], v[84:85], v[78:79]
	s_waitcnt lgkmcnt(1)
	v_pk_fma_f32 v[78:79], v[138:139], v[86:87], v[78:79]
	s_nop 0
	v_pk_fma_f32 v[78:79], v[136:137], v[88:89], v[78:79]
	s_waitcnt lgkmcnt(0)
	v_pk_fma_f32 v[86:87], v[142:143], v[90:91], v[78:79]
	ds_read_b128 v[78:81], v70 offset:13312
	ds_read_b128 v[82:85], v70 offset:12288
	v_pk_fma_f32 v[86:87], v[140:141], v[92:93], v[86:87]
	s_waitcnt lgkmcnt(0)
	v_pk_fma_f32 v[82:83], v[130:131], v[82:83], 0 op_sel_hi:[1,1,0]
	v_add_f32_e32 v77, v86, v87
	ds_read_b128 v[86:89], v70 offset:15360
	ds_read_b128 v[90:93], v70 offset:14336
	v_pk_fma_f32 v[82:83], v[128:129], v[84:85], v[82:83]
	s_nop 0
	v_pk_fma_f32 v[78:79], v[134:135], v[78:79], v[82:83]
	s_nop 0
	v_pk_fma_f32 v[78:79], v[132:133], v[80:81], v[78:79]
	s_waitcnt lgkmcnt(0)
	v_pk_fma_f32 v[78:79], v[138:139], v[90:91], v[78:79]
	s_nop 0
	v_pk_fma_f32 v[78:79], v[136:137], v[92:93], v[78:79]
	s_nop 0
	v_pk_fma_f32 v[78:79], v[142:143], v[86:87], v[78:79]
	s_nop 0
	v_pk_fma_f32 v[78:79], v[140:141], v[88:89], v[78:79]
	s_nop 0
	v_add_f32_e32 v95, v78, v79
	ds_read_b128 v[78:81], v70 offset:16384
	ds_read_b128 v[82:85], v70 offset:17408
	ds_read_b128 v[86:89], v70 offset:18432
	ds_read_b128 v[90:93], v70 offset:19456
	s_waitcnt lgkmcnt(3)
	v_pk_fma_f32 v[78:79], v[130:131], v[78:79], 0 op_sel_hi:[1,1,0]
	s_nop 0
	v_pk_fma_f32 v[78:79], v[128:129], v[80:81], v[78:79]
	s_waitcnt lgkmcnt(2)
	v_pk_fma_f32 v[78:79], v[134:135], v[82:83], v[78:79]
	s_nop 0
	v_pk_fma_f32 v[78:79], v[132:133], v[84:85], v[78:79]
	s_waitcnt lgkmcnt(1)
	v_pk_fma_f32 v[78:79], v[138:139], v[86:87], v[78:79]
	s_nop 0
	v_pk_fma_f32 v[78:79], v[136:137], v[88:89], v[78:79]
	s_waitcnt lgkmcnt(0)
	v_pk_fma_f32 v[86:87], v[142:143], v[90:91], v[78:79]
	ds_read_b128 v[78:81], v70 offset:21504
	ds_read_b128 v[82:85], v70 offset:20480
	v_pk_fma_f32 v[86:87], v[140:141], v[92:93], v[86:87]
	s_waitcnt lgkmcnt(0)
	v_pk_fma_f32 v[82:83], v[130:131], v[82:83], 0 op_sel_hi:[1,1,0]
	v_add_f32_e32 v96, v86, v87
	ds_read_b128 v[86:89], v70 offset:23552
	ds_read_b128 v[90:93], v70 offset:22528
	v_pk_fma_f32 v[82:83], v[128:129], v[84:85], v[82:83]
	s_nop 0
	v_pk_fma_f32 v[78:79], v[134:135], v[78:79], v[82:83]
	s_nop 0
	v_pk_fma_f32 v[78:79], v[132:133], v[80:81], v[78:79]
	s_waitcnt lgkmcnt(0)
	v_pk_fma_f32 v[78:79], v[138:139], v[90:91], v[78:79]
	s_nop 0
	v_pk_fma_f32 v[78:79], v[136:137], v[92:93], v[78:79]
	s_nop 0
	v_pk_fma_f32 v[78:79], v[142:143], v[86:87], v[78:79]
	s_nop 0
	v_pk_fma_f32 v[78:79], v[140:141], v[88:89], v[78:79]
	s_nop 0
	v_add_f32_e32 v97, v78, v79
	ds_read_b128 v[78:81], v70 offset:24576
	ds_read_b128 v[82:85], v70 offset:25600
	ds_read_b128 v[86:89], v70 offset:26624
	ds_read_b128 v[90:93], v70 offset:27648
	s_waitcnt lgkmcnt(3)
	v_pk_fma_f32 v[78:79], v[130:131], v[78:79], 0 op_sel_hi:[1,1,0]
	s_nop 0
	v_pk_fma_f32 v[78:79], v[128:129], v[80:81], v[78:79]
	s_waitcnt lgkmcnt(2)
	v_pk_fma_f32 v[78:79], v[134:135], v[82:83], v[78:79]
	s_nop 0
	v_pk_fma_f32 v[78:79], v[132:133], v[84:85], v[78:79]
	s_waitcnt lgkmcnt(1)
	v_pk_fma_f32 v[78:79], v[138:139], v[86:87], v[78:79]
	s_nop 0
	v_pk_fma_f32 v[78:79], v[136:137], v[88:89], v[78:79]
	s_waitcnt lgkmcnt(0)
	v_pk_fma_f32 v[86:87], v[142:143], v[90:91], v[78:79]
	ds_read_b128 v[78:81], v70 offset:29696
	ds_read_b128 v[82:85], v70 offset:28672
	v_pk_fma_f32 v[86:87], v[140:141], v[92:93], v[86:87]
	s_waitcnt lgkmcnt(0)
	v_pk_fma_f32 v[82:83], v[130:131], v[82:83], 0 op_sel_hi:[1,1,0]
	v_add_f32_e32 v98, v86, v87
	ds_read_b128 v[86:89], v70 offset:31744
	ds_read_b128 v[90:93], v70 offset:30720
	v_pk_fma_f32 v[82:83], v[128:129], v[84:85], v[82:83]
	s_nop 0
	v_pk_fma_f32 v[78:79], v[134:135], v[78:79], v[82:83]
	s_nop 0
	v_pk_fma_f32 v[78:79], v[132:133], v[80:81], v[78:79]
	s_waitcnt lgkmcnt(0)
	v_pk_fma_f32 v[78:79], v[138:139], v[90:91], v[78:79]
	s_nop 0
	v_pk_fma_f32 v[78:79], v[136:137], v[92:93], v[78:79]
	s_nop 0
	v_pk_fma_f32 v[78:79], v[142:143], v[86:87], v[78:79]
	s_nop 0
	v_pk_fma_f32 v[78:79], v[140:141], v[88:89], v[78:79]
	s_nop 0
	v_add_f32_e32 v78, v78, v79
	v_cndmask_b32_e64 v79, v94, v96, s[2:3]
	ds_bpermute_b32 v79, v69, v79
	v_cndmask_b32_e64 v80, v96, v94, s[2:3]
	v_cndmask_b32_e64 v81, v45, v97, s[2:3]
	v_cndmask_b32_e64 v82, v95, v78, s[2:3]
	ds_bpermute_b32 v81, v69, v81
	s_waitcnt lgkmcnt(1)
	v_add_f32_e32 v79, v80, v79
	v_cndmask_b32_e64 v80, v77, v98, s[2:3]
	ds_bpermute_b32 v80, v69, v80
	ds_bpermute_b32 v82, v69, v82
	v_cndmask_b32_e64 v45, v97, v45, s[2:3]
	v_cndmask_b32_e64 v77, v98, v77, s[2:3]
	v_cndmask_b32_e64 v78, v78, v95, s[2:3]
	s_waitcnt lgkmcnt(2)
	v_add_f32_e32 v45, v45, v81
	s_waitcnt lgkmcnt(1)
	v_add_f32_e32 v77, v77, v80
	s_waitcnt lgkmcnt(0)
	v_add_f32_e32 v78, v78, v82
	v_cndmask_b32_e64 v80, v79, v77, s[4:5]
	v_cndmask_b32_e64 v81, v45, v78, s[4:5]
	ds_bpermute_b32 v80, v68, v80
	ds_bpermute_b32 v81, v68, v81
	v_cndmask_b32_e64 v77, v77, v79, s[4:5]
	v_cndmask_b32_e64 v45, v78, v45, s[4:5]
	s_waitcnt lgkmcnt(1)
	v_add_f32_e32 v77, v77, v80
	s_waitcnt lgkmcnt(0)
	v_add_f32_e32 v45, v45, v81
	v_cndmask_b32_e64 v78, v77, v45, s[6:7]
	ds_bpermute_b32 v78, v67, v78
	v_cndmask_b32_e64 v45, v45, v77, s[6:7]
	s_waitcnt lgkmcnt(0)
	v_add_f32_e32 v45, v45, v78
	ds_bpermute_b32 v77, v66, v45
	s_waitcnt lgkmcnt(0)
	v_add_f32_e32 v45, v45, v77
	ds_bpermute_b32 v77, v65, v45
	s_waitcnt lgkmcnt(0)
	v_add_f32_e32 v45, v45, v77
	ds_bpermute_b32 v77, v64, v45
	s_and_saveexec_b64 s[10:11], s[8:9]
	s_cbranch_execz .LBB0_105
	global_load_dword v78, v[42:43], off
	s_waitcnt lgkmcnt(0)
	v_add_f32_e32 v45, v45, v77
	s_add_i32 s20, s39, s40
	s_ashr_i32 s21, s20, 31
	s_waitcnt vmcnt(0)
	v_add_f32_e32 v45, v45, v78
	v_mul_f32_e64 v77, |v45|, s30
	v_exp_f32_e32 v77, v77
	v_min_f32_e32 v92, 0, v45
	v_add_f32_e32 v45, 1.0, v77
	v_add_f32_e32 v80, -1.0, v45
	v_frexp_mant_f32_e32 v81, v45
	v_cvt_f64_f32_e32 v[78:79], v45
	v_sub_f32_e32 v82, v80, v45
	v_frexp_exp_i32_f64_e32 v78, v[78:79]
	v_cmp_gt_f32_e32 vcc, s31, v81
	v_sub_f32_e32 v80, v77, v80
	v_add_f32_e32 v79, 1.0, v82
	v_subbrev_co_u32_e32 v78, vcc, 0, v78, vcc
	v_add_f32_e32 v79, v80, v79
	v_sub_u32_e32 v80, 0, v78
	v_ldexp_f32 v45, v45, v80
	v_ldexp_f32 v79, v79, v80
	v_add_f32_e32 v80, -1.0, v45
	v_add_f32_e32 v82, 1.0, v45
	v_add_f32_e32 v81, 1.0, v80
	v_add_f32_e32 v83, -1.0, v82
	v_sub_f32_e32 v81, v45, v81
	v_sub_f32_e32 v45, v45, v83
	v_add_f32_e32 v45, v79, v45
	v_add_f32_e32 v83, v79, v81
	v_add_f32_e32 v79, v82, v45
	v_rcp_f32_e32 v86, v79
	v_add_f32_e32 v81, v80, v83
	v_sub_f32_e32 v82, v79, v82
	v_sub_f32_e32 v45, v45, v82
	v_mul_f32_e32 v88, v81, v86
	v_mul_f32_e32 v82, v79, v88
	v_fma_f32 v84, v88, v79, -v82
	v_sub_f32_e32 v80, v81, v80
	v_fmac_f32_e32 v84, v88, v45
	v_sub_f32_e32 v87, v83, v80
	v_add_f32_e32 v80, v82, v84
	v_sub_f32_e32 v83, v81, v80
	v_mov_b32_e32 v85, v80
	v_pk_add_f32 v[80:81], v[80:81], v[82:83] neg_lo:[0,1] neg_hi:[0,1]
	v_cvt_f32_i32_e32 v78, v78
	v_pk_add_f32 v[80:81], v[80:81], v[84:85] neg_lo:[0,1] neg_hi:[0,1]
	v_cmp_neq_f32_e32 vcc, s34, v77
	v_add_f32_e32 v81, v87, v81
	v_add_f32_e32 v80, v80, v81
	v_add_f32_e32 v81, v83, v80
	v_mul_f32_e32 v85, v86, v81
	v_mul_f32_e32 v82, v79, v85
	v_fma_f32 v84, v85, v79, -v82
	v_sub_f32_e32 v83, v83, v81
	v_fmac_f32_e32 v84, v85, v45
	v_add_f32_e32 v87, v80, v83
	v_add_f32_e32 v89, v88, v85
	v_add_f32_e32 v80, v82, v84
	v_sub_f32_e32 v79, v89, v88
	v_sub_f32_e32 v83, v81, v80
	v_sub_f32_e32 v45, v85, v79
	v_mov_b32_e32 v85, v80
	v_pk_add_f32 v[80:81], v[80:81], v[82:83] neg_lo:[0,1] neg_hi:[0,1]
	s_nop 0
	v_pk_add_f32 v[80:81], v[80:81], v[84:85] neg_lo:[0,1] neg_hi:[0,1]
	s_nop 0
	v_add_f32_e32 v79, v87, v81
	v_add_f32_e32 v79, v80, v79
	v_add_f32_e32 v79, v83, v79
	v_mul_f32_e32 v79, v86, v79
	v_add_f32_e32 v45, v45, v79
	v_add_f32_e32 v79, v89, v45
	v_mul_f32_e32 v80, v79, v79
	v_sub_f32_e32 v82, v79, v89
	v_fmamk_f32 v83, v80, 0x3e9b6dac, v72
	v_ldexp_f32 v81, v79, 1
	v_sub_f32_e32 v82, v45, v82
	v_mul_f32_e32 v79, v79, v80
	v_fmaak_f32 v45, v80, v83, 0x3f2aaada
	v_ldexp_f32 v85, v82, 1
	v_pk_mul_f32 v[82:83], v[78:79], v[44:45]
	s_nop 0
	v_fma_f32 v80, v78, s33, -v82
	v_fmac_f32_e32 v80, 0xb102e308, v78
	v_pk_add_f32 v[78:79], v[82:83], v[80:81]
	v_mov_b32_e32 v84, v82
	v_sub_f32_e32 v45, v79, v81
	v_sub_f32_e32 v45, v83, v45
	v_add_f32_e32 v85, v85, v45
	v_pk_add_f32 v[86:87], v[78:79], v[82:83] neg_lo:[0,1] neg_hi:[0,1]
	v_pk_add_f32 v[82:83], v[78:79], v[84:85]
	v_mov_b32_e32 v81, v78
	v_mov_b32_e32 v87, v83
	v_pk_add_f32 v[90:91], v[80:81], v[86:87] neg_lo:[0,1] neg_hi:[0,1]
	v_pk_add_f32 v[80:81], v[80:81], v[86:87]
	v_mov_b32_e32 v89, v78
	v_pk_add_f32 v[86:87], v[80:81], v[78:79] op_sel:[1,0] op_sel_hi:[0,1] neg_lo:[0,1] neg_hi:[0,1]
	v_mov_b32_e32 v88, v85
	v_mov_b32_e32 v84, v83
	v_mov_b32_e32 v85, v81
	v_pk_mov_b32 v[78:79], v[78:79], v[86:87] op_sel:[1,0]
	v_pk_add_f32 v[82:83], v[82:83], v[86:87] op_sel_hi:[1,0] neg_lo:[0,1] neg_hi:[0,1]
	v_pk_add_f32 v[78:79], v[84:85], v[78:79] neg_lo:[0,1] neg_hi:[0,1]
	v_mov_b32_e32 v82, v90
	v_pk_add_f32 v[78:79], v[88:89], v[78:79] neg_lo:[0,1] neg_hi:[0,1]
	v_mov_b32_e32 v91, v81
	v_pk_add_f32 v[82:83], v[82:83], v[78:79]
	s_nop 0
	v_pk_add_f32 v[84:85], v[82:83], v[82:83] op_sel:[0,1] op_sel_hi:[1,0]
	s_nop 0
	v_pk_add_f32 v[80:81], v[80:81], v[84:85] op_sel:[1,0] op_sel_hi:[0,1]
	v_mov_b32_e32 v83, v80
	v_mov_b32_e32 v79, v84
	v_pk_add_f32 v[84:85], v[82:83], v[90:91] neg_lo:[0,1] neg_hi:[0,1]
	s_nop 0
	v_sub_f32_e32 v45, v82, v84
	v_pk_add_f32 v[78:79], v[78:79], v[84:85] neg_lo:[0,1] neg_hi:[0,1]
	v_sub_f32_e32 v45, v90, v45
	v_add_f32_e32 v45, v78, v45
	v_add_f32_e32 v45, v45, v79
	v_add_f32_e32 v45, v80, v45
	v_cndmask_b32_e32 v45, v74, v45, vcc
	v_cmp_ngt_f32_e32 vcc, -1.0, v77
	v_lshl_add_u64 v[78:79], s[20:21], 2, v[46:47]
	s_nop 0
	v_cndmask_b32_e32 v45, v75, v45, vcc
	v_cmp_neq_f32_e32 vcc, -1.0, v77
	s_nop 1
	v_cndmask_b32_e32 v45, v76, v45, vcc
	v_cmp_lt_f32_e64 vcc, |v77|, s35
	s_nop 1
	v_cndmask_b32_e32 v45, v45, v77, vcc
	v_sub_f32_e32 v45, v92, v45
	global_store_dword v[78:79], v45, off
.LBB0_105:
	s_or_b64 exec, exec, s[10:11]
	s_waitcnt vmcnt(7)
	v_pk_fma_f32 v[78:79], v[20:21], v[20:21], 0 op_sel_hi:[1,1,0]
	v_mov_b32_e32 v88, 0
	v_pk_fma_f32 v[78:79], v[22:23], v[22:23], v[78:79]
	s_lshl_b64 s[18:19], s[18:19], 10
	s_waitcnt vmcnt(6)
	v_pk_fma_f32 v[78:79], v[16:17], v[16:17], v[78:79]
	v_lshl_add_u64 v[82:83], v[40:41], 0, s[18:19]
	v_pk_fma_f32 v[78:79], v[18:19], v[18:19], v[78:79]
	s_waitcnt vmcnt(5)
	v_pk_fma_f32 v[78:79], v[28:29], v[28:29], v[78:79]
	s_nop 0
	v_pk_fma_f32 v[78:79], v[30:31], v[30:31], v[78:79]
	s_waitcnt vmcnt(4)
	v_pk_fma_f32 v[78:79], v[24:25], v[24:25], v[78:79]
	s_nop 0
	v_pk_fma_f32 v[78:79], v[26:27], v[26:27], v[78:79]
	s_nop 0
	v_add_f32_e32 v45, v78, v79
	s_waitcnt lgkmcnt(0)
	s_waitcnt lgkmcnt(0)
	s_nop 1
	v_add_f32_dpp v45, v45, v45 quad_perm:[1,0,3,2] row_mask:0xf bank_mask:0xf
	s_waitcnt lgkmcnt(0)
	s_nop 1
	v_add_f32_dpp v45, v45, v45 quad_perm:[2,3,0,1] row_mask:0xf bank_mask:0xf
	s_waitcnt lgkmcnt(0)
	s_nop 1
	v_add_f32_dpp v45, v45, v45 row_half_mirror row_mask:0xf bank_mask:0xf
	s_waitcnt lgkmcnt(0)
	s_nop 1
	v_add_f32_dpp v45, v45, v45 row_mirror row_mask:0xf bank_mask:0xf
	s_waitcnt lgkmcnt(0)
	v_mov_b32_e32 v77, v45
	s_nop 1
	v_permlane16_swap_b32_e32 v45, v77
	v_add_f32_e32 v45, v45, v77
	s_waitcnt lgkmcnt(0)
	v_mov_b32_e32 v77, v45
	s_nop 1
	v_permlane32_swap_b32_e32 v45, v77
	v_add_f32_e32 v45, v45, v77
	v_fmamk_f32 v45, v45, 0x3a800000, v35
	v_mul_f32_e32 v77, 0x4f800000, v45
	v_cmp_gt_f32_e32 vcc, s28, v45
	s_nop 1
	v_cndmask_b32_e32 v45, v45, v77, vcc
	v_sqrt_f32_e32 v77, v45
	s_nop 0
	v_add_u32_e32 v78, -1, v77
	v_add_u32_e32 v79, 1, v77
	v_fma_f32 v80, -v78, v77, v45
	v_fma_f32 v81, -v79, v77, v45
	v_cmp_ge_f32_e64 s[10:11], 0, v80
	s_nop 1
	v_cndmask_b32_e64 v77, v77, v78, s[10:11]
	v_cmp_lt_f32_e64 s[10:11], 0, v81
	s_nop 1
	v_cndmask_b32_e64 v77, v77, v79, s[10:11]
	v_mul_f32_e32 v78, 0x37800000, v77
	v_cndmask_b32_e32 v77, v77, v78, vcc
	v_cmp_class_f32_e32 vcc, v45, v71
	s_nop 1
	v_cndmask_b32_e32 v45, v77, v45, vcc
	v_div_scale_f32 v77, s[10:11], v45, v45, 1.0
	v_rcp_f32_e32 v78, v77
	v_div_scale_f32 v79, vcc, 1.0, v45, 1.0
	v_fma_f32 v80, -v77, v78, 1.0
	v_fmac_f32_e32 v78, v80, v78
	v_mul_f32_e32 v80, v79, v78
	v_fma_f32 v81, -v77, v80, v79
	v_fmac_f32_e32 v80, v81, v78
	v_fma_f32 v77, -v77, v80, v79
	v_div_fmas_f32 v77, v77, v78, v80
	v_div_fixup_f32 v78, v77, v45, 1.0
	v_pk_mul_f32 v[20:21], v[20:21], v[78:79] op_sel_hi:[1,0]
	v_pk_mul_f32 v[84:85], v[30:31], v[78:79] op_sel_hi:[1,0]
	v_pk_fma_f32 v[30:31], v[50:51], v[20:21], v[0:1]
	v_pk_mul_f32 v[22:23], v[22:23], v[78:79] op_sel_hi:[1,0]
	v_mul_f32_e32 v45, 0x41000000, v30
	v_mul_f32_e32 v77, 0x41000000, v31
	v_med3_f32 v45, v45, s29, v73
	v_med3_f32 v77, v77, s29, v73
	v_cvt_pk_fp8_f32 v88, v45, v77
	v_pk_mul_f32 v[16:17], v[16:17], v[78:79] op_sel_hi:[1,0]
	v_pk_mul_f32 v[18:19], v[18:19], v[78:79] op_sel_hi:[1,0]
	v_pk_mul_f32 v[80:81], v[28:29], v[78:79] op_sel_hi:[1,0]
	v_pk_mul_f32 v[86:87], v[24:25], v[78:79] op_sel_hi:[1,0]
	v_pk_mul_f32 v[78:79], v[26:27], v[78:79] op_sel_hi:[1,0]
	v_pk_fma_f32 v[24:25], v[48:49], v[22:23], v[2:3]
	v_pk_fma_f32 v[28:29], v[54:55], v[16:17], v[4:5]
	v_pk_fma_f32 v[16:17], v[60:61], v[78:79], v[14:15]
	v_mul_f32_e32 v78, 0x41000000, v24
	v_mul_f32_e32 v45, 0x41000000, v25
	v_med3_f32 v77, v78, s29, v73
	v_med3_f32 v45, v45, s29, v73
	v_cvt_pk_fp8_f32 v88, v77, v45 op_sel:[0,0,1]
	v_mul_f32_e32 v45, 0x41000000, v28
	v_mul_f32_e32 v77, 0x41000000, v29
	v_pk_fma_f32 v[20:21], v[52:53], v[18:19], v[6:7]
	v_pk_fma_f32 v[18:19], v[56:57], v[84:85], v[10:11]
	v_med3_f32 v45, v45, s29, v73
	v_med3_f32 v77, v77, s29, v73
	v_mov_b32_e32 v84, 0
	v_cvt_pk_fp8_f32 v84, v45, v77
	v_mul_f32_e32 v78, 0x41000000, v20
	v_mul_f32_e32 v45, 0x41000000, v21
	v_pk_fma_f32 v[26:27], v[58:59], v[80:81], v[8:9]
	v_med3_f32 v77, v78, s29, v73
	v_med3_f32 v45, v45, s29, v73
	v_cvt_pk_fp8_f32 v84, v77, v45 op_sel:[0,0,1]
	v_mul_f32_e32 v45, 0x41000000, v26
	v_mul_f32_e32 v77, 0x41000000, v27
	v_med3_f32 v45, v45, s29, v73
	v_med3_f32 v77, v77, s29, v73
	v_mov_b32_e32 v85, 0
	v_cvt_pk_fp8_f32 v85, v45, v77
	v_mul_f32_e32 v78, 0x41000000, v18
	v_mul_f32_e32 v45, 0x41000000, v19
	v_pk_fma_f32 v[22:23], v[62:63], v[86:87], v[12:13]
	v_med3_f32 v77, v78, s29, v73
	v_med3_f32 v45, v45, s29, v73
	v_cvt_pk_fp8_f32 v85, v77, v45 op_sel:[0,0,1]
	v_mul_f32_e32 v45, 0x41000000, v22
	v_mul_f32_e32 v77, 0x41000000, v23
	v_med3_f32 v45, v45, s29, v73
	v_med3_f32 v77, v77, s29, v73
	v_mov_b32_e32 v86, 0
	v_cvt_pk_fp8_f32 v86, v45, v77
	v_mul_f32_e32 v78, 0x41000000, v16
	v_mul_f32_e32 v45, 0x41000000, v17
	v_med3_f32 v77, v78, s29, v73
	v_med3_f32 v45, v45, s29, v73
	v_cvt_pk_fp8_f32 v86, v77, v45 op_sel:[0,0,1]
	ds_read_b128 v[78:81], v70
	global_store_dword v[82:83], v88, off
	global_store_dword v[82:83], v84, off offset:256
	global_store_dword v[82:83], v85, off offset:512
	global_store_dword v[82:83], v86, off offset:768
	ds_read_b128 v[82:85], v70 offset:1024
	ds_read_b128 v[86:89], v70 offset:2048
	s_waitcnt lgkmcnt(2)
	v_pk_fma_f32 v[78:79], v[30:31], v[78:79], 0 op_sel_hi:[1,1,0]
	s_nop 0
	v_pk_fma_f32 v[90:91], v[24:25], v[80:81], v[78:79]
	ds_read_b128 v[78:81], v70 offset:3072
	s_waitcnt lgkmcnt(2)
	v_pk_fma_f32 v[82:83], v[28:29], v[82:83], v[90:91]
	s_nop 0
	v_pk_fma_f32 v[82:83], v[20:21], v[84:85], v[82:83]
	s_waitcnt lgkmcnt(1)
	v_pk_fma_f32 v[82:83], v[26:27], v[86:87], v[82:83]
	s_nop 0
	v_pk_fma_f32 v[82:83], v[18:19], v[88:89], v[82:83]
	s_waitcnt lgkmcnt(0)
	v_pk_fma_f32 v[78:79], v[22:23], v[78:79], v[82:83]
	ds_read_b128 v[82:85], v70 offset:5120
	ds_read_b128 v[86:89], v70 offset:4096
	v_pk_fma_f32 v[78:79], v[16:17], v[80:81], v[78:79]
	s_waitcnt lgkmcnt(0)
	v_pk_fma_f32 v[86:87], v[30:31], v[86:87], 0 op_sel_hi:[1,1,0]
	v_add_f32_e32 v45, v78, v79
	ds_read_b128 v[78:81], v70 offset:7168
	ds_read_b128 v[90:93], v70 offset:6144
	v_pk_fma_f32 v[86:87], v[24:25], v[88:89], v[86:87]
	s_nop 0
	v_pk_fma_f32 v[82:83], v[28:29], v[82:83], v[86:87]
	s_nop 0
	v_pk_fma_f32 v[82:83], v[20:21], v[84:85], v[82:83]
	s_waitcnt lgkmcnt(0)
	v_pk_fma_f32 v[82:83], v[26:27], v[90:91], v[82:83]
	s_nop 0
	v_pk_fma_f32 v[82:83], v[18:19], v[92:93], v[82:83]
	s_nop 0
	v_pk_fma_f32 v[78:79], v[22:23], v[78:79], v[82:83]
	s_nop 0
	v_pk_fma_f32 v[78:79], v[16:17], v[80:81], v[78:79]
	s_nop 0
	v_add_f32_e32 v77, v78, v79
	ds_read_b128 v[78:81], v70 offset:8192
	ds_read_b128 v[82:85], v70 offset:9216
	ds_read_b128 v[86:89], v70 offset:10240
	ds_read_b128 v[90:93], v70 offset:11264
	s_waitcnt lgkmcnt(3)
	v_pk_fma_f32 v[78:79], v[30:31], v[78:79], 0 op_sel_hi:[1,1,0]
	s_nop 0
	v_pk_fma_f32 v[78:79], v[24:25], v[80:81], v[78:79]
	s_waitcnt lgkmcnt(2)
	v_pk_fma_f32 v[78:79], v[28:29], v[82:83], v[78:79]
	s_nop 0
	v_pk_fma_f32 v[78:79], v[20:21], v[84:85], v[78:79]
	s_waitcnt lgkmcnt(1)
	v_pk_fma_f32 v[78:79], v[26:27], v[86:87], v[78:79]
	s_nop 0
	v_pk_fma_f32 v[78:79], v[18:19], v[88:89], v[78:79]
	s_waitcnt lgkmcnt(0)
	v_pk_fma_f32 v[86:87], v[22:23], v[90:91], v[78:79]
	ds_read_b128 v[78:81], v70 offset:13312
	ds_read_b128 v[82:85], v70 offset:12288
	v_pk_fma_f32 v[86:87], v[16:17], v[92:93], v[86:87]
	s_waitcnt lgkmcnt(0)
	v_pk_fma_f32 v[82:83], v[30:31], v[82:83], 0 op_sel_hi:[1,1,0]
	v_add_f32_e32 v94, v86, v87
	ds_read_b128 v[86:89], v70 offset:15360
	ds_read_b128 v[90:93], v70 offset:14336
	v_pk_fma_f32 v[82:83], v[24:25], v[84:85], v[82:83]
	s_nop 0
	v_pk_fma_f32 v[78:79], v[28:29], v[78:79], v[82:83]
	s_nop 0
	v_pk_fma_f32 v[78:79], v[20:21], v[80:81], v[78:79]
	s_waitcnt lgkmcnt(0)
	v_pk_fma_f32 v[78:79], v[26:27], v[90:91], v[78:79]
	s_nop 0
	v_pk_fma_f32 v[78:79], v[18:19], v[92:93], v[78:79]
	s_nop 0
	v_pk_fma_f32 v[78:79], v[22:23], v[86:87], v[78:79]
	s_nop 0
	v_pk_fma_f32 v[78:79], v[16:17], v[88:89], v[78:79]
	s_nop 0
	v_add_f32_e32 v95, v78, v79
	ds_read_b128 v[78:81], v70 offset:16384
	ds_read_b128 v[82:85], v70 offset:17408
	ds_read_b128 v[86:89], v70 offset:18432
	ds_read_b128 v[90:93], v70 offset:19456
	s_waitcnt lgkmcnt(3)
	v_pk_fma_f32 v[78:79], v[30:31], v[78:79], 0 op_sel_hi:[1,1,0]
	s_nop 0
	v_pk_fma_f32 v[78:79], v[24:25], v[80:81], v[78:79]
	s_waitcnt lgkmcnt(2)
	v_pk_fma_f32 v[78:79], v[28:29], v[82:83], v[78:79]
	s_nop 0
	v_pk_fma_f32 v[78:79], v[20:21], v[84:85], v[78:79]
	s_waitcnt lgkmcnt(1)
	v_pk_fma_f32 v[78:79], v[26:27], v[86:87], v[78:79]
	s_nop 0
	v_pk_fma_f32 v[78:79], v[18:19], v[88:89], v[78:79]
	s_waitcnt lgkmcnt(0)
	v_pk_fma_f32 v[86:87], v[22:23], v[90:91], v[78:79]
	ds_read_b128 v[78:81], v70 offset:21504
	ds_read_b128 v[82:85], v70 offset:20480
	v_pk_fma_f32 v[86:87], v[16:17], v[92:93], v[86:87]
	s_waitcnt lgkmcnt(0)
	v_pk_fma_f32 v[82:83], v[30:31], v[82:83], 0 op_sel_hi:[1,1,0]
	v_add_f32_e32 v96, v86, v87
	ds_read_b128 v[86:89], v70 offset:23552
	ds_read_b128 v[90:93], v70 offset:22528
	v_pk_fma_f32 v[82:83], v[24:25], v[84:85], v[82:83]
	s_nop 0
	v_pk_fma_f32 v[78:79], v[28:29], v[78:79], v[82:83]
	s_nop 0
	v_pk_fma_f32 v[78:79], v[20:21], v[80:81], v[78:79]
	s_waitcnt lgkmcnt(0)
	v_pk_fma_f32 v[78:79], v[26:27], v[90:91], v[78:79]
	s_nop 0
	v_pk_fma_f32 v[78:79], v[18:19], v[92:93], v[78:79]
	s_nop 0
	v_pk_fma_f32 v[78:79], v[22:23], v[86:87], v[78:79]
	s_nop 0
	v_pk_fma_f32 v[78:79], v[16:17], v[88:89], v[78:79]
	s_nop 0
	v_add_f32_e32 v97, v78, v79
	ds_read_b128 v[78:81], v70 offset:24576
	ds_read_b128 v[82:85], v70 offset:25600
	ds_read_b128 v[86:89], v70 offset:26624
	ds_read_b128 v[90:93], v70 offset:27648
	s_waitcnt lgkmcnt(3)
	v_pk_fma_f32 v[78:79], v[30:31], v[78:79], 0 op_sel_hi:[1,1,0]
	s_nop 0
	v_pk_fma_f32 v[78:79], v[24:25], v[80:81], v[78:79]
	s_waitcnt lgkmcnt(2)
	v_pk_fma_f32 v[78:79], v[28:29], v[82:83], v[78:79]
	s_nop 0
	v_pk_fma_f32 v[78:79], v[20:21], v[84:85], v[78:79]
	s_waitcnt lgkmcnt(1)
	v_pk_fma_f32 v[78:79], v[26:27], v[86:87], v[78:79]
	s_nop 0
	v_pk_fma_f32 v[78:79], v[18:19], v[88:89], v[78:79]
	s_waitcnt lgkmcnt(0)
	v_pk_fma_f32 v[86:87], v[22:23], v[90:91], v[78:79]
	ds_read_b128 v[78:81], v70 offset:29696
	ds_read_b128 v[82:85], v70 offset:28672
	v_pk_fma_f32 v[86:87], v[16:17], v[92:93], v[86:87]
	s_waitcnt lgkmcnt(0)
	v_pk_fma_f32 v[30:31], v[30:31], v[82:83], 0 op_sel_hi:[1,1,0]
	v_add_f32_e32 v98, v86, v87
	ds_read_b128 v[86:89], v70 offset:31744
	ds_read_b128 v[90:93], v70 offset:30720
	v_pk_fma_f32 v[24:25], v[24:25], v[84:85], v[30:31]
	s_nop 0
	v_pk_fma_f32 v[24:25], v[28:29], v[78:79], v[24:25]
	s_nop 0
	v_pk_fma_f32 v[20:21], v[20:21], v[80:81], v[24:25]
	s_waitcnt lgkmcnt(0)
	v_pk_fma_f32 v[20:21], v[26:27], v[90:91], v[20:21]
	s_nop 0
	v_pk_fma_f32 v[18:19], v[18:19], v[92:93], v[20:21]
	s_nop 0
	v_pk_fma_f32 v[18:19], v[22:23], v[86:87], v[18:19]
	s_nop 0
	v_pk_fma_f32 v[16:17], v[16:17], v[88:89], v[18:19]
	s_nop 0
	v_add_f32_e32 v16, v16, v17
	v_cndmask_b32_e64 v17, v45, v96, s[2:3]
	ds_bpermute_b32 v17, v69, v17
	v_cndmask_b32_e64 v18, v96, v45, s[2:3]
	v_cndmask_b32_e64 v19, v77, v97, s[2:3]
	ds_bpermute_b32 v19, v69, v19
	v_cndmask_b32_e64 v21, v95, v16, s[2:3]
	s_waitcnt lgkmcnt(1)
	v_add_f32_e32 v17, v18, v17
	v_cndmask_b32_e64 v18, v94, v98, s[2:3]
	ds_bpermute_b32 v18, v69, v18
	ds_bpermute_b32 v21, v69, v21
	v_cndmask_b32_e64 v20, v97, v77, s[2:3]
	s_waitcnt lgkmcnt(2)
	v_add_f32_e32 v19, v20, v19
	v_cndmask_b32_e64 v20, v98, v94, s[2:3]
	v_cndmask_b32_e64 v16, v16, v95, s[2:3]
	s_waitcnt lgkmcnt(1)
	v_add_f32_e32 v18, v20, v18
	s_waitcnt lgkmcnt(0)
	v_add_f32_e32 v16, v16, v21
	v_cndmask_b32_e64 v20, v17, v18, s[4:5]
	v_cndmask_b32_e64 v21, v19, v16, s[4:5]
	ds_bpermute_b32 v20, v68, v20
	ds_bpermute_b32 v21, v68, v21
	v_cndmask_b32_e64 v17, v18, v17, s[4:5]
	v_cndmask_b32_e64 v16, v16, v19, s[4:5]
	s_waitcnt lgkmcnt(1)
	v_add_f32_e32 v17, v17, v20
	s_waitcnt lgkmcnt(0)
	v_add_f32_e32 v16, v16, v21
	v_cndmask_b32_e64 v18, v17, v16, s[6:7]
	ds_bpermute_b32 v18, v67, v18
	v_cndmask_b32_e64 v16, v16, v17, s[6:7]
	s_waitcnt lgkmcnt(0)
	v_add_f32_e32 v16, v16, v18
	ds_bpermute_b32 v17, v66, v16
	s_waitcnt lgkmcnt(0)
	v_add_f32_e32 v16, v16, v17
	ds_bpermute_b32 v17, v65, v16
	s_waitcnt lgkmcnt(0)
	v_add_f32_e32 v16, v16, v17
	ds_bpermute_b32 v17, v64, v16
	s_and_saveexec_b64 s[10:11], s[8:9]
	s_cbranch_execz .LBB0_102
	global_load_dword v18, v[42:43], off
	s_waitcnt lgkmcnt(0)
	v_add_f32_e32 v16, v16, v17
	s_sub_u32 s16, s16, s37
	s_subb_u32 s17, s17, s38
	s_waitcnt vmcnt(0)
	v_add_f32_e32 v16, v16, v18
	v_mul_f32_e64 v17, |v16|, s30
	v_exp_f32_e32 v30, v17
	v_min_f32_e32 v31, 0, v16
	v_add_f32_e32 v18, 1.0, v30
	v_add_f32_e32 v19, -1.0, v18
	v_frexp_mant_f32_e32 v20, v18
	v_cvt_f64_f32_e32 v[16:17], v18
	v_sub_f32_e32 v21, v19, v18
	v_frexp_exp_i32_f64_e32 v16, v[16:17]
	v_cmp_gt_f32_e32 vcc, s31, v20
	v_sub_f32_e32 v19, v30, v19
	v_add_f32_e32 v17, 1.0, v21
	v_subbrev_co_u32_e32 v16, vcc, 0, v16, vcc
	v_add_f32_e32 v17, v19, v17
	v_sub_u32_e32 v19, 0, v16
	v_ldexp_f32 v18, v18, v19
	v_add_f32_e32 v20, -1.0, v18
	v_add_f32_e32 v21, 1.0, v18
	v_ldexp_f32 v17, v17, v19
	v_add_f32_e32 v19, 1.0, v20
	v_add_f32_e32 v22, -1.0, v21
	v_sub_f32_e32 v19, v18, v19
	v_sub_f32_e32 v18, v18, v22
	v_add_f32_e32 v22, v17, v19
	v_add_f32_e32 v17, v17, v18
	v_add_f32_e32 v24, v21, v17
	v_rcp_f32_e32 v25, v24
	v_add_f32_e32 v19, v20, v22
	v_sub_f32_e32 v20, v19, v20
	v_sub_f32_e32 v18, v24, v21
	v_mul_f32_e32 v27, v19, v25
	v_sub_f32_e32 v26, v22, v20
	v_mul_f32_e32 v20, v24, v27
	v_sub_f32_e32 v17, v17, v18
	v_fma_f32 v22, v27, v24, -v20
	v_fmac_f32_e32 v22, v27, v17
	v_add_f32_e32 v18, v20, v22
	v_sub_f32_e32 v21, v19, v18
	v_mov_b32_e32 v23, v18
	v_pk_add_f32 v[18:19], v[18:19], v[20:21] neg_lo:[0,1] neg_hi:[0,1]
	v_cvt_f32_i32_e32 v16, v16
	v_pk_add_f32 v[18:19], v[18:19], v[22:23] neg_lo:[0,1] neg_hi:[0,1]
	v_cmp_neq_f32_e32 vcc, s34, v30
	v_add_f32_e32 v19, v26, v19
	v_add_f32_e32 v18, v18, v19
	v_add_f32_e32 v19, v21, v18
	v_mul_f32_e32 v23, v25, v19
	v_mul_f32_e32 v20, v24, v23
	v_sub_f32_e32 v21, v21, v19
	v_add_f32_e32 v28, v27, v23
	v_fma_f32 v22, v23, v24, -v20
	v_add_f32_e32 v26, v18, v21
	v_sub_f32_e32 v18, v28, v27
	v_fmac_f32_e32 v22, v23, v17
	v_sub_f32_e32 v17, v23, v18
	v_add_f32_e32 v18, v20, v22
	v_sub_f32_e32 v21, v19, v18
	v_mov_b32_e32 v23, v18
	v_pk_add_f32 v[18:19], v[18:19], v[20:21] neg_lo:[0,1] neg_hi:[0,1]
	s_nop 0
	v_pk_add_f32 v[18:19], v[18:19], v[22:23] neg_lo:[0,1] neg_hi:[0,1]
	s_nop 0
	v_add_f32_e32 v19, v26, v19
	v_add_f32_e32 v18, v18, v19
	v_add_f32_e32 v18, v21, v18
	v_mul_f32_e32 v18, v25, v18
	v_add_f32_e32 v17, v17, v18
	v_add_f32_e32 v18, v28, v17
	v_mul_f32_e32 v20, v18, v18
	v_sub_f32_e32 v21, v18, v28
	v_fmamk_f32 v22, v20, 0x3e9b6dac, v72
	v_sub_f32_e32 v21, v17, v21
	v_mul_f32_e32 v17, v18, v20
	v_fmaak_f32 v45, v20, v22, 0x3f2aaada
	v_ldexp_f32 v23, v21, 1
	v_pk_mul_f32 v[20:21], v[16:17], v[44:45]
	v_ldexp_f32 v19, v18, 1
	v_fma_f32 v18, v16, s33, -v20
	v_fmac_f32_e32 v18, 0xb102e308, v16
	v_pk_add_f32 v[16:17], v[20:21], v[18:19]
	v_mov_b32_e32 v22, v20
	v_sub_f32_e32 v26, v17, v19
	v_pk_add_f32 v[24:25], v[16:17], v[20:21] neg_lo:[0,1] neg_hi:[0,1]
	v_sub_f32_e32 v20, v21, v26
	v_add_f32_e32 v23, v23, v20
	v_pk_add_f32 v[20:21], v[16:17], v[22:23]
	v_mov_b32_e32 v19, v16
	v_mov_b32_e32 v25, v21
	v_pk_add_f32 v[28:29], v[18:19], v[24:25] neg_lo:[0,1] neg_hi:[0,1]
	v_pk_add_f32 v[18:19], v[18:19], v[24:25]
	v_mov_b32_e32 v27, v16
	v_pk_add_f32 v[24:25], v[18:19], v[16:17] op_sel:[1,0] op_sel_hi:[0,1] neg_lo:[0,1] neg_hi:[0,1]
	v_mov_b32_e32 v26, v23
	v_mov_b32_e32 v22, v21
	v_mov_b32_e32 v23, v19
	v_pk_mov_b32 v[16:17], v[16:17], v[24:25] op_sel:[1,0]
	v_pk_add_f32 v[20:21], v[20:21], v[24:25] op_sel_hi:[1,0] neg_lo:[0,1] neg_hi:[0,1]
	v_pk_add_f32 v[16:17], v[22:23], v[16:17] neg_lo:[0,1] neg_hi:[0,1]
	v_mov_b32_e32 v20, v28
	v_pk_add_f32 v[16:17], v[26:27], v[16:17] neg_lo:[0,1] neg_hi:[0,1]
	v_mov_b32_e32 v29, v19
	v_pk_add_f32 v[20:21], v[20:21], v[16:17]
	s_nop 0
	v_pk_add_f32 v[22:23], v[20:21], v[20:21] op_sel:[0,1] op_sel_hi:[1,0]
	s_nop 0
	v_pk_add_f32 v[18:19], v[18:19], v[22:23] op_sel:[1,0] op_sel_hi:[0,1]
	v_mov_b32_e32 v21, v18
	v_mov_b32_e32 v17, v22
	v_pk_add_f32 v[22:23], v[20:21], v[28:29] neg_lo:[0,1] neg_hi:[0,1]
	s_nop 0
	v_sub_f32_e32 v19, v20, v22
	v_pk_add_f32 v[16:17], v[16:17], v[22:23] neg_lo:[0,1] neg_hi:[0,1]
	v_sub_f32_e32 v19, v28, v19
	v_add_f32_e32 v16, v16, v19
	v_add_f32_e32 v16, v16, v17
	v_add_f32_e32 v16, v18, v16
	v_cndmask_b32_e32 v16, v74, v16, vcc
	v_cmp_ngt_f32_e32 vcc, -1.0, v30
	s_nop 1
	v_cndmask_b32_e32 v16, v75, v16, vcc
	v_cmp_neq_f32_e32 vcc, -1.0, v30
	s_nop 1
	v_cndmask_b32_e32 v16, v76, v16, vcc
	v_cmp_lt_f32_e64 vcc, |v30|, s35
	s_nop 1
	v_cndmask_b32_e32 v16, v16, v30, vcc
	v_sub_f32_e32 v18, v31, v16
	v_lshl_add_u64 v[16:17], s[16:17], 2, v[46:47]
	global_store_dword v[16:17], v18, off offset:4
	s_branch .LBB0_102

.LBB0_502:
	s_or_b32 s20, s48, s47
	s_ashr_i32 s21, s20, 31
	s_lshl_b64 s[12:13], s[20:21], 11
	global_load_dwordx4 v[16:19], v[140:141], off
	global_load_dwordx4 v[20:23], v[140:141], off offset:1024
	global_load_dwordx4 v[24:27], v[140:141], off offset:2048
	global_load_dwordx4 v[28:31], v[140:141], off offset:3072
	global_load_dwordx4 v[32:35], v[130:131], off
	v_lshl_add_u64 v[0:1], v[132:133], 0, s[12:13]
	global_load_dwordx4 v[36:39], v[130:131], off offset:1024
	global_load_dwordx4 v[40:43], v[130:131], off offset:2048
	global_load_dwordx4 v[44:47], v[130:131], off offset:3072
	global_load_dwordx2 v[48:49], v[0:1], off nt
	global_load_dwordx2 v[50:51], v[0:1], off offset:512 nt
	global_load_dwordx2 v[52:53], v[0:1], off offset:1024 nt
	global_load_dwordx2 v[54:55], v[0:1], off offset:1536 nt
	s_or_b32 s18, s20, 1
	s_ashr_i32 s19, s18, 31
	s_or_b32 s16, s20, 2
	s_lshl_b64 s[12:13], s[18:19], 11
	s_ashr_i32 s17, s16, 31
	v_lshl_add_u64 v[0:1], v[132:133], 0, s[12:13]
	s_lshl_b64 s[12:13], s[16:17], 11
	v_lshl_add_u64 v[64:65], v[132:133], 0, s[12:13]
	global_load_dwordx2 v[56:57], v[0:1], off nt
	global_load_dwordx2 v[58:59], v[0:1], off offset:512 nt
	global_load_dwordx2 v[60:61], v[0:1], off offset:1024 nt
	global_load_dwordx2 v[62:63], v[0:1], off offset:1536 nt
	global_load_dwordx2 v[80:81], v[64:65], off nt
	global_load_dwordx2 v[82:83], v[64:65], off offset:512 nt
	s_waitcnt lgkmcnt(0)
	global_load_dwordx4 v[12:15], v[142:143], off
	global_load_dwordx4 v[4:7], v[142:143], off offset:1024
	global_load_dwordx2 v[84:85], v[64:65], off offset:1024 nt
	global_load_dwordx4 v[8:11], v[142:143], off offset:2048
	global_load_dwordx4 v[0:3], v[142:143], off offset:3072
	global_load_dwordx2 v[86:87], v[64:65], off offset:1536 nt
	s_or_b32 s14, s20, 3
	s_ashr_i32 s15, s14, 31
	s_lshl_b64 s[12:13], s[14:15], 11
	v_lshl_add_u64 v[64:65], v[132:133], 0, s[12:13]
	global_load_dwordx2 v[88:89], v[64:65], off nt
	global_load_dwordx2 v[90:91], v[64:65], off offset:512 nt
	global_load_dwordx2 v[92:93], v[64:65], off offset:1024 nt
	global_load_dwordx2 v[94:95], v[64:65], off offset:1536 nt
	v_mov_b32_e32 v235, v227
	v_mov_b32_e32 v236, v226
	s_waitcnt vmcnt(27)
	v_pk_add_f32 v[16:17], v[16:17], 1.0 op_sel_hi:[1,0]
	v_pk_add_f32 v[18:19], v[18:19], 1.0 op_sel_hi:[1,0]
	s_waitcnt vmcnt(26)
	v_pk_add_f32 v[22:23], v[22:23], 1.0 op_sel_hi:[1,0]
	s_waitcnt vmcnt(24)
	v_pk_add_f32 v[68:69], v[30:31], 1.0 op_sel_hi:[1,0]
	s_waitcnt vmcnt(23)
	v_pk_mul_f32 v[30:31], v[32:33], v[16:17]
	s_waitcnt vmcnt(19)
	v_lshlrev_b32_e32 v96, 16, v48
	v_and_b32_e32 v97, 0xffff0000, v48
	v_lshlrev_b32_e32 v98, 16, v49
	v_and_b32_e32 v99, 0xffff0000, v49
	v_pk_fma_f32 v[32:33], v[96:97], v[96:97], 0 op_sel_hi:[1,1,0]
	s_waitcnt vmcnt(18)
	v_lshlrev_b32_e32 v100, 16, v50
	v_and_b32_e32 v101, 0xffff0000, v50
	v_pk_fma_f32 v[32:33], v[98:99], v[98:99], v[32:33]
	v_lshlrev_b32_e32 v102, 16, v51
	v_and_b32_e32 v103, 0xffff0000, v51
	v_pk_fma_f32 v[32:33], v[100:101], v[100:101], v[32:33]
	s_waitcnt vmcnt(17)
	v_lshlrev_b32_e32 v104, 16, v52
	v_and_b32_e32 v105, 0xffff0000, v52
	v_pk_fma_f32 v[32:33], v[102:103], v[102:103], v[32:33]
	v_lshlrev_b32_e32 v106, 16, v53
	v_and_b32_e32 v107, 0xffff0000, v53
	v_pk_fma_f32 v[32:33], v[104:105], v[104:105], v[32:33]
	s_waitcnt vmcnt(16)
	v_lshlrev_b32_e32 v108, 16, v54
	v_and_b32_e32 v109, 0xffff0000, v54
	v_pk_fma_f32 v[32:33], v[106:107], v[106:107], v[32:33]
	v_lshlrev_b32_e32 v110, 16, v55
	v_and_b32_e32 v111, 0xffff0000, v55
	v_pk_fma_f32 v[32:33], v[108:109], v[108:109], v[32:33]
	v_pk_add_f32 v[70:71], v[28:29], 1.0 op_sel_hi:[1,0]
	v_pk_fma_f32 v[32:33], v[110:111], v[110:111], v[32:33]
	v_pk_mul_f32 v[28:29], v[34:35], v[18:19]
	v_add_f32_e32 v32, v32, v33
	v_pk_add_f32 v[66:67], v[24:25], 1.0 op_sel_hi:[1,0]
	v_pk_mul_f32 v[24:25], v[38:39], v[22:23]
	v_pk_add_f32 v[20:21], v[20:21], 1.0 op_sel_hi:[1,0]
	v_pk_add_f32 v[64:65], v[26:27], 1.0 op_sel_hi:[1,0]
	s_waitcnt lgkmcnt(0)
	s_nop 1
	v_add_f32_dpp v32, v32, v32 quad_perm:[1,0,3,2] row_mask:0xf bank_mask:0xf
	v_pk_mul_f32 v[26:27], v[36:37], v[20:21]
	v_pk_mul_f32 v[20:21], v[42:43], v[64:65]
	v_pk_mul_f32 v[16:17], v[46:47], v[68:69]
	s_waitcnt vmcnt(11)
	v_lshlrev_b32_e32 v48, 16, v80
	s_waitcnt lgkmcnt(0)
	s_nop 1
	v_add_f32_dpp v32, v32, v32 quad_perm:[2,3,0,1] row_mask:0xf bank_mask:0xf
	v_and_b32_e32 v49, 0xffff0000, v80
	v_lshlrev_b32_e32 v52, 16, v81
	v_and_b32_e32 v53, 0xffff0000, v81
	s_waitcnt vmcnt(10)
	v_lshlrev_b32_e32 v50, 16, v82
	s_waitcnt lgkmcnt(0)
	s_nop 1
	v_add_f32_dpp v34, v32, v32 row_half_mirror row_mask:0xf bank_mask:0xf
	v_and_b32_e32 v51, 0xffff0000, v82
	v_pk_mul_f32 v[18:19], v[44:45], v[70:71]
	v_lshlrev_b32_e32 v70, 16, v56
	v_and_b32_e32 v71, 0xffff0000, v56
	s_waitcnt lgkmcnt(0)
	s_nop 1
	v_add_f32_dpp v38, v34, v34 row_mirror row_mask:0xf bank_mask:0xf
	v_lshlrev_b32_e32 v78, 16, v57
	v_and_b32_e32 v79, 0xffff0000, v57
	v_lshlrev_b32_e32 v56, 16, v83
	v_and_b32_e32 v57, 0xffff0000, v83
	s_waitcnt lgkmcnt(0)
	v_mov_b32_e32 v42, v38
	v_mov_b32_e32 v39, v38
	s_nop 1
	v_permlane16_swap_b32_e32 v42, v39
	v_add_f32_e32 v42, v42, v39
	s_waitcnt vmcnt(7)
	v_lshlrev_b32_e32 v54, 16, v84
	v_and_b32_e32 v55, 0xffff0000, v84
	v_pk_mul_f32 v[22:23], v[40:41], v[66:67]
	v_lshlrev_b32_e32 v66, 16, v60
	s_waitcnt lgkmcnt(0)
	v_mov_b32_e32 v43, v42
	s_nop 1
	v_permlane32_swap_b32_e32 v42, v43
	v_add_f32_e32 v42, v42, v43
	v_fmamk_f32 v42, v42, 0x3a800000, v229
	v_mul_f32_e32 v43, 0x4f800000, v42
	v_cmp_gt_f32_e32 vcc, s43, v42
	v_and_b32_e32 v67, 0xffff0000, v60
	v_lshlrev_b32_e32 v74, 16, v61
	v_cndmask_b32_e32 v43, v42, v43, vcc
	v_sqrt_f32_e32 v46, v43
	v_and_b32_e32 v75, 0xffff0000, v61
	v_lshlrev_b32_e32 v60, 16, v85
	v_and_b32_e32 v61, 0xffff0000, v85
	v_add_u32_e32 v47, -1, v46
	v_fma_f32 v80, -v47, v46, v43
	v_cmp_ge_f32_e64 s[12:13], 0, v80
	v_add_u32_e32 v80, 1, v46
	v_lshlrev_b32_e32 v68, 16, v58
	v_cndmask_b32_e64 v47, v46, v47, s[12:13]
	v_fma_f32 v46, -v80, v46, v43
	v_cmp_lt_f32_e64 s[12:13], 0, v46
	v_and_b32_e32 v69, 0xffff0000, v58
	v_lshlrev_b32_e32 v76, 16, v59
	v_cndmask_b32_e64 v46, v47, v80, s[12:13]
	v_mul_f32_e32 v47, 0x37800000, v46
	v_cndmask_b32_e32 v46, v46, v47, vcc
	v_cmp_class_f32_e32 vcc, v43, v230
	v_and_b32_e32 v77, 0xffff0000, v59
	v_lshlrev_b32_e32 v64, 16, v62
	v_cndmask_b32_e32 v80, v46, v43, vcc
	v_div_scale_f32 v81, s[12:13], v80, v80, 1.0
	v_rcp_f32_e32 v82, v81
	v_and_b32_e32 v65, 0xffff0000, v62
	v_lshlrev_b32_e32 v72, 16, v63
	v_and_b32_e32 v73, 0xffff0000, v63
	v_fma_f32 v83, -v81, v82, 1.0
	v_fmac_f32_e32 v82, v83, v82
	v_div_scale_f32 v83, vcc, 1.0, v80, 1.0
	v_mul_f32_e32 v84, v83, v82
	v_fma_f32 v85, -v81, v84, v83
	v_fmac_f32_e32 v84, v85, v82
	v_fma_f32 v81, -v81, v84, v83
	v_div_fmas_f32 v81, v81, v82, v84
	v_div_fixup_f32 v80, v81, v80, 1.0
	v_pk_mul_f32 v[82:83], v[80:81], v[96:97] op_sel_hi:[0,1]
	v_pk_fma_f32 v[146:147], v[30:31], v[82:83], v[12:13]
	v_pk_mul_f32 v[82:83], v[80:81], v[100:101] op_sel_hi:[0,1]
	v_pk_fma_f32 v[150:151], v[26:27], v[82:83], v[4:5]
	v_pk_mul_f32 v[82:83], v[80:81], v[104:105] op_sel_hi:[0,1]
	s_waitcnt vmcnt(6)
	v_pk_fma_f32 v[154:155], v[22:23], v[82:83], v[8:9]
	v_pk_mul_f32 v[82:83], v[80:81], v[108:109] op_sel_hi:[0,1]
	s_waitcnt vmcnt(5)
	v_pk_fma_f32 v[158:159], v[18:19], v[82:83], v[0:1]
	v_mul_f32_e32 v82, 0x41000000, v150
	v_mul_f32_e32 v83, 0x41000000, v151
	s_waitcnt vmcnt(4)
	v_lshlrev_b32_e32 v58, 16, v86
	v_and_b32_e32 v59, 0xffff0000, v86
	v_lshlrev_b32_e32 v62, 16, v87
	v_and_b32_e32 v63, 0xffff0000, v87
	v_med3_f32 v86, v82, s44, v231
	v_med3_f32 v87, v83, s44, v231
	v_pk_fma_f32 v[82:83], v[70:71], v[70:71], 0 op_sel_hi:[1,1,0]
	v_pk_mul_f32 v[84:85], v[80:81], v[98:99] op_sel_hi:[0,1]
	v_pk_fma_f32 v[82:83], v[78:79], v[78:79], v[82:83]
	v_pk_fma_f32 v[144:145], v[28:29], v[84:85], v[14:15]
	v_pk_fma_f32 v[82:83], v[68:69], v[68:69], v[82:83]
	v_pk_mul_f32 v[84:85], v[80:81], v[102:103] op_sel_hi:[0,1]
	v_pk_fma_f32 v[82:83], v[76:77], v[76:77], v[82:83]
	v_pk_fma_f32 v[148:149], v[24:25], v[84:85], v[6:7]
	v_pk_fma_f32 v[82:83], v[66:67], v[66:67], v[82:83]
	v_pk_mul_f32 v[84:85], v[80:81], v[106:107] op_sel_hi:[0,1]
	v_pk_fma_f32 v[82:83], v[74:75], v[74:75], v[82:83]
	v_pk_mul_f32 v[80:81], v[80:81], v[110:111] op_sel_hi:[0,1]
	v_pk_fma_f32 v[82:83], v[64:65], v[64:65], v[82:83]
	v_pk_fma_f32 v[156:157], v[16:17], v[80:81], v[2:3]
	v_pk_fma_f32 v[82:83], v[72:73], v[72:73], v[82:83]
	v_mul_f32_e32 v80, 0x41000000, v146
	v_add_f32_e32 v82, v82, v83
	v_mul_f32_e32 v81, 0x41000000, v147
	v_pk_fma_f32 v[152:153], v[20:21], v[84:85], v[10:11]
	v_med3_f32 v80, v80, s44, v231
	v_med3_f32 v81, v81, s44, v231
	s_waitcnt lgkmcnt(0)
	s_nop 1
	v_add_f32_dpp v82, v82, v82 quad_perm:[1,0,3,2] row_mask:0xf bank_mask:0xf
	v_mov_b32_e32 v85, 0
	v_cvt_pk_fp8_f32 v85, v80, v81
	v_mul_f32_e32 v84, 0x41000000, v144
	v_mul_f32_e32 v80, 0x41000000, v145
	s_waitcnt lgkmcnt(0)
	s_nop 1
	v_add_f32_dpp v82, v82, v82 quad_perm:[2,3,0,1] row_mask:0xf bank_mask:0xf
	v_med3_f32 v81, v84, s44, v231
	v_med3_f32 v80, v80, s44, v231
	v_cvt_pk_fp8_f32 v85, v81, v80 op_sel:[0,0,1]
	s_waitcnt vmcnt(3)
	v_lshlrev_b32_e32 v32, 16, v88
	s_waitcnt lgkmcnt(0)
	s_nop 1
	v_add_f32_dpp v82, v82, v82 row_half_mirror row_mask:0xf bank_mask:0xf
	v_and_b32_e32 v33, 0xffff0000, v88
	v_mov_b32_e32 v88, 0
	s_lshl_b64 s[12:13], s[20:21], 10
	v_cvt_pk_fp8_f32 v88, v86, v87
	s_waitcnt lgkmcnt(0)
	s_nop 1
	v_add_f32_dpp v82, v82, v82 row_mirror row_mask:0xf bank_mask:0xf
	v_lshl_add_u64 v[80:81], v[134:135], 0, s[12:13]
	global_store_dword v[80:81], v85, off
	v_mul_f32_e32 v84, 0x41000000, v148
	v_mul_f32_e32 v85, 0x41000000, v149
	s_waitcnt lgkmcnt(0)
	v_mov_b32_e32 v83, v82
	s_nop 1
	v_permlane16_swap_b32_e32 v82, v83
	v_add_f32_e32 v82, v82, v83
	v_med3_f32 v84, v84, s44, v231
	v_med3_f32 v85, v85, s44, v231
	v_cvt_pk_fp8_f32 v88, v84, v85 op_sel:[0,0,1]
	v_mul_f32_e32 v84, 0x41000000, v154
	v_mul_f32_e32 v85, 0x41000000, v155
	v_med3_f32 v84, v84, s44, v231
	v_med3_f32 v85, v85, s44, v231
	v_mov_b32_e32 v87, 0
	v_cvt_pk_fp8_f32 v87, v84, v85
	v_mul_f32_e32 v86, 0x41000000, v152
	v_mul_f32_e32 v84, 0x41000000, v153
	s_waitcnt lgkmcnt(0)
	v_mov_b32_e32 v83, v82
	s_nop 1
	v_permlane32_swap_b32_e32 v82, v83
	v_add_f32_e32 v82, v82, v83
	v_med3_f32 v85, v86, s44, v231
	v_med3_f32 v84, v84, s44, v231
	v_fmamk_f32 v82, v82, 0x3a800000, v229
	v_cvt_pk_fp8_f32 v87, v85, v84 op_sel:[0,0,1]
	v_mul_f32_e32 v84, 0x41000000, v158
	v_mul_f32_e32 v85, 0x41000000, v159
	v_mul_f32_e32 v83, 0x4f800000, v82
	v_cmp_gt_f32_e32 vcc, s43, v82
	s_waitcnt vmcnt(3)
	v_lshlrev_b32_e32 v34, 16, v90
	v_and_b32_e32 v35, 0xffff0000, v90
	v_med3_f32 v84, v84, s44, v231
	v_med3_f32 v85, v85, s44, v231
	v_mov_b32_e32 v90, 0
	v_cndmask_b32_e32 v82, v82, v83, vcc
	v_cvt_pk_fp8_f32 v90, v84, v85
	v_sqrt_f32_e32 v83, v82
	v_lshlrev_b32_e32 v36, 16, v89
	v_and_b32_e32 v37, 0xffff0000, v89
	v_mul_f32_e32 v86, 0x41000000, v156
	v_mul_f32_e32 v89, 0x41000000, v157
	v_med3_f32 v84, v86, s44, v231
	v_med3_f32 v85, v89, s44, v231
	v_cvt_pk_fp8_f32 v90, v84, v85 op_sel:[0,0,1]
	v_add_u32_e32 v84, -1, v83
	v_fma_f32 v85, -v84, v83, v82
	v_cmp_ge_f32_e64 s[12:13], 0, v85
	v_add_u32_e32 v85, 1, v83
	global_store_dword v[80:81], v88, off offset:256
	global_store_dword v[80:81], v87, off offset:512
	global_store_dword v[80:81], v90, off offset:768
	v_cndmask_b32_e64 v84, v83, v84, s[12:13]
	v_fma_f32 v83, -v85, v83, v82
	v_cmp_lt_f32_e64 s[12:13], 0, v83
	v_lshlrev_b32_e32 v40, 16, v91
	v_and_b32_e32 v41, 0xffff0000, v91
	v_cndmask_b32_e64 v83, v84, v85, s[12:13]
	v_mul_f32_e32 v84, 0x37800000, v83
	v_cndmask_b32_e32 v83, v83, v84, vcc
	v_cmp_class_f32_e32 vcc, v82, v230
	s_waitcnt vmcnt(5)
	v_lshlrev_b32_e32 v38, 16, v92
	v_and_b32_e32 v39, 0xffff0000, v92
	v_cndmask_b32_e32 v82, v83, v82, vcc
	v_div_scale_f32 v83, s[12:13], v82, v82, 1.0
	v_rcp_f32_e32 v84, v83
	s_lshl_b64 s[12:13], s[18:19], 10
	v_lshlrev_b32_e32 v44, 16, v93
	v_and_b32_e32 v45, 0xffff0000, v93
	v_fma_f32 v80, -v83, v84, 1.0
	v_fmac_f32_e32 v84, v80, v84
	v_div_scale_f32 v80, vcc, 1.0, v82, 1.0
	v_mul_f32_e32 v81, v80, v84
	v_fma_f32 v85, -v83, v81, v80
	v_fmac_f32_e32 v81, v85, v84
	v_fma_f32 v80, -v83, v81, v80
	v_div_fmas_f32 v80, v80, v84, v81
	v_div_fixup_f32 v80, v80, v82, 1.0
	v_pk_mul_f32 v[70:71], v[80:81], v[70:71] op_sel_hi:[0,1]
	v_pk_mul_f32 v[66:67], v[80:81], v[66:67] op_sel_hi:[0,1]
	v_pk_fma_f32 v[162:163], v[30:31], v[70:71], v[12:13]
	v_pk_mul_f32 v[68:69], v[80:81], v[68:69] op_sel_hi:[0,1]
	v_pk_fma_f32 v[170:171], v[22:23], v[66:67], v[8:9]
	v_pk_mul_f32 v[66:67], v[80:81], v[72:73] op_sel_hi:[0,1]
	v_pk_fma_f32 v[166:167], v[26:27], v[68:69], v[4:5]
	v_pk_mul_f32 v[68:69], v[80:81], v[74:75] op_sel_hi:[0,1]
	v_pk_fma_f32 v[172:173], v[16:17], v[66:67], v[2:3]
	v_mul_f32_e32 v66, 0x41000000, v162
	v_mul_f32_e32 v67, 0x41000000, v163
	v_pk_fma_f32 v[168:169], v[20:21], v[68:69], v[10:11]
	v_med3_f32 v66, v66, s44, v231
	v_med3_f32 v67, v67, s44, v231
	v_mov_b32_e32 v69, 0
	v_pk_mul_f32 v[78:79], v[80:81], v[78:79] op_sel_hi:[0,1]
	v_cvt_pk_fp8_f32 v69, v66, v67
	v_pk_fma_f32 v[160:161], v[28:29], v[78:79], v[14:15]
	v_pk_mul_f32 v[70:71], v[80:81], v[76:77] op_sel_hi:[0,1]
	v_mul_f32_e32 v68, 0x41000000, v160
	v_mul_f32_e32 v66, 0x41000000, v161
	v_med3_f32 v67, v68, s44, v231
	v_med3_f32 v66, v66, s44, v231
	v_cvt_pk_fp8_f32 v69, v67, v66 op_sel:[0,0,1]
	v_mul_f32_e32 v66, 0x41000000, v166
	v_mul_f32_e32 v67, 0x41000000, v167
	v_pk_fma_f32 v[164:165], v[24:25], v[70:71], v[6:7]
	v_med3_f32 v70, v66, s44, v231
	v_med3_f32 v71, v67, s44, v231
	v_pk_fma_f32 v[66:67], v[48:49], v[48:49], 0 op_sel_hi:[1,1,0]
	v_mov_b32_e32 v72, 0
	v_pk_fma_f32 v[66:67], v[52:53], v[52:53], v[66:67]
	v_pk_mul_f32 v[64:65], v[80:81], v[64:65] op_sel_hi:[0,1]
	v_pk_fma_f32 v[66:67], v[50:51], v[50:51], v[66:67]
	v_cvt_pk_fp8_f32 v72, v70, v71
	v_pk_fma_f32 v[66:67], v[56:57], v[56:57], v[66:67]
	v_pk_fma_f32 v[174:175], v[18:19], v[64:65], v[0:1]
	v_pk_fma_f32 v[66:67], v[54:55], v[54:55], v[66:67]
	v_lshl_add_u64 v[64:65], v[134:135], 0, s[12:13]
	v_pk_fma_f32 v[66:67], v[60:61], v[60:61], v[66:67]
	global_store_dword v[64:65], v69, off
	v_pk_fma_f32 v[66:67], v[58:59], v[58:59], v[66:67]
	v_mul_f32_e32 v68, 0x41000000, v164
	v_pk_fma_f32 v[66:67], v[62:63], v[62:63], v[66:67]
	v_mul_f32_e32 v69, 0x41000000, v165
	v_add_f32_e32 v66, v66, v67
	v_med3_f32 v68, v68, s44, v231
	v_med3_f32 v69, v69, s44, v231
	v_cvt_pk_fp8_f32 v72, v68, v69 op_sel:[0,0,1]
	v_mul_f32_e32 v68, 0x41000000, v170
	s_waitcnt lgkmcnt(0)
	s_nop 1
	v_add_f32_dpp v66, v66, v66 quad_perm:[1,0,3,2] row_mask:0xf bank_mask:0xf
	v_mul_f32_e32 v69, 0x41000000, v171
	v_med3_f32 v68, v68, s44, v231
	v_med3_f32 v69, v69, s44, v231
	v_mov_b32_e32 v71, 0
	s_waitcnt lgkmcnt(0)
	s_nop 1
	v_add_f32_dpp v66, v66, v66 quad_perm:[2,3,0,1] row_mask:0xf bank_mask:0xf
	v_cvt_pk_fp8_f32 v71, v68, v69
	v_mul_f32_e32 v70, 0x41000000, v168
	v_mul_f32_e32 v68, 0x41000000, v169
	v_med3_f32 v69, v70, s44, v231
	s_waitcnt lgkmcnt(0)
	s_nop 1
	v_add_f32_dpp v66, v66, v66 row_half_mirror row_mask:0xf bank_mask:0xf
	v_med3_f32 v68, v68, s44, v231
	v_cvt_pk_fp8_f32 v71, v69, v68 op_sel:[0,0,1]
	v_mul_f32_e32 v68, 0x41000000, v174
	v_mul_f32_e32 v69, 0x41000000, v175
	s_waitcnt lgkmcnt(0)
	s_nop 1
	v_add_f32_dpp v66, v66, v66 row_mirror row_mask:0xf bank_mask:0xf
	v_med3_f32 v68, v68, s44, v231
	v_med3_f32 v69, v69, s44, v231
	v_mov_b32_e32 v74, 0
	v_cvt_pk_fp8_f32 v74, v68, v69
	s_waitcnt lgkmcnt(0)
	v_mov_b32_e32 v67, v66
	s_nop 1
	v_permlane16_swap_b32_e32 v66, v67
	v_add_f32_e32 v66, v66, v67
	v_mul_f32_e32 v70, 0x41000000, v172
	v_mul_f32_e32 v73, 0x41000000, v173
	v_med3_f32 v68, v70, s44, v231
	v_med3_f32 v69, v73, s44, v231
	s_waitcnt lgkmcnt(0)
	v_mov_b32_e32 v67, v66
	s_nop 1
	v_permlane32_swap_b32_e32 v66, v67
	v_add_f32_e32 v66, v66, v67
	v_fmamk_f32 v66, v66, 0x3a800000, v229
	v_mul_f32_e32 v67, 0x4f800000, v66
	v_cmp_gt_f32_e32 vcc, s43, v66
	v_cvt_pk_fp8_f32 v74, v68, v69 op_sel:[0,0,1]
	global_store_dword v[64:65], v72, off offset:256
	global_store_dword v[64:65], v71, off offset:512
	global_store_dword v[64:65], v74, off offset:768
	v_cndmask_b32_e32 v66, v66, v67, vcc
	v_sqrt_f32_e32 v67, v66
	s_waitcnt vmcnt(8)
	v_lshlrev_b32_e32 v42, 16, v94
	v_and_b32_e32 v43, 0xffff0000, v94
	v_lshlrev_b32_e32 v46, 16, v95
	v_add_u32_e32 v68, -1, v67
	v_fma_f32 v69, -v68, v67, v66
	v_cmp_ge_f32_e64 s[12:13], 0, v69
	v_add_u32_e32 v69, 1, v67
	v_and_b32_e32 v47, 0xffff0000, v95
	v_cndmask_b32_e64 v68, v67, v68, s[12:13]
	v_fma_f32 v67, -v69, v67, v66
	v_cmp_lt_f32_e64 s[12:13], 0, v67
	s_nop 1
	v_cndmask_b32_e64 v67, v68, v69, s[12:13]
	v_mul_f32_e32 v68, 0x37800000, v67
	v_cndmask_b32_e32 v67, v67, v68, vcc
	v_cmp_class_f32_e32 vcc, v66, v230
	s_nop 1
	v_cndmask_b32_e32 v66, v67, v66, vcc
	v_div_scale_f32 v67, s[12:13], v66, v66, 1.0
	v_rcp_f32_e32 v68, v67
	s_lshl_b64 s[12:13], s[16:17], 10
	v_fma_f32 v64, -v67, v68, 1.0
	v_fmac_f32_e32 v68, v64, v68
	v_div_scale_f32 v64, vcc, 1.0, v66, 1.0
	v_mul_f32_e32 v65, v64, v68
	v_fma_f32 v69, -v67, v65, v64
	v_fmac_f32_e32 v65, v69, v68
	v_fma_f32 v64, -v67, v65, v64
	v_div_fmas_f32 v64, v64, v68, v65
	v_div_fixup_f32 v64, v64, v66, 1.0
	v_pk_mul_f32 v[48:49], v[64:65], v[48:49] op_sel_hi:[0,1]
	v_pk_fma_f32 v[178:179], v[30:31], v[48:49], v[12:13]
	v_pk_mul_f32 v[48:49], v[64:65], v[50:51] op_sel_hi:[0,1]
	v_pk_mul_f32 v[50:51], v[64:65], v[56:57] op_sel_hi:[0,1]
	v_pk_fma_f32 v[180:181], v[24:25], v[50:51], v[6:7]
	v_pk_mul_f32 v[50:51], v[64:65], v[60:61] op_sel_hi:[0,1]
	v_pk_fma_f32 v[184:185], v[20:21], v[50:51], v[10:11]
	v_pk_mul_f32 v[50:51], v[64:65], v[62:63] op_sel_hi:[0,1]
	v_pk_mul_f32 v[52:53], v[64:65], v[52:53] op_sel_hi:[0,1]
	v_pk_fma_f32 v[188:189], v[16:17], v[50:51], v[2:3]
	v_mul_f32_e32 v50, 0x41000000, v178
	v_mul_f32_e32 v51, 0x41000000, v179
	v_pk_fma_f32 v[176:177], v[28:29], v[52:53], v[14:15]
	v_med3_f32 v50, v50, s44, v231
	v_med3_f32 v51, v51, s44, v231
	v_mov_b32_e32 v53, 0
	v_cvt_pk_fp8_f32 v53, v50, v51
	v_mul_f32_e32 v52, 0x41000000, v176
	v_mul_f32_e32 v50, 0x41000000, v177
	v_pk_fma_f32 v[182:183], v[26:27], v[48:49], v[4:5]
	v_med3_f32 v51, v52, s44, v231
	v_med3_f32 v50, v50, s44, v231
	v_cvt_pk_fp8_f32 v53, v51, v50 op_sel:[0,0,1]
	v_mul_f32_e32 v50, 0x41000000, v182
	v_mul_f32_e32 v51, 0x41000000, v183
	v_pk_mul_f32 v[48:49], v[64:65], v[54:55] op_sel_hi:[0,1]
	v_med3_f32 v54, v50, s44, v231
	v_med3_f32 v55, v51, s44, v231
	v_pk_fma_f32 v[50:51], v[32:33], v[32:33], 0 op_sel_hi:[1,1,0]
	v_mov_b32_e32 v56, 0
	v_pk_fma_f32 v[50:51], v[36:37], v[36:37], v[50:51]
	v_pk_fma_f32 v[186:187], v[22:23], v[48:49], v[8:9]
	v_pk_fma_f32 v[50:51], v[34:35], v[34:35], v[50:51]
	v_pk_mul_f32 v[48:49], v[64:65], v[58:59] op_sel_hi:[0,1]
	v_pk_fma_f32 v[50:51], v[40:41], v[40:41], v[50:51]
	v_cvt_pk_fp8_f32 v56, v54, v55
	v_pk_fma_f32 v[50:51], v[38:39], v[38:39], v[50:51]
	v_pk_fma_f32 v[190:191], v[18:19], v[48:49], v[0:1]
	v_pk_fma_f32 v[50:51], v[44:45], v[44:45], v[50:51]
	v_lshl_add_u64 v[48:49], v[134:135], 0, s[12:13]
	v_pk_fma_f32 v[50:51], v[42:43], v[42:43], v[50:51]
	global_store_dword v[48:49], v53, off
	v_pk_fma_f32 v[50:51], v[46:47], v[46:47], v[50:51]
	v_mul_f32_e32 v52, 0x41000000, v180
	v_add_f32_e32 v50, v50, v51
	v_mul_f32_e32 v53, 0x41000000, v181
	v_med3_f32 v52, v52, s44, v231
	v_med3_f32 v53, v53, s44, v231
	v_cvt_pk_fp8_f32 v56, v52, v53 op_sel:[0,0,1]
	s_waitcnt lgkmcnt(0)
	s_nop 1
	v_add_f32_dpp v50, v50, v50 quad_perm:[1,0,3,2] row_mask:0xf bank_mask:0xf
	v_mul_f32_e32 v52, 0x41000000, v186
	v_mul_f32_e32 v53, 0x41000000, v187
	v_med3_f32 v52, v52, s44, v231
	v_med3_f32 v53, v53, s44, v231
	s_waitcnt lgkmcnt(0)
	s_nop 1
	v_add_f32_dpp v50, v50, v50 quad_perm:[2,3,0,1] row_mask:0xf bank_mask:0xf
	v_mov_b32_e32 v55, 0
	v_cvt_pk_fp8_f32 v55, v52, v53
	v_mul_f32_e32 v54, 0x41000000, v184
	v_mul_f32_e32 v52, 0x41000000, v185
	s_waitcnt lgkmcnt(0)
	s_nop 1
	v_add_f32_dpp v50, v50, v50 row_half_mirror row_mask:0xf bank_mask:0xf
	v_med3_f32 v53, v54, s44, v231
	v_med3_f32 v52, v52, s44, v231
	v_cvt_pk_fp8_f32 v55, v53, v52 op_sel:[0,0,1]
	v_mul_f32_e32 v52, 0x41000000, v190
	s_waitcnt lgkmcnt(0)
	s_nop 1
	v_add_f32_dpp v50, v50, v50 row_mirror row_mask:0xf bank_mask:0xf
	v_mul_f32_e32 v53, 0x41000000, v191
	v_med3_f32 v52, v52, s44, v231
	v_med3_f32 v53, v53, s44, v231
	v_mov_b32_e32 v58, 0
	s_waitcnt lgkmcnt(0)
	v_mov_b32_e32 v51, v50
	s_nop 1
	v_permlane16_swap_b32_e32 v50, v51
	v_add_f32_e32 v50, v50, v51
	v_cvt_pk_fp8_f32 v58, v52, v53
	v_mul_f32_e32 v54, 0x41000000, v188
	v_mul_f32_e32 v57, 0x41000000, v189
	v_med3_f32 v52, v54, s44, v231
	s_waitcnt lgkmcnt(0)
	v_mov_b32_e32 v51, v50
	s_nop 1
	v_permlane32_swap_b32_e32 v50, v51
	v_add_f32_e32 v50, v50, v51
	v_fmamk_f32 v50, v50, 0x3a800000, v229
	v_mul_f32_e32 v51, 0x4f800000, v50
	v_cmp_gt_f32_e32 vcc, s43, v50
	v_med3_f32 v53, v57, s44, v231
	v_cvt_pk_fp8_f32 v58, v52, v53 op_sel:[0,0,1]
	v_cndmask_b32_e32 v50, v50, v51, vcc
	v_sqrt_f32_e32 v51, v50
	global_store_dword v[48:49], v56, off offset:256
	global_store_dword v[48:49], v55, off offset:512
	global_store_dword v[48:49], v58, off offset:768
	v_add_u32_e32 v52, -1, v51
	v_fma_f32 v53, -v52, v51, v50
	v_cmp_ge_f32_e64 s[12:13], 0, v53
	v_add_u32_e32 v53, 1, v51
	s_nop 0
	v_cndmask_b32_e64 v52, v51, v52, s[12:13]
	v_fma_f32 v51, -v53, v51, v50
	v_cmp_lt_f32_e64 s[12:13], 0, v51
	s_nop 1
	v_cndmask_b32_e64 v51, v52, v53, s[12:13]
	v_mul_f32_e32 v52, 0x37800000, v51
	v_cndmask_b32_e32 v51, v51, v52, vcc
	v_cmp_class_f32_e32 vcc, v50, v230
	s_nop 1
	v_cndmask_b32_e32 v50, v51, v50, vcc
	v_div_scale_f32 v51, s[12:13], v50, v50, 1.0
	v_rcp_f32_e32 v52, v51
	s_lshl_b64 s[12:13], s[14:15], 10
	v_fma_f32 v48, -v51, v52, 1.0
	v_fmac_f32_e32 v52, v48, v52
	v_div_scale_f32 v48, vcc, 1.0, v50, 1.0
	v_mul_f32_e32 v49, v48, v52
	v_fma_f32 v53, -v51, v49, v48
	v_fmac_f32_e32 v49, v53, v52
	v_fma_f32 v48, -v51, v49, v48
	v_div_fmas_f32 v48, v48, v52, v49
	v_div_fixup_f32 v48, v48, v50, 1.0
	v_pk_mul_f32 v[36:37], v[48:49], v[36:37] op_sel_hi:[0,1]
	v_pk_mul_f32 v[32:33], v[48:49], v[32:33] op_sel_hi:[0,1]
	v_pk_fma_f32 v[192:193], v[28:29], v[36:37], v[14:15]
	v_pk_mul_f32 v[14:15], v[48:49], v[40:41] op_sel_hi:[0,1]
	v_pk_fma_f32 v[194:195], v[30:31], v[32:33], v[12:13]
	v_pk_mul_f32 v[12:13], v[48:49], v[34:35] op_sel_hi:[0,1]
	v_pk_fma_f32 v[196:197], v[24:25], v[14:15], v[6:7]
	v_pk_mul_f32 v[6:7], v[48:49], v[44:45] op_sel_hi:[0,1]
	v_pk_fma_f32 v[198:199], v[26:27], v[12:13], v[4:5]
	v_pk_mul_f32 v[4:5], v[48:49], v[38:39] op_sel_hi:[0,1]
	v_pk_fma_f32 v[200:201], v[20:21], v[6:7], v[10:11]
	v_pk_mul_f32 v[6:7], v[48:49], v[46:47] op_sel_hi:[0,1]
	v_pk_fma_f32 v[202:203], v[22:23], v[4:5], v[8:9]
	v_pk_mul_f32 v[4:5], v[48:49], v[42:43] op_sel_hi:[0,1]
	v_pk_fma_f32 v[204:205], v[16:17], v[6:7], v[2:3]
	v_mul_f32_e32 v2, 0x41000000, v194
	v_mul_f32_e32 v3, 0x41000000, v195
	v_pk_fma_f32 v[206:207], v[18:19], v[4:5], v[0:1]
	v_med3_f32 v2, v2, s44, v231
	v_med3_f32 v3, v3, s44, v231
	v_mov_b32_e32 v5, 0
	v_cvt_pk_fp8_f32 v5, v2, v3
	v_mul_f32_e32 v4, 0x41000000, v192
	v_mul_f32_e32 v2, 0x41000000, v193
	v_med3_f32 v3, v4, s44, v231
	v_med3_f32 v2, v2, s44, v231
	v_cvt_pk_fp8_f32 v5, v3, v2 op_sel:[0,0,1]
	v_mul_f32_e32 v2, 0x41000000, v198
	v_mul_f32_e32 v3, 0x41000000, v199
	v_med3_f32 v2, v2, s44, v231
	v_med3_f32 v3, v3, s44, v231
	v_mov_b32_e32 v6, 0
	v_cvt_pk_fp8_f32 v6, v2, v3
	v_mul_f32_e32 v4, 0x41000000, v196
	v_mul_f32_e32 v2, 0x41000000, v197
	v_med3_f32 v3, v4, s44, v231
	v_med3_f32 v2, v2, s44, v231
	v_cvt_pk_fp8_f32 v6, v3, v2 op_sel:[0,0,1]
	v_mul_f32_e32 v2, 0x41000000, v202
	v_mul_f32_e32 v3, 0x41000000, v203
	v_med3_f32 v2, v2, s44, v231
	v_med3_f32 v3, v3, s44, v231
	v_mov_b32_e32 v7, 0
	v_cvt_pk_fp8_f32 v7, v2, v3
	v_mul_f32_e32 v4, 0x41000000, v200
	v_mul_f32_e32 v2, 0x41000000, v201
	v_med3_f32 v3, v4, s44, v231
	v_med3_f32 v2, v2, s44, v231
	v_cvt_pk_fp8_f32 v7, v3, v2 op_sel:[0,0,1]
	v_mul_f32_e32 v2, 0x41000000, v206
	v_mul_f32_e32 v3, 0x41000000, v207
	v_med3_f32 v2, v2, s44, v231
	v_med3_f32 v3, v3, s44, v231
	v_mov_b32_e32 v8, 0
	v_cvt_pk_fp8_f32 v8, v2, v3
	v_mul_f32_e32 v4, 0x41000000, v204
	v_mul_f32_e32 v2, 0x41000000, v205
	v_med3_f32 v3, v4, s44, v231
	v_med3_f32 v2, v2, s44, v231
	v_lshl_add_u64 v[0:1], v[134:135], 0, s[12:13]
	v_cvt_pk_fp8_f32 v8, v3, v2 op_sel:[0,0,1]
	s_mov_b64 s[12:13], 0
	global_store_dword v[0:1], v5, off
	global_store_dword v[0:1], v6, off offset:256
	global_store_dword v[0:1], v7, off offset:512
	global_store_dword v[0:1], v8, off offset:768
	s_branch .LBB0_504

.LBB0_748:
	s_add_i32 s10, s40, s50
	s_add_i32 s24, s10, 2
	s_add_i32 s20, s10, 3
	s_add_i32 s10, s18, -7
	s_ashr_i32 s25, s24, 31
	s_ashr_i32 s21, s20, 31
	s_ashr_i32 s11, s10, 31
	s_lshl_b64 s[26:27], s[24:25], 11
	s_lshl_b64 s[22:23], s[20:21], 11
	s_lshl_b64 s[10:11], s[10:11], 2
	s_add_u32 s28, s33, s10
	s_addc_u32 s29, s34, s11
	s_add_u32 s10, s35, s10
	v_lshl_add_u64 v[72:73], v[34:35], 0, s[26:27]
	global_load_dword v82, v95, s[28:29]
	global_load_dwordx2 v[74:75], v[72:73], off nt
	s_addc_u32 s11, s36, s11
	s_add_i32 s28, s18, -6
	s_ashr_i32 s29, s28, 31
	s_lshl_b64 s[28:29], s[28:29], 2
	s_add_u32 s52, s33, s28
	s_addc_u32 s53, s34, s29
	global_load_dword v105, v95, s[52:53]
	s_add_u32 s28, s35, s28
	s_addc_u32 s29, s36, s29
	s_add_i32 s52, s18, -5
	s_ashr_i32 s53, s52, 31
	s_lshl_b64 s[52:53], s[52:53], 2
	s_add_u32 s54, s33, s52
	s_addc_u32 s55, s34, s53
	global_load_dword v113, v95, s[54:55]
	s_add_u32 s52, s35, s52
	s_addc_u32 s53, s36, s53
	s_add_i32 s54, s18, -4
	s_ashr_i32 s55, s54, 31
	s_lshl_b64 s[54:55], s[54:55], 2
	s_add_u32 s56, s33, s54
	s_addc_u32 s57, s34, s55
	s_add_u32 s54, s35, s54
	s_addc_u32 s55, s36, s55
	s_add_i32 s58, s18, -3
	s_ashr_i32 s59, s58, 31
	s_waitcnt lgkmcnt(0)
	v_lshl_add_u64 v[62:63], v[34:35], 0, s[22:23]
	global_load_dwordx2 v[76:77], v[72:73], off offset:512 nt
	global_load_dwordx2 v[78:79], v[72:73], off offset:1024 nt
	global_load_dwordx2 v[80:81], v[72:73], off offset:1536 nt
	global_load_dwordx2 v[70:71], v[62:63], off nt
	global_load_dwordx2 v[68:69], v[62:63], off offset:512 nt
	global_load_dwordx2 v[66:67], v[62:63], off offset:1024 nt
	global_load_dwordx2 v[64:65], v[62:63], off offset:1536 nt
	global_load_dword v112, v95, s[10:11]
	global_load_dword v126, v95, s[28:29]
	global_load_dword v127, v95, s[52:53]
	global_load_dword v114, v95, s[56:57]
	global_load_dword v128, v95, s[54:55]
	s_lshl_b64 s[10:11], s[58:59], 2
	s_add_u32 s28, s33, s10
	s_addc_u32 s29, s34, s11
	global_load_dword v115, v95, s[28:29]
	s_add_u32 s10, s35, s10
	s_addc_u32 s11, s36, s11
	s_add_i32 s28, s18, -2
	s_ashr_i32 s29, s28, 31
	s_lshl_b64 s[28:29], s[28:29], 2
	s_add_u32 s52, s33, s28
	s_addc_u32 s53, s34, s29
	s_add_u32 s28, s35, s28
	s_addc_u32 s29, s36, s29
	s_add_i32 s54, s18, -1
	s_ashr_i32 s55, s54, 31
	s_lshl_b64 s[54:55], s[54:55], 2
	s_add_u32 s56, s33, s54
	s_addc_u32 s57, s34, s55
	global_load_dword v116, v95, s[52:53]
	global_load_dword v132, v95, s[56:57]
	s_add_u32 s52, s35, s54
	s_addc_u32 s53, s36, s55
	s_ashr_i32 s19, s18, 31
	s_lshl_b64 s[54:55], s[18:19], 2
	s_add_u32 s56, s33, s54
	s_addc_u32 s57, s34, s55
	s_add_u32 s54, s35, s54
	s_addc_u32 s55, s36, s55
	s_waitcnt vmcnt(18)
	v_lshlrev_b32_sdwa v83, v98, v82 dst_sel:DWORD dst_unused:UNUSED_PAD src0_sel:DWORD src1_sel:BYTE_3
	v_add_u32_e32 v83, s45, v83
	ds_read_b32 v83, v83
	v_and_b32_e32 v82, 0xffffff, v82
	s_waitcnt vmcnt(17)
	v_and_b32_e32 v85, 0xffff0000, v74
	v_lshlrev_b32_e32 v86, 16, v75
	v_and_b32_e32 v87, 0xffff0000, v75
	s_waitcnt vmcnt(16)
	v_lshlrev_b32_sdwa v84, v98, v105 dst_sel:DWORD dst_unused:UNUSED_PAD src0_sel:DWORD src1_sel:BYTE_3
	v_add_u32_e32 v84, s45, v84
	ds_read_b32 v106, v84
	s_waitcnt lgkmcnt(1)
	v_add_u32_e32 v82, v83, v82
	v_ashrrev_i32_e32 v83, 31, v82
	v_lshlrev_b64 v[82:83], 10, v[82:83]
	v_lshl_add_u64 v[82:83], v[36:37], 0, v[82:83]
	global_load_dword v117, v[82:83], off nt
	global_load_dword v120, v[82:83], off offset:256 nt
	global_load_dword v124, v[82:83], off offset:512 nt
	global_load_dword v104, v95, s[10:11]
	global_load_dword v103, v95, s[28:29]
	global_load_dword v102, v95, s[52:53]
	global_load_dword v133, v95, s[56:57]
	global_load_dword v101, v95, s[54:55]
	v_lshlrev_b32_e32 v84, 16, v74
	v_and_b32_e32 v74, 0xffffff, v105
	global_load_dword v105, v[82:83], off offset:768 nt
	s_waitcnt vmcnt(24)
	v_lshlrev_b32_sdwa v75, v98, v113 dst_sel:DWORD dst_unused:UNUSED_PAD src0_sel:DWORD src1_sel:BYTE_3
	v_add_u32_e32 v75, s45, v75
	s_waitcnt lgkmcnt(0)
	v_add_u32_e32 v74, v106, v74
	ds_read_b32 v118, v75
	v_ashrrev_i32_e32 v75, 31, v74
	v_lshlrev_b64 v[74:75], 10, v[74:75]
	v_lshl_add_u64 v[74:75], v[36:37], 0, v[74:75]
	global_load_dword v129, v[74:75], off nt
	global_load_dword v130, v[74:75], off offset:256 nt
	global_load_dword v131, v[74:75], off offset:512 nt
	global_load_dword v134, v[74:75], off offset:768 nt
	s_waitcnt vmcnt(27)
	v_lshlrev_b32_e32 v82, 16, v76
	v_and_b32_e32 v83, 0xffff0000, v76
	v_and_b32_e32 v76, 0xffffff, v113
	s_waitcnt vmcnt(17)
	v_lshlrev_b32_sdwa v74, v98, v114 dst_sel:DWORD dst_unused:UNUSED_PAD src0_sel:DWORD src1_sel:BYTE_3
	s_waitcnt vmcnt(15)
	v_lshlrev_b32_sdwa v113, v98, v115 dst_sel:DWORD dst_unused:UNUSED_PAD src0_sel:DWORD src1_sel:BYTE_3
	v_add_u32_e32 v74, s45, v74
	v_add_u32_e32 v113, s45, v113
	v_lshlrev_b32_e32 v106, 16, v77
	v_and_b32_e32 v107, 0xffff0000, v77
	ds_read_b32 v77, v74
	ds_read_b32 v113, v113
	s_waitcnt lgkmcnt(2)
	v_add_u32_e32 v74, v118, v76
	v_ashrrev_i32_e32 v75, 31, v74
	v_lshlrev_b64 v[74:75], 10, v[74:75]
	v_lshl_add_u64 v[74:75], v[36:37], 0, v[74:75]
	global_load_dword v135, v[74:75], off nt
	global_load_dword v136, v[74:75], off offset:256 nt
	v_and_b32_e32 v76, 0xffffff, v114
	s_waitcnt lgkmcnt(1)
	v_add_u32_e32 v76, v77, v76
	v_ashrrev_i32_e32 v77, 31, v76
	v_lshlrev_b64 v[76:77], 10, v[76:77]
	v_lshl_add_u64 v[76:77], v[36:37], 0, v[76:77]
	global_load_dword v137, v[74:75], off offset:512 nt
	global_load_dword v138, v[74:75], off offset:768 nt
	global_load_dword v139, v[76:77], off nt
	global_load_dword v140, v[76:77], off offset:256 nt
	global_load_dword v141, v[76:77], off offset:512 nt
	global_load_dword v142, v[76:77], off offset:768 nt
	s_waitcnt vmcnt(22)
	v_lshlrev_b32_sdwa v74, v98, v116 dst_sel:DWORD dst_unused:UNUSED_PAD src0_sel:DWORD src1_sel:BYTE_3
	v_and_b32_e32 v114, 0xffffff, v115
	v_add_u32_e32 v74, s45, v74
	ds_read_b32 v77, v74
	s_waitcnt lgkmcnt(1)
	v_add_u32_e32 v74, v113, v114
	s_waitcnt vmcnt(21)
	v_lshlrev_b32_sdwa v113, v98, v132 dst_sel:DWORD dst_unused:UNUSED_PAD src0_sel:DWORD src1_sel:BYTE_3
	v_mul_f32_e32 v112, 0x3d000000, v112
	v_add_u32_e32 v113, s45, v113
	v_and_b32_e32 v76, 0xffffff, v116
	v_lshlrev_b32_e32 v108, 16, v78
	v_and_b32_e32 v109, 0xffff0000, v78
	v_lshlrev_b32_e32 v78, 16, v79
	v_and_b32_e32 v79, 0xffff0000, v79
	v_lshlrev_b32_e32 v110, 16, v80
	v_and_b32_e32 v111, 0xffff0000, v80
	ds_read_b32 v143, v113
	v_lshlrev_b32_e32 v80, 16, v81
	v_and_b32_e32 v81, 0xffff0000, v81
	v_ashrrev_i32_e32 v75, 31, v74
	s_waitcnt lgkmcnt(1)
	v_add_u32_e32 v76, v77, v76
	v_lshlrev_b64 v[74:75], 10, v[74:75]
	v_ashrrev_i32_e32 v77, 31, v76
	v_lshl_add_u64 v[74:75], v[36:37], 0, v[74:75]
	v_lshlrev_b64 v[76:77], 10, v[76:77]
	v_lshl_add_u64 v[76:77], v[36:37], 0, v[76:77]
	s_lshl_b64 s[28:29], s[24:25], 10
	s_waitcnt vmcnt(18)
	v_cvt_pk_f32_fp8_e32 v[122:123], v124
	v_cvt_pk_f32_fp8_sdwa v[124:125], v124 src0_sel:WORD_1
	v_cvt_pk_f32_fp8_e32 v[114:115], v117
	v_cvt_pk_f32_fp8_e32 v[118:119], v120
	v_cvt_pk_f32_fp8_sdwa v[120:121], v120 src0_sel:WORD_1
	v_cvt_pk_f32_fp8_sdwa v[116:117], v117 src0_sel:WORD_1
	v_pk_mul_f32 v[114:115], v[112:113], v[114:115] op_sel_hi:[0,1]
	v_pk_mul_f32 v[118:119], v[112:113], v[118:119] op_sel_hi:[0,1]
	v_pk_mul_f32 v[120:121], v[112:113], v[120:121] op_sel_hi:[0,1]
	v_pk_fma_f32 v[82:83], v[12:13], v[118:119], v[82:83]
	v_pk_fma_f32 v[106:107], v[14:15], v[120:121], v[106:107]
	s_waitcnt vmcnt(12)
	v_cvt_pk_f32_fp8_sdwa v[118:119], v105 src0_sel:WORD_1
	v_cvt_pk_f32_fp8_e32 v[120:121], v105
	v_pk_mul_f32 v[116:117], v[112:113], v[116:117] op_sel_hi:[0,1]
	v_pk_fma_f32 v[84:85], v[0:1], v[114:115], v[84:85]
	v_pk_mul_f32 v[114:115], v[112:113], v[124:125] op_sel_hi:[0,1]
	v_pk_fma_f32 v[86:87], v[2:3], v[116:117], v[86:87]
	v_pk_mul_f32 v[116:117], v[112:113], v[122:123] op_sel_hi:[0,1]
	v_pk_fma_f32 v[78:79], v[26:27], v[114:115], v[78:79]
	v_pk_mul_f32 v[114:115], v[112:113], v[118:119] op_sel_hi:[0,1]
	v_pk_mul_f32 v[112:113], v[112:113], v[120:121] op_sel_hi:[0,1]
	v_pk_fma_f32 v[108:109], v[24:25], v[116:117], v[108:109]
	v_pk_fma_f32 v[110:111], v[28:29], v[112:113], v[110:111]
	s_waitcnt vmcnt(11)
	v_cvt_pk_f32_fp8_e32 v[112:113], v129
	v_cvt_pk_f32_fp8_sdwa v[116:117], v129 src0_sel:WORD_1
	s_waitcnt vmcnt(10)
	v_cvt_pk_f32_fp8_e32 v[118:119], v130
	v_cvt_pk_f32_fp8_sdwa v[120:121], v130 src0_sel:WORD_1
	v_pk_fma_f32 v[80:81], v[30:31], v[114:115], v[80:81]
	v_mul_f32_e32 v114, 0x3d000000, v126
	v_pk_mul_f32 v[112:113], v[114:115], v[112:113] op_sel_hi:[0,1]
	v_pk_mul_f32 v[116:117], v[114:115], v[116:117] op_sel_hi:[0,1]
	v_pk_fma_f32 v[86:87], v[2:3], v[116:117], v[86:87]
	v_pk_fma_f32 v[84:85], v[0:1], v[112:113], v[84:85]
	v_pk_mul_f32 v[112:113], v[114:115], v[118:119] op_sel_hi:[0,1]
	v_pk_mul_f32 v[116:117], v[114:115], v[120:121] op_sel_hi:[0,1]
	s_waitcnt vmcnt(9)
	v_cvt_pk_f32_fp8_e32 v[118:119], v131
	v_cvt_pk_f32_fp8_sdwa v[120:121], v131 src0_sel:WORD_1
	v_pk_fma_f32 v[106:107], v[14:15], v[116:117], v[106:107]
	v_pk_fma_f32 v[82:83], v[12:13], v[112:113], v[82:83]
	v_pk_mul_f32 v[112:113], v[114:115], v[118:119] op_sel_hi:[0,1]
	v_pk_mul_f32 v[116:117], v[114:115], v[120:121] op_sel_hi:[0,1]
	s_waitcnt vmcnt(8)
	v_cvt_pk_f32_fp8_e32 v[118:119], v134
	v_cvt_pk_f32_fp8_sdwa v[120:121], v134 src0_sel:WORD_1
	v_pk_fma_f32 v[108:109], v[24:25], v[112:113], v[108:109]
	v_pk_fma_f32 v[78:79], v[26:27], v[116:117], v[78:79]
	v_pk_mul_f32 v[112:113], v[114:115], v[118:119] op_sel_hi:[0,1]
	v_pk_mul_f32 v[114:115], v[114:115], v[120:121] op_sel_hi:[0,1]
	v_pk_fma_f32 v[80:81], v[30:31], v[114:115], v[80:81]
	s_waitcnt vmcnt(7)
	v_cvt_pk_f32_fp8_sdwa v[114:115], v135 src0_sel:WORD_1
	v_cvt_pk_f32_fp8_e32 v[116:117], v135
	s_waitcnt vmcnt(6)
	v_cvt_pk_f32_fp8_sdwa v[118:119], v136 src0_sel:WORD_1
	v_cvt_pk_f32_fp8_e32 v[120:121], v136
	v_pk_fma_f32 v[110:111], v[28:29], v[112:113], v[110:111]
	v_mul_f32_e32 v112, 0x3d000000, v127
	v_pk_mul_f32 v[114:115], v[112:113], v[114:115] op_sel_hi:[0,1]
	v_pk_mul_f32 v[116:117], v[112:113], v[116:117] op_sel_hi:[0,1]
	v_pk_fma_f32 v[84:85], v[0:1], v[116:117], v[84:85]
	v_pk_fma_f32 v[86:87], v[2:3], v[114:115], v[86:87]
	v_pk_mul_f32 v[114:115], v[112:113], v[118:119] op_sel_hi:[0,1]
	v_pk_mul_f32 v[116:117], v[112:113], v[120:121] op_sel_hi:[0,1]
	s_waitcnt vmcnt(5)
	v_cvt_pk_f32_fp8_sdwa v[118:119], v137 src0_sel:WORD_1
	v_cvt_pk_f32_fp8_e32 v[120:121], v137
	v_pk_fma_f32 v[82:83], v[12:13], v[116:117], v[82:83]
	v_pk_fma_f32 v[106:107], v[14:15], v[114:115], v[106:107]
	v_pk_mul_f32 v[114:115], v[112:113], v[118:119] op_sel_hi:[0,1]
	v_pk_mul_f32 v[116:117], v[112:113], v[120:121] op_sel_hi:[0,1]
	s_waitcnt vmcnt(4)
	v_cvt_pk_f32_fp8_sdwa v[118:119], v138 src0_sel:WORD_1
	v_cvt_pk_f32_fp8_e32 v[120:121], v138
	v_pk_fma_f32 v[78:79], v[26:27], v[114:115], v[78:79]
	v_pk_fma_f32 v[108:109], v[24:25], v[116:117], v[108:109]
	v_pk_mul_f32 v[114:115], v[112:113], v[118:119] op_sel_hi:[0,1]
	v_pk_mul_f32 v[112:113], v[112:113], v[120:121] op_sel_hi:[0,1]
	v_pk_fma_f32 v[110:111], v[28:29], v[112:113], v[110:111]
	s_waitcnt vmcnt(3)
	v_cvt_pk_f32_fp8_e32 v[112:113], v139
	s_waitcnt vmcnt(2)
	v_cvt_pk_f32_fp8_e32 v[118:119], v140
	v_cvt_pk_f32_fp8_sdwa v[116:117], v139 src0_sel:WORD_1
	v_pk_fma_f32 v[80:81], v[30:31], v[114:115], v[80:81]
	v_mul_f32_e32 v114, 0x3d000000, v128
	v_cvt_pk_f32_fp8_sdwa v[120:121], v140 src0_sel:WORD_1
	v_pk_mul_f32 v[112:113], v[114:115], v[112:113] op_sel_hi:[0,1]
	v_pk_fma_f32 v[84:85], v[0:1], v[112:113], v[84:85]
	v_pk_mul_f32 v[112:113], v[114:115], v[118:119] op_sel_hi:[0,1]
	s_waitcnt vmcnt(1)
	v_cvt_pk_f32_fp8_e32 v[118:119], v141
	v_pk_mul_f32 v[116:117], v[114:115], v[116:117] op_sel_hi:[0,1]
	v_pk_fma_f32 v[86:87], v[2:3], v[116:117], v[86:87]
	v_pk_mul_f32 v[116:117], v[114:115], v[120:121] op_sel_hi:[0,1]
	v_cvt_pk_f32_fp8_sdwa v[120:121], v141 src0_sel:WORD_1
	v_pk_fma_f32 v[82:83], v[12:13], v[112:113], v[82:83]
	v_pk_mul_f32 v[112:113], v[114:115], v[118:119] op_sel_hi:[0,1]
	s_waitcnt vmcnt(0)
	v_cvt_pk_f32_fp8_e32 v[118:119], v142
	v_pk_fma_f32 v[106:107], v[14:15], v[116:117], v[106:107]
	v_pk_mul_f32 v[116:117], v[114:115], v[120:121] op_sel_hi:[0,1]
	v_cvt_pk_f32_fp8_sdwa v[120:121], v142 src0_sel:WORD_1
	v_pk_fma_f32 v[108:109], v[24:25], v[112:113], v[108:109]
	v_pk_mul_f32 v[112:113], v[114:115], v[118:119] op_sel_hi:[0,1]
	v_and_b32_sdwa v105, v85, v99 dst_sel:DWORD dst_unused:UNUSED_PAD src0_sel:WORD_1 src1_sel:DWORD
	v_pk_fma_f32 v[110:111], v[28:29], v[112:113], v[110:111]
	v_and_b32_sdwa v112, v84, v99 dst_sel:DWORD dst_unused:UNUSED_PAD src0_sel:WORD_1 src1_sel:DWORD
	v_add3_u32 v85, v85, v105, s46
	v_and_b32_sdwa v105, v87, v99 dst_sel:DWORD dst_unused:UNUSED_PAD src0_sel:WORD_1 src1_sel:DWORD
	v_pk_mul_f32 v[114:115], v[114:115], v[120:121] op_sel_hi:[0,1]
	v_add3_u32 v121, v84, v112, s46
	v_and_b32_sdwa v112, v86, v99 dst_sel:DWORD dst_unused:UNUSED_PAD src0_sel:WORD_1 src1_sel:DWORD
	v_add3_u32 v87, v87, v105, s46
	v_and_b32_sdwa v105, v83, v99 dst_sel:DWORD dst_unused:UNUSED_PAD src0_sel:WORD_1 src1_sel:DWORD
	v_add3_u32 v134, v86, v112, s46
	v_and_b32_sdwa v112, v82, v99 dst_sel:DWORD dst_unused:UNUSED_PAD src0_sel:WORD_1 src1_sel:DWORD
	v_add3_u32 v83, v83, v105, s46
	v_and_b32_sdwa v105, v107, v99 dst_sel:DWORD dst_unused:UNUSED_PAD src0_sel:WORD_1 src1_sel:DWORD
	v_add3_u32 v135, v82, v112, s46
	v_and_b32_sdwa v112, v106, v99 dst_sel:DWORD dst_unused:UNUSED_PAD src0_sel:WORD_1 src1_sel:DWORD
	v_add3_u32 v105, v107, v105, s46
	v_pk_fma_f32 v[78:79], v[26:27], v[116:117], v[78:79]
	v_add3_u32 v136, v106, v112, s46
	v_and_b32_e32 v123, 0xffff0000, v105
	v_and_b32_sdwa v105, v109, v99 dst_sel:DWORD dst_unused:UNUSED_PAD src0_sel:WORD_1 src1_sel:DWORD
	v_and_b32_sdwa v106, v108, v99 dst_sel:DWORD dst_unused:UNUSED_PAD src0_sel:WORD_1 src1_sel:DWORD
	v_add3_u32 v105, v109, v105, s46
	v_add3_u32 v137, v108, v106, s46
	v_and_b32_sdwa v106, v78, v99 dst_sel:DWORD dst_unused:UNUSED_PAD src0_sel:WORD_1 src1_sel:DWORD
	v_and_b32_e32 v125, 0xffff0000, v105
	v_and_b32_sdwa v105, v79, v99 dst_sel:DWORD dst_unused:UNUSED_PAD src0_sel:WORD_1 src1_sel:DWORD
	v_add3_u32 v138, v78, v106, s46
	v_and_b32_sdwa v78, v111, v99 dst_sel:DWORD dst_unused:UNUSED_PAD src0_sel:WORD_1 src1_sel:DWORD
	v_pk_fma_f32 v[80:81], v[30:31], v[114:115], v[80:81]
	v_add3_u32 v79, v79, v105, s46
	v_add3_u32 v78, v111, v78, s46
	v_and_b32_e32 v127, 0xffff0000, v79
	v_and_b32_sdwa v79, v110, v99 dst_sel:DWORD dst_unused:UNUSED_PAD src0_sel:WORD_1 src1_sel:DWORD
	v_and_b32_e32 v129, 0xffff0000, v78
	v_and_b32_sdwa v78, v81, v99 dst_sel:DWORD dst_unused:UNUSED_PAD src0_sel:WORD_1 src1_sel:DWORD
	v_and_b32_e32 v85, 0xffff0000, v85
	v_and_b32_e32 v84, 0xffff0000, v121
	v_add3_u32 v139, v110, v79, s46
	v_and_b32_sdwa v79, v80, v99 dst_sel:DWORD dst_unused:UNUSED_PAD src0_sel:WORD_1 src1_sel:DWORD
	v_add3_u32 v78, v81, v78, s46
	v_and_b32_e32 v87, 0xffff0000, v87
	v_and_b32_e32 v86, 0xffff0000, v134
	v_add3_u32 v80, v80, v79, s46
	v_and_b32_e32 v131, 0xffff0000, v78
	v_pk_fma_f32 v[78:79], v[84:85], v[84:85], 0 op_sel_hi:[1,1,0]
	v_and_b32_e32 v83, 0xffff0000, v83
	v_and_b32_e32 v82, 0xffff0000, v135
	v_pk_fma_f32 v[78:79], v[86:87], v[86:87], v[78:79]
	v_and_b32_e32 v122, 0xffff0000, v136
	v_pk_fma_f32 v[78:79], v[82:83], v[82:83], v[78:79]
	v_and_b32_e32 v124, 0xffff0000, v137
	v_pk_fma_f32 v[78:79], v[122:123], v[122:123], v[78:79]
	v_and_b32_e32 v126, 0xffff0000, v138
	v_pk_fma_f32 v[78:79], v[124:125], v[124:125], v[78:79]
	v_and_b32_e32 v128, 0xffff0000, v139
	v_pk_fma_f32 v[78:79], v[126:127], v[126:127], v[78:79]
	v_and_b32_e32 v130, 0xffff0000, v80
	v_pk_fma_f32 v[78:79], v[128:129], v[128:129], v[78:79]
	global_load_dword v120, v[74:75], off nt
	global_load_dword v119, v[74:75], off offset:256 nt
	global_load_dword v118, v[74:75], off offset:512 nt
	global_load_dword v117, v[74:75], off offset:768 nt
	global_load_dword v116, v[76:77], off nt
	global_load_dword v115, v[76:77], off offset:256 nt
	global_load_dword v113, v[76:77], off offset:512 nt
	global_load_dword v111, v[76:77], off offset:768 nt
	v_pk_fma_f32 v[78:79], v[130:131], v[130:131], v[78:79]
	v_lshlrev_b32_sdwa v77, v98, v133 dst_sel:DWORD dst_unused:UNUSED_PAD src0_sel:DWORD src1_sel:BYTE_3
	v_add_f32_e32 v78, v78, v79
	v_add_u32_e32 v77, s45, v77
	ds_read_b32 v77, v77
	v_and_b32_e32 v74, 0xffffff, v132
	s_waitcnt lgkmcnt(0)
	v_add_u32_e32 v74, v143, v74
	s_waitcnt lgkmcnt(0)
	s_nop 1
	v_add_f32_dpp v75, v78, v78 quad_perm:[1,0,3,2] row_mask:0xf bank_mask:0xf
	v_and_b32_e32 v79, 0xffffff, v133
	s_waitcnt lgkmcnt(0)
	s_nop 1
	v_add_f32_dpp v76, v75, v75 quad_perm:[2,3,0,1] row_mask:0xf bank_mask:0xf
	v_ashrrev_i32_e32 v75, 31, v74
	v_lshlrev_b64 v[74:75], 10, v[74:75]
	v_lshl_add_u64 v[74:75], v[36:37], 0, v[74:75]
	s_waitcnt lgkmcnt(0)
	s_nop 1
	v_add_f32_dpp v78, v76, v76 row_half_mirror row_mask:0xf bank_mask:0xf
	v_add_u32_e32 v76, v77, v79
	v_ashrrev_i32_e32 v77, 31, v76
	v_lshlrev_b64 v[76:77], 10, v[76:77]
	v_lshl_add_u64 v[76:77], v[36:37], 0, v[76:77]
	s_waitcnt lgkmcnt(0)
	s_nop 1
	v_add_f32_dpp v78, v78, v78 row_mirror row_mask:0xf bank_mask:0xf
	global_load_dword v114, v[74:75], off nt
	global_load_dword v112, v[74:75], off offset:256 nt
	global_load_dword v110, v[74:75], off offset:512 nt
	global_load_dword v109, v[74:75], off offset:768 nt
	global_load_dword v108, v[76:77], off nt
	global_load_dword v107, v[76:77], off offset:256 nt
	global_load_dword v106, v[76:77], off offset:512 nt
	global_load_dword v105, v[76:77], off offset:768 nt
	v_or_b32_sdwa v74, v85, v121 dst_sel:DWORD dst_unused:UNUSED_PAD src0_sel:DWORD src1_sel:WORD_1
	v_or_b32_sdwa v75, v87, v134 dst_sel:DWORD dst_unused:UNUSED_PAD src0_sel:DWORD src1_sel:WORD_1
	global_store_dwordx2 v[72:73], v[74:75], off
	s_waitcnt lgkmcnt(0)
	v_mov_b32_e32 v76, v78
	v_mov_b32_e32 v79, v78
	s_nop 1
	v_permlane16_swap_b32_e32 v76, v79
	v_add_f32_e32 v76, v76, v79
	v_or_b32_sdwa v74, v83, v135 dst_sel:DWORD dst_unused:UNUSED_PAD src0_sel:DWORD src1_sel:WORD_1
	v_or_b32_sdwa v75, v123, v136 dst_sel:DWORD dst_unused:UNUSED_PAD src0_sel:DWORD src1_sel:WORD_1
	global_store_dwordx2 v[72:73], v[74:75], off offset:512
	s_waitcnt lgkmcnt(0)
	v_mov_b32_e32 v74, v76
	v_mov_b32_e32 v77, v76
	s_nop 1
	v_permlane32_swap_b32_e32 v74, v77
	v_add_f32_e32 v74, v74, v77
	v_fmamk_f32 v74, v74, 0x3a800000, v96
	v_mul_f32_e32 v75, 0x4f800000, v74
	v_cmp_gt_f32_e32 vcc, s47, v74
	s_nop 1
	v_cndmask_b32_e32 v76, v74, v75, vcc
	v_sqrt_f32_e32 v77, v76
	v_or_b32_sdwa v74, v125, v137 dst_sel:DWORD dst_unused:UNUSED_PAD src0_sel:DWORD src1_sel:WORD_1
	v_or_b32_sdwa v75, v127, v138 dst_sel:DWORD dst_unused:UNUSED_PAD src0_sel:DWORD src1_sel:WORD_1
	global_store_dwordx2 v[72:73], v[74:75], off offset:1024
	v_add_u32_e32 v74, -1, v77
	v_fma_f32 v75, -v74, v77, v76
	v_cmp_ge_f32_e64 s[10:11], 0, v75
	v_add_u32_e32 v75, 1, v77
	s_nop 0
	v_cndmask_b32_e64 v74, v77, v74, s[10:11]
	v_fma_f32 v77, -v75, v77, v76
	v_cmp_lt_f32_e64 s[10:11], 0, v77
	s_nop 1
	v_cndmask_b32_e64 v74, v74, v75, s[10:11]
	v_mul_f32_e32 v75, 0x37800000, v74
	v_cndmask_b32_e32 v74, v74, v75, vcc
	v_cmp_class_f32_e32 vcc, v76, v97
	v_or_b32_sdwa v75, v131, v80 dst_sel:DWORD dst_unused:UNUSED_PAD src0_sel:DWORD src1_sel:WORD_1
	s_nop 0
	v_cndmask_b32_e32 v76, v74, v76, vcc
	v_div_scale_f32 v77, s[10:11], v76, v76, 1.0
	v_rcp_f32_e32 v78, v77
	v_or_b32_sdwa v74, v129, v139 dst_sel:DWORD dst_unused:UNUSED_PAD src0_sel:DWORD src1_sel:WORD_1
	global_store_dwordx2 v[72:73], v[74:75], off offset:1536
	v_fma_f32 v72, -v77, v78, 1.0
	v_fmac_f32_e32 v78, v72, v78
	v_div_scale_f32 v72, vcc, 1.0, v76, 1.0
	v_mul_f32_e32 v73, v72, v78
	v_fma_f32 v74, -v77, v73, v72
	v_fmac_f32_e32 v73, v74, v78
	v_fma_f32 v72, -v77, v73, v72
	v_div_fmas_f32 v72, v72, v78, v73
	v_div_fixup_f32 v132, v72, v76, 1.0
	v_pk_mul_f32 v[74:75], v[132:133], v[84:85] op_sel_hi:[0,1]
	v_pk_fma_f32 v[74:75], v[48:49], v[74:75], v[4:5]
	v_pk_mul_f32 v[72:73], v[132:133], v[86:87] op_sel_hi:[0,1]
	v_bfe_u32 v121, v74, 16, 1
	v_pk_mul_f32 v[78:79], v[132:133], v[82:83] op_sel_hi:[0,1]
	v_pk_mul_f32 v[82:83], v[132:133], v[124:125] op_sel_hi:[0,1]
	v_add3_u32 v121, v74, v121, s46
	v_bfe_u32 v124, v75, 16, 1
	v_pk_fma_f32 v[72:73], v[46:47], v[72:73], v[6:7]
	v_lshrrev_b32_e32 v121, 16, v121
	v_add3_u32 v124, v75, v124, s46
	v_and_or_b32 v124, v124, s44, v121
	v_bfe_u32 v121, v72, 16, 1
	v_add3_u32 v121, v72, v121, s46
	v_bfe_u32 v125, v73, 16, 1
	v_pk_fma_f32 v[78:79], v[52:53], v[78:79], v[8:9]
	v_lshrrev_b32_e32 v121, 16, v121
	v_add3_u32 v125, v73, v125, s46
	v_pk_mul_f32 v[76:77], v[132:133], v[122:123] op_sel_hi:[0,1]
	v_lshl_add_u64 v[122:123], v[38:39], 0, s[26:27]
	v_and_or_b32 v125, v125, s44, v121
	v_bfe_u32 v121, v78, 16, 1
	global_store_dwordx2 v[122:123], v[124:125], off
	v_add3_u32 v121, v78, v121, s46
	v_bfe_u32 v124, v79, 16, 1
	v_pk_fma_f32 v[76:77], v[50:51], v[76:77], v[10:11]
	v_lshrrev_b32_e32 v121, 16, v121
	v_add3_u32 v124, v79, v124, s46
	v_and_or_b32 v124, v124, s44, v121
	v_bfe_u32 v121, v76, 16, 1
	v_add3_u32 v121, v76, v121, s46
	v_bfe_u32 v125, v77, 16, 1
	v_pk_fma_f32 v[82:83], v[56:57], v[82:83], v[16:17]
	v_lshrrev_b32_e32 v121, 16, v121
	v_add3_u32 v125, v77, v125, s46
	v_and_or_b32 v125, v125, s44, v121
	v_bfe_u32 v121, v82, 16, 1
	v_pk_mul_f32 v[80:81], v[132:133], v[126:127] op_sel_hi:[0,1]
	global_store_dwordx2 v[122:123], v[124:125], off offset:512
	v_add3_u32 v121, v82, v121, s46
	v_bfe_u32 v124, v83, 16, 1
	v_pk_fma_f32 v[80:81], v[54:55], v[80:81], v[18:19]
	v_lshrrev_b32_e32 v121, 16, v121
	v_add3_u32 v124, v83, v124, s46
	v_and_or_b32 v124, v124, s44, v121
	v_bfe_u32 v121, v80, 16, 1
	v_pk_mul_f32 v[86:87], v[132:133], v[128:129] op_sel_hi:[0,1]
	v_add3_u32 v121, v80, v121, s46
	v_bfe_u32 v125, v81, 16, 1
	v_pk_fma_f32 v[86:87], v[60:61], v[86:87], v[20:21]
	v_lshrrev_b32_e32 v121, 16, v121
	v_add3_u32 v125, v81, v125, s46
	v_and_or_b32 v125, v125, s44, v121
	v_bfe_u32 v121, v86, 16, 1
	v_pk_mul_f32 v[84:85], v[132:133], v[130:131] op_sel_hi:[0,1]
	global_store_dwordx2 v[122:123], v[124:125], off offset:1024
	v_add3_u32 v121, v86, v121, s46
	v_bfe_u32 v124, v87, 16, 1
	v_pk_fma_f32 v[84:85], v[58:59], v[84:85], v[22:23]
	v_lshrrev_b32_e32 v121, 16, v121
	v_add3_u32 v124, v87, v124, s46
	v_and_or_b32 v124, v124, s44, v121
	v_bfe_u32 v121, v84, 16, 1
	v_add3_u32 v121, v84, v121, s46
	v_bfe_u32 v125, v85, 16, 1
	v_mul_f32_e32 v126, 0x41000000, v74
	v_mul_f32_e32 v127, 0x41000000, v75
	v_lshrrev_b32_e32 v121, 16, v121
	v_add3_u32 v125, v85, v125, s46
	v_med3_f32 v126, v126, s48, v100
	v_med3_f32 v127, v127, s48, v100
	v_mov_b32_e32 v129, 0
	v_cvt_pk_fp8_f32 v129, v126, v127
	v_and_or_b32 v125, v125, s44, v121
	v_mul_f32_e32 v128, 0x41000000, v72
	global_store_dwordx2 v[122:123], v[124:125], off offset:1536
	v_mul_f32_e32 v121, 0x41000000, v78
	v_mul_f32_e32 v122, 0x41000000, v79
	v_mul_f32_e32 v126, 0x41000000, v73
	v_med3_f32 v127, v128, s48, v100
	v_med3_f32 v121, v121, s48, v100
	v_med3_f32 v122, v122, s48, v100
	v_mov_b32_e32 v128, 0
	v_med3_f32 v126, v126, s48, v100
	v_cvt_pk_fp8_f32 v128, v121, v122
	v_cvt_pk_fp8_f32 v129, v127, v126 op_sel:[0,0,1]
	v_mul_f32_e32 v123, 0x41000000, v76
	v_mul_f32_e32 v121, 0x41000000, v77
	v_med3_f32 v122, v123, s48, v100
	v_med3_f32 v121, v121, s48, v100
	v_lshl_add_u64 v[126:127], v[40:41], 0, s[28:29]
	v_cvt_pk_fp8_f32 v128, v122, v121 op_sel:[0,0,1]
	v_mul_f32_e32 v121, 0x41000000, v82
	v_mul_f32_e32 v122, 0x41000000, v83
	global_store_dword v[126:127], v129, off
	v_med3_f32 v121, v121, s48, v100
	v_med3_f32 v122, v122, s48, v100
	v_mov_b32_e32 v129, 0
	v_cvt_pk_fp8_f32 v129, v121, v122
	v_mul_f32_e32 v123, 0x41000000, v80
	v_mul_f32_e32 v121, 0x41000000, v81
	v_med3_f32 v122, v123, s48, v100
	v_med3_f32 v121, v121, s48, v100
	v_cvt_pk_fp8_f32 v129, v122, v121 op_sel:[0,0,1]
	v_mul_f32_e32 v121, 0x41000000, v86
	v_mul_f32_e32 v122, 0x41000000, v87
	v_med3_f32 v121, v121, s48, v100
	v_med3_f32 v122, v122, s48, v100
	v_mov_b32_e32 v130, 0
	v_cvt_pk_fp8_f32 v130, v121, v122
	v_mul_f32_e32 v123, 0x41000000, v84
	v_mul_f32_e32 v121, 0x41000000, v85
	v_med3_f32 v122, v123, s48, v100
	v_med3_f32 v121, v121, s48, v100
	v_cvt_pk_fp8_f32 v130, v122, v121 op_sel:[0,0,1]
	ds_read_b128 v[122:125], v94
	global_store_dword v[126:127], v128, off offset:256
	global_store_dword v[126:127], v129, off offset:512
	global_store_dword v[126:127], v130, off offset:768
	ds_read_b128 v[126:129], v94 offset:1024
	ds_read_b128 v[130:133], v94 offset:2048
	s_waitcnt lgkmcnt(2)
	v_pk_fma_f32 v[122:123], v[74:75], v[122:123], 0 op_sel_hi:[1,1,0]
	s_nop 0
	v_pk_fma_f32 v[134:135], v[72:73], v[124:125], v[122:123]
	ds_read_b128 v[122:125], v94 offset:3072
	s_waitcnt lgkmcnt(2)
	v_pk_fma_f32 v[126:127], v[78:79], v[126:127], v[134:135]
	s_nop 0
	v_pk_fma_f32 v[126:127], v[76:77], v[128:129], v[126:127]
	s_waitcnt lgkmcnt(1)
	v_pk_fma_f32 v[126:127], v[82:83], v[130:131], v[126:127]
	s_nop 0
	v_pk_fma_f32 v[126:127], v[80:81], v[132:133], v[126:127]
	s_waitcnt lgkmcnt(0)
	v_pk_fma_f32 v[122:123], v[86:87], v[122:123], v[126:127]
	ds_read_b128 v[126:129], v94 offset:5120
	ds_read_b128 v[130:133], v94 offset:4096
	v_pk_fma_f32 v[122:123], v[84:85], v[124:125], v[122:123]
	s_waitcnt lgkmcnt(0)
	v_pk_fma_f32 v[130:131], v[74:75], v[130:131], 0 op_sel_hi:[1,1,0]
	v_add_f32_e32 v121, v122, v123
	ds_read_b128 v[122:125], v94 offset:7168
	ds_read_b128 v[134:137], v94 offset:6144
	v_pk_fma_f32 v[130:131], v[72:73], v[132:133], v[130:131]
	s_nop 0
	v_pk_fma_f32 v[126:127], v[78:79], v[126:127], v[130:131]
	s_nop 0
	v_pk_fma_f32 v[126:127], v[76:77], v[128:129], v[126:127]
	s_waitcnt lgkmcnt(0)
	v_pk_fma_f32 v[126:127], v[82:83], v[134:135], v[126:127]
	s_nop 0
	v_pk_fma_f32 v[126:127], v[80:81], v[136:137], v[126:127]
	s_nop 0
	v_pk_fma_f32 v[122:123], v[86:87], v[122:123], v[126:127]
	s_nop 0
	v_pk_fma_f32 v[122:123], v[84:85], v[124:125], v[122:123]
	s_nop 0
	v_add_f32_e32 v138, v122, v123
	ds_read_b128 v[122:125], v94 offset:8192
	ds_read_b128 v[126:129], v94 offset:9216
	ds_read_b128 v[130:133], v94 offset:10240
	ds_read_b128 v[134:137], v94 offset:11264
	s_waitcnt lgkmcnt(3)
	v_pk_fma_f32 v[122:123], v[74:75], v[122:123], 0 op_sel_hi:[1,1,0]
	s_nop 0
	v_pk_fma_f32 v[122:123], v[72:73], v[124:125], v[122:123]
	s_waitcnt lgkmcnt(2)
	v_pk_fma_f32 v[122:123], v[78:79], v[126:127], v[122:123]
	s_nop 0
	v_pk_fma_f32 v[122:123], v[76:77], v[128:129], v[122:123]
	s_waitcnt lgkmcnt(1)
	v_pk_fma_f32 v[122:123], v[82:83], v[130:131], v[122:123]
	s_nop 0
	v_pk_fma_f32 v[122:123], v[80:81], v[132:133], v[122:123]
	s_waitcnt lgkmcnt(0)
	v_pk_fma_f32 v[130:131], v[86:87], v[134:135], v[122:123]
	ds_read_b128 v[122:125], v94 offset:13312
	ds_read_b128 v[126:129], v94 offset:12288
	v_pk_fma_f32 v[130:131], v[84:85], v[136:137], v[130:131]
	s_waitcnt lgkmcnt(0)
	v_pk_fma_f32 v[126:127], v[74:75], v[126:127], 0 op_sel_hi:[1,1,0]
	v_add_f32_e32 v139, v130, v131
	ds_read_b128 v[130:133], v94 offset:15360
	ds_read_b128 v[134:137], v94 offset:14336
	v_pk_fma_f32 v[126:127], v[72:73], v[128:129], v[126:127]
	s_nop 0
	v_pk_fma_f32 v[122:123], v[78:79], v[122:123], v[126:127]
	s_nop 0
	v_pk_fma_f32 v[122:123], v[76:77], v[124:125], v[122:123]
	s_waitcnt lgkmcnt(0)
	v_pk_fma_f32 v[122:123], v[82:83], v[134:135], v[122:123]
	s_nop 0
	v_pk_fma_f32 v[122:123], v[80:81], v[136:137], v[122:123]
	s_nop 0
	v_pk_fma_f32 v[122:123], v[86:87], v[130:131], v[122:123]
	s_nop 0
	v_pk_fma_f32 v[122:123], v[84:85], v[132:133], v[122:123]
	s_nop 0
	v_add_f32_e32 v140, v122, v123
	ds_read_b128 v[122:125], v94 offset:16384
	ds_read_b128 v[126:129], v94 offset:17408
	ds_read_b128 v[130:133], v94 offset:18432
	ds_read_b128 v[134:137], v94 offset:19456
	s_waitcnt lgkmcnt(3)
	v_pk_fma_f32 v[122:123], v[74:75], v[122:123], 0 op_sel_hi:[1,1,0]
	s_nop 0
	v_pk_fma_f32 v[122:123], v[72:73], v[124:125], v[122:123]
	s_waitcnt lgkmcnt(2)
	v_pk_fma_f32 v[122:123], v[78:79], v[126:127], v[122:123]
	s_nop 0
	v_pk_fma_f32 v[122:123], v[76:77], v[128:129], v[122:123]
	s_waitcnt lgkmcnt(1)
	v_pk_fma_f32 v[122:123], v[82:83], v[130:131], v[122:123]
	s_nop 0
	v_pk_fma_f32 v[122:123], v[80:81], v[132:133], v[122:123]
	s_waitcnt lgkmcnt(0)
	v_pk_fma_f32 v[130:131], v[86:87], v[134:135], v[122:123]
	ds_read_b128 v[122:125], v94 offset:21504
	ds_read_b128 v[126:129], v94 offset:20480
	v_pk_fma_f32 v[130:131], v[84:85], v[136:137], v[130:131]
	s_waitcnt lgkmcnt(0)
	v_pk_fma_f32 v[126:127], v[74:75], v[126:127], 0 op_sel_hi:[1,1,0]
	v_add_f32_e32 v141, v130, v131
	ds_read_b128 v[130:133], v94 offset:23552
	ds_read_b128 v[134:137], v94 offset:22528
	v_pk_fma_f32 v[126:127], v[72:73], v[128:129], v[126:127]
	s_nop 0
	v_pk_fma_f32 v[122:123], v[78:79], v[122:123], v[126:127]
	s_nop 0
	v_pk_fma_f32 v[122:123], v[76:77], v[124:125], v[122:123]
	s_waitcnt lgkmcnt(0)
	v_pk_fma_f32 v[122:123], v[82:83], v[134:135], v[122:123]
	s_nop 0
	v_pk_fma_f32 v[122:123], v[80:81], v[136:137], v[122:123]
	s_nop 0
	v_pk_fma_f32 v[122:123], v[86:87], v[130:131], v[122:123]
	s_nop 0
	v_pk_fma_f32 v[122:123], v[84:85], v[132:133], v[122:123]
	s_nop 0
	v_add_f32_e32 v142, v122, v123
	ds_read_b128 v[122:125], v94 offset:24576
	ds_read_b128 v[126:129], v94 offset:25600
	ds_read_b128 v[130:133], v94 offset:26624
	ds_read_b128 v[134:137], v94 offset:27648
	s_waitcnt lgkmcnt(3)
	v_pk_fma_f32 v[122:123], v[74:75], v[122:123], 0 op_sel_hi:[1,1,0]
	s_nop 0
	v_pk_fma_f32 v[122:123], v[72:73], v[124:125], v[122:123]
	s_waitcnt lgkmcnt(2)
	v_pk_fma_f32 v[122:123], v[78:79], v[126:127], v[122:123]
	s_nop 0
	v_pk_fma_f32 v[122:123], v[76:77], v[128:129], v[122:123]
	s_waitcnt lgkmcnt(1)
	v_pk_fma_f32 v[122:123], v[82:83], v[130:131], v[122:123]
	s_nop 0
	v_pk_fma_f32 v[122:123], v[80:81], v[132:133], v[122:123]
	s_waitcnt lgkmcnt(0)
	v_pk_fma_f32 v[130:131], v[86:87], v[134:135], v[122:123]
	ds_read_b128 v[122:125], v94 offset:29696
	ds_read_b128 v[126:129], v94 offset:28672
	v_pk_fma_f32 v[130:131], v[84:85], v[136:137], v[130:131]
	s_waitcnt lgkmcnt(0)
	v_pk_fma_f32 v[74:75], v[74:75], v[126:127], 0 op_sel_hi:[1,1,0]
	v_add_f32_e32 v143, v130, v131
	ds_read_b128 v[130:133], v94 offset:31744
	ds_read_b128 v[134:137], v94 offset:30720
	v_pk_fma_f32 v[72:73], v[72:73], v[128:129], v[74:75]
	s_nop 0
	v_pk_fma_f32 v[72:73], v[78:79], v[122:123], v[72:73]
	s_nop 0
	v_pk_fma_f32 v[72:73], v[76:77], v[124:125], v[72:73]
	s_waitcnt lgkmcnt(0)
	v_pk_fma_f32 v[72:73], v[82:83], v[134:135], v[72:73]
	s_nop 0
	v_pk_fma_f32 v[72:73], v[80:81], v[136:137], v[72:73]
	s_nop 0
	v_pk_fma_f32 v[72:73], v[86:87], v[130:131], v[72:73]
	s_nop 0
	v_pk_fma_f32 v[72:73], v[84:85], v[132:133], v[72:73]
	s_nop 0
	v_add_f32_e32 v72, v72, v73
	v_cndmask_b32_e64 v73, v121, v141, s[2:3]
	ds_bpermute_b32 v73, v93, v73
	v_cndmask_b32_e64 v74, v141, v121, s[2:3]
	v_cndmask_b32_e64 v75, v138, v142, s[2:3]
	ds_bpermute_b32 v75, v93, v75
	v_cndmask_b32_e64 v77, v140, v72, s[2:3]
	s_waitcnt lgkmcnt(1)
	v_add_f32_e32 v73, v74, v73
	v_cndmask_b32_e64 v74, v139, v143, s[2:3]
	ds_bpermute_b32 v74, v93, v74
	ds_bpermute_b32 v77, v93, v77
	v_cndmask_b32_e64 v76, v142, v138, s[2:3]
	s_waitcnt lgkmcnt(2)
	v_add_f32_e32 v75, v76, v75
	v_cndmask_b32_e64 v76, v143, v139, s[2:3]
	v_cndmask_b32_e64 v72, v72, v140, s[2:3]
	s_waitcnt lgkmcnt(1)
	v_add_f32_e32 v74, v76, v74
	s_waitcnt lgkmcnt(0)
	v_add_f32_e32 v72, v72, v77
	v_cndmask_b32_e64 v76, v73, v74, s[4:5]
	v_cndmask_b32_e64 v77, v75, v72, s[4:5]
	ds_bpermute_b32 v76, v92, v76
	ds_bpermute_b32 v77, v92, v77
	v_cndmask_b32_e64 v73, v74, v73, s[4:5]
	v_cndmask_b32_e64 v72, v72, v75, s[4:5]
	s_waitcnt lgkmcnt(1)
	v_add_f32_e32 v73, v73, v76
	s_waitcnt lgkmcnt(0)
	v_add_f32_e32 v72, v72, v77
	v_cndmask_b32_e64 v74, v73, v72, s[6:7]
	ds_bpermute_b32 v74, v91, v74
	v_cndmask_b32_e64 v72, v72, v73, s[6:7]
	s_waitcnt lgkmcnt(0)
	v_add_f32_e32 v72, v72, v74
	ds_bpermute_b32 v73, v90, v72
	s_waitcnt lgkmcnt(0)
	v_add_f32_e32 v72, v72, v73
	ds_bpermute_b32 v73, v89, v72
	s_waitcnt lgkmcnt(0)
	v_add_f32_e32 v72, v72, v73
	ds_bpermute_b32 v73, v88, v72
	s_and_saveexec_b64 s[10:11], s[8:9]
	s_cbranch_execz .LBB0_750
	s_lshl_b64 s[24:25], s[24:25], 5
	v_lshl_add_u64 v[74:75], v[42:43], 0, s[24:25]
	s_waitcnt lgkmcnt(0)
	v_add_f32_e32 v72, v72, v73
	global_store_dword v[74:75], v72, off
.LBB0_750:
	s_or_b64 exec, exec, s[10:11]
	s_waitcnt vmcnt(27)
	v_cvt_pk_f32_fp8_sdwa v[80:81], v120 src0_sel:WORD_1
	s_waitcnt vmcnt(26)
	v_cvt_pk_f32_fp8_sdwa v[86:87], v119 src0_sel:WORD_1
	v_cvt_pk_f32_fp8_e32 v[82:83], v120
	v_mul_f32_e32 v84, 0x3d000000, v104
	v_lshlrev_b32_e32 v72, 16, v70
	s_waitcnt lgkmcnt(0)
	v_and_b32_e32 v73, 0xffff0000, v70
	v_lshlrev_b32_e32 v70, 16, v71
	v_and_b32_e32 v71, 0xffff0000, v71
	v_pk_mul_f32 v[80:81], v[84:85], v[80:81] op_sel_hi:[0,1]
	v_cvt_pk_f32_fp8_e32 v[120:121], v119
	v_pk_fma_f32 v[70:71], v[2:3], v[80:81], v[70:71]
	v_pk_mul_f32 v[80:81], v[84:85], v[86:87] op_sel_hi:[0,1]
	s_waitcnt vmcnt(25)
	v_cvt_pk_f32_fp8_sdwa v[86:87], v118 src0_sel:WORD_1
	v_cvt_pk_f32_fp8_e32 v[118:119], v118
	v_pk_mul_f32 v[82:83], v[84:85], v[82:83] op_sel_hi:[0,1]
	v_lshlrev_b32_e32 v74, 16, v68
	v_and_b32_e32 v75, 0xffff0000, v68
	v_pk_fma_f32 v[72:73], v[0:1], v[82:83], v[72:73]
	v_pk_mul_f32 v[82:83], v[84:85], v[120:121] op_sel_hi:[0,1]
	v_lshlrev_b32_e32 v68, 16, v69
	v_and_b32_e32 v69, 0xffff0000, v69
	v_pk_fma_f32 v[74:75], v[12:13], v[82:83], v[74:75]
	v_pk_mul_f32 v[82:83], v[84:85], v[118:119] op_sel_hi:[0,1]
	s_waitcnt vmcnt(24)
	v_cvt_pk_f32_fp8_e32 v[118:119], v117
	v_pk_fma_f32 v[68:69], v[14:15], v[80:81], v[68:69]
	v_pk_mul_f32 v[80:81], v[84:85], v[86:87] op_sel_hi:[0,1]
	v_cvt_pk_f32_fp8_sdwa v[86:87], v117 src0_sel:WORD_1
	v_lshlrev_b32_e32 v76, 16, v66
	v_and_b32_e32 v77, 0xffff0000, v66
	v_lshlrev_b32_e32 v66, 16, v67
	v_and_b32_e32 v67, 0xffff0000, v67
	v_lshlrev_b32_e32 v78, 16, v64
	v_and_b32_e32 v79, 0xffff0000, v64
	v_pk_fma_f32 v[76:77], v[24:25], v[82:83], v[76:77]
	v_pk_mul_f32 v[82:83], v[84:85], v[118:119] op_sel_hi:[0,1]
	v_pk_fma_f32 v[66:67], v[26:27], v[80:81], v[66:67]
	v_pk_mul_f32 v[80:81], v[84:85], v[86:87] op_sel_hi:[0,1]
	v_pk_fma_f32 v[78:79], v[28:29], v[82:83], v[78:79]
	s_waitcnt vmcnt(23)
	v_cvt_pk_f32_fp8_e32 v[82:83], v116
	v_cvt_pk_f32_fp8_sdwa v[84:85], v116 src0_sel:WORD_1
	s_waitcnt vmcnt(22)
	v_cvt_pk_f32_fp8_e32 v[86:87], v115
	v_cvt_pk_f32_fp8_sdwa v[116:117], v115 src0_sel:WORD_1
	v_lshlrev_b32_e32 v64, 16, v65
	v_and_b32_e32 v65, 0xffff0000, v65
	v_pk_fma_f32 v[64:65], v[30:31], v[80:81], v[64:65]
	v_mul_f32_e32 v80, 0x3d000000, v103
	v_pk_mul_f32 v[82:83], v[80:81], v[82:83] op_sel_hi:[0,1]
	v_pk_mul_f32 v[84:85], v[80:81], v[84:85] op_sel_hi:[0,1]
	v_pk_fma_f32 v[70:71], v[2:3], v[84:85], v[70:71]
	v_pk_fma_f32 v[72:73], v[0:1], v[82:83], v[72:73]
	v_pk_mul_f32 v[82:83], v[80:81], v[86:87] op_sel_hi:[0,1]
	v_pk_mul_f32 v[84:85], v[80:81], v[116:117] op_sel_hi:[0,1]
	s_waitcnt vmcnt(21)
	v_cvt_pk_f32_fp8_e32 v[86:87], v113
	v_cvt_pk_f32_fp8_sdwa v[116:117], v113 src0_sel:WORD_1
	v_pk_fma_f32 v[68:69], v[14:15], v[84:85], v[68:69]
	v_pk_fma_f32 v[74:75], v[12:13], v[82:83], v[74:75]
	v_pk_mul_f32 v[82:83], v[80:81], v[86:87] op_sel_hi:[0,1]
	v_pk_mul_f32 v[84:85], v[80:81], v[116:117] op_sel_hi:[0,1]
	s_waitcnt vmcnt(20)
	v_cvt_pk_f32_fp8_e32 v[86:87], v111
	v_cvt_pk_f32_fp8_sdwa v[116:117], v111 src0_sel:WORD_1
	v_pk_fma_f32 v[76:77], v[24:25], v[82:83], v[76:77]
	v_pk_fma_f32 v[66:67], v[26:27], v[84:85], v[66:67]
	v_pk_mul_f32 v[82:83], v[80:81], v[86:87] op_sel_hi:[0,1]
	v_pk_mul_f32 v[80:81], v[80:81], v[116:117] op_sel_hi:[0,1]
	v_pk_fma_f32 v[64:65], v[30:31], v[80:81], v[64:65]
	s_waitcnt vmcnt(19)
	v_cvt_pk_f32_fp8_sdwa v[80:81], v114 src0_sel:WORD_1
	v_cvt_pk_f32_fp8_e32 v[84:85], v114
	v_pk_fma_f32 v[78:79], v[28:29], v[82:83], v[78:79]
	v_mul_f32_e32 v82, 0x3d000000, v102
	s_waitcnt vmcnt(18)
	v_cvt_pk_f32_fp8_sdwa v[86:87], v112 src0_sel:WORD_1
	v_cvt_pk_f32_fp8_e32 v[102:103], v112
	v_pk_mul_f32 v[80:81], v[82:83], v[80:81] op_sel_hi:[0,1]
	v_pk_mul_f32 v[84:85], v[82:83], v[84:85] op_sel_hi:[0,1]
	v_pk_fma_f32 v[72:73], v[0:1], v[84:85], v[72:73]
	v_pk_fma_f32 v[70:71], v[2:3], v[80:81], v[70:71]
	v_pk_mul_f32 v[80:81], v[82:83], v[86:87] op_sel_hi:[0,1]
	v_pk_mul_f32 v[84:85], v[82:83], v[102:103] op_sel_hi:[0,1]
	s_waitcnt vmcnt(17)
	v_cvt_pk_f32_fp8_sdwa v[86:87], v110 src0_sel:WORD_1
	v_cvt_pk_f32_fp8_e32 v[102:103], v110
	v_pk_fma_f32 v[74:75], v[12:13], v[84:85], v[74:75]
	v_pk_fma_f32 v[68:69], v[14:15], v[80:81], v[68:69]
	v_pk_mul_f32 v[80:81], v[82:83], v[86:87] op_sel_hi:[0,1]
	v_pk_mul_f32 v[84:85], v[82:83], v[102:103] op_sel_hi:[0,1]
	s_waitcnt vmcnt(16)
	v_cvt_pk_f32_fp8_sdwa v[86:87], v109 src0_sel:WORD_1
	v_cvt_pk_f32_fp8_e32 v[102:103], v109
	v_pk_fma_f32 v[66:67], v[26:27], v[80:81], v[66:67]
	v_pk_fma_f32 v[76:77], v[24:25], v[84:85], v[76:77]
	v_pk_mul_f32 v[80:81], v[82:83], v[86:87] op_sel_hi:[0,1]
	v_pk_mul_f32 v[82:83], v[82:83], v[102:103] op_sel_hi:[0,1]
	v_pk_fma_f32 v[78:79], v[28:29], v[82:83], v[78:79]
	s_waitcnt vmcnt(15)
	v_cvt_pk_f32_fp8_e32 v[82:83], v108
	v_cvt_pk_f32_fp8_sdwa v[84:85], v108 src0_sel:WORD_1
	s_waitcnt vmcnt(14)
	v_cvt_pk_f32_fp8_e32 v[86:87], v107
	v_cvt_pk_f32_fp8_sdwa v[102:103], v107 src0_sel:WORD_1
	v_pk_fma_f32 v[64:65], v[30:31], v[80:81], v[64:65]
	v_mul_f32_e32 v80, 0x3d000000, v101
	v_pk_mul_f32 v[82:83], v[80:81], v[82:83] op_sel_hi:[0,1]
	v_pk_mul_f32 v[84:85], v[80:81], v[84:85] op_sel_hi:[0,1]
	v_pk_fma_f32 v[70:71], v[2:3], v[84:85], v[70:71]
	v_pk_fma_f32 v[72:73], v[0:1], v[82:83], v[72:73]
	v_pk_mul_f32 v[82:83], v[80:81], v[86:87] op_sel_hi:[0,1]
	v_pk_mul_f32 v[84:85], v[80:81], v[102:103] op_sel_hi:[0,1]
	s_waitcnt vmcnt(13)
	v_cvt_pk_f32_fp8_e32 v[86:87], v106
	v_cvt_pk_f32_fp8_sdwa v[102:103], v106 src0_sel:WORD_1
	v_pk_fma_f32 v[68:69], v[14:15], v[84:85], v[68:69]
	v_pk_fma_f32 v[74:75], v[12:13], v[82:83], v[74:75]
	v_pk_mul_f32 v[82:83], v[80:81], v[86:87] op_sel_hi:[0,1]
	v_pk_mul_f32 v[84:85], v[80:81], v[102:103] op_sel_hi:[0,1]
	s_waitcnt vmcnt(12)
	v_cvt_pk_f32_fp8_e32 v[86:87], v105
	v_cvt_pk_f32_fp8_sdwa v[102:103], v105 src0_sel:WORD_1
	v_pk_fma_f32 v[76:77], v[24:25], v[82:83], v[76:77]
	v_pk_fma_f32 v[66:67], v[26:27], v[84:85], v[66:67]
	v_pk_mul_f32 v[82:83], v[80:81], v[86:87] op_sel_hi:[0,1]
	v_pk_mul_f32 v[80:81], v[80:81], v[102:103] op_sel_hi:[0,1]
	v_pk_fma_f32 v[64:65], v[30:31], v[80:81], v[64:65]
	v_and_b32_sdwa v80, v73, v99 dst_sel:DWORD dst_unused:UNUSED_PAD src0_sel:WORD_1 src1_sel:DWORD
	v_and_b32_sdwa v81, v72, v99 dst_sel:DWORD dst_unused:UNUSED_PAD src0_sel:WORD_1 src1_sel:DWORD
	v_add3_u32 v73, v73, v80, s46
	v_and_b32_sdwa v80, v71, v99 dst_sel:DWORD dst_unused:UNUSED_PAD src0_sel:WORD_1 src1_sel:DWORD
	v_pk_fma_f32 v[78:79], v[28:29], v[82:83], v[78:79]
	v_add3_u32 v82, v72, v81, s46
	v_and_b32_sdwa v81, v70, v99 dst_sel:DWORD dst_unused:UNUSED_PAD src0_sel:WORD_1 src1_sel:DWORD
	v_add3_u32 v71, v71, v80, s46
	v_and_b32_sdwa v80, v75, v99 dst_sel:DWORD dst_unused:UNUSED_PAD src0_sel:WORD_1 src1_sel:DWORD
	v_add3_u32 v83, v70, v81, s46
	v_and_b32_sdwa v81, v74, v99 dst_sel:DWORD dst_unused:UNUSED_PAD src0_sel:WORD_1 src1_sel:DWORD
	v_add3_u32 v75, v75, v80, s46
	v_and_b32_sdwa v80, v69, v99 dst_sel:DWORD dst_unused:UNUSED_PAD src0_sel:WORD_1 src1_sel:DWORD
	v_add3_u32 v84, v74, v81, s46
	v_and_b32_sdwa v81, v68, v99 dst_sel:DWORD dst_unused:UNUSED_PAD src0_sel:WORD_1 src1_sel:DWORD
	v_add3_u32 v69, v69, v80, s46
	v_and_b32_sdwa v80, v77, v99 dst_sel:DWORD dst_unused:UNUSED_PAD src0_sel:WORD_1 src1_sel:DWORD
	v_add3_u32 v85, v68, v81, s46
	v_and_b32_sdwa v81, v76, v99 dst_sel:DWORD dst_unused:UNUSED_PAD src0_sel:WORD_1 src1_sel:DWORD
	v_add3_u32 v77, v77, v80, s46
	v_and_b32_sdwa v80, v67, v99 dst_sel:DWORD dst_unused:UNUSED_PAD src0_sel:WORD_1 src1_sel:DWORD
	v_add3_u32 v86, v76, v81, s46
	v_and_b32_sdwa v81, v66, v99 dst_sel:DWORD dst_unused:UNUSED_PAD src0_sel:WORD_1 src1_sel:DWORD
	v_add3_u32 v67, v67, v80, s46
	v_and_b32_sdwa v80, v79, v99 dst_sel:DWORD dst_unused:UNUSED_PAD src0_sel:WORD_1 src1_sel:DWORD
	v_add3_u32 v87, v66, v81, s46
	v_and_b32_sdwa v81, v78, v99 dst_sel:DWORD dst_unused:UNUSED_PAD src0_sel:WORD_1 src1_sel:DWORD
	v_add3_u32 v79, v79, v80, s46
	v_and_b32_sdwa v80, v65, v99 dst_sel:DWORD dst_unused:UNUSED_PAD src0_sel:WORD_1 src1_sel:DWORD
	v_and_b32_e32 v73, 0xffff0000, v73
	v_and_b32_e32 v72, 0xffff0000, v82
	v_add3_u32 v101, v78, v81, s46
	v_and_b32_sdwa v81, v64, v99 dst_sel:DWORD dst_unused:UNUSED_PAD src0_sel:WORD_1 src1_sel:DWORD
	v_add3_u32 v65, v65, v80, s46
	v_and_b32_e32 v71, 0xffff0000, v71
	v_and_b32_e32 v70, 0xffff0000, v83
	v_add3_u32 v102, v64, v81, s46
	v_and_b32_e32 v81, 0xffff0000, v65
	v_pk_fma_f32 v[64:65], v[72:73], v[72:73], 0 op_sel_hi:[1,1,0]
	v_and_b32_e32 v75, 0xffff0000, v75
	v_and_b32_e32 v74, 0xffff0000, v84
	v_pk_fma_f32 v[64:65], v[70:71], v[70:71], v[64:65]
	v_and_b32_e32 v69, 0xffff0000, v69
	v_and_b32_e32 v68, 0xffff0000, v85
	v_pk_fma_f32 v[64:65], v[74:75], v[74:75], v[64:65]
	v_and_b32_e32 v77, 0xffff0000, v77
	v_and_b32_e32 v76, 0xffff0000, v86
	v_pk_fma_f32 v[64:65], v[68:69], v[68:69], v[64:65]
	v_and_b32_e32 v67, 0xffff0000, v67
	v_and_b32_e32 v66, 0xffff0000, v87
	v_pk_fma_f32 v[64:65], v[76:77], v[76:77], v[64:65]
	v_and_b32_e32 v79, 0xffff0000, v79
	v_and_b32_e32 v78, 0xffff0000, v101
	v_pk_fma_f32 v[64:65], v[66:67], v[66:67], v[64:65]
	v_and_b32_e32 v80, 0xffff0000, v102
	v_pk_fma_f32 v[64:65], v[78:79], v[78:79], v[64:65]
	s_lshl_b64 s[24:25], s[20:21], 10
	v_pk_fma_f32 v[64:65], v[80:81], v[80:81], v[64:65]
	s_nop 0
	v_add_f32_e32 v64, v64, v65
	s_waitcnt lgkmcnt(0)
	s_nop 1
	v_add_f32_dpp v64, v64, v64 quad_perm:[1,0,3,2] row_mask:0xf bank_mask:0xf
	s_waitcnt lgkmcnt(0)
	s_nop 1
	v_add_f32_dpp v64, v64, v64 quad_perm:[2,3,0,1] row_mask:0xf bank_mask:0xf
	s_waitcnt lgkmcnt(0)
	s_nop 1
	v_add_f32_dpp v64, v64, v64 row_half_mirror row_mask:0xf bank_mask:0xf
	s_waitcnt lgkmcnt(0)
	s_nop 1
	v_add_f32_dpp v103, v64, v64 row_mirror row_mask:0xf bank_mask:0xf
	v_or_b32_sdwa v64, v73, v82 dst_sel:DWORD dst_unused:UNUSED_PAD src0_sel:DWORD src1_sel:WORD_1
	v_or_b32_sdwa v65, v71, v83 dst_sel:DWORD dst_unused:UNUSED_PAD src0_sel:DWORD src1_sel:WORD_1
	global_store_dwordx2 v[62:63], v[64:65], off
	v_or_b32_sdwa v64, v75, v84 dst_sel:DWORD dst_unused:UNUSED_PAD src0_sel:DWORD src1_sel:WORD_1
	s_waitcnt lgkmcnt(0)
	v_mov_b32_e32 v82, v103
	v_mov_b32_e32 v104, v103
	s_nop 1
	v_permlane16_swap_b32_e32 v82, v104
	v_add_f32_e32 v82, v82, v104
	v_or_b32_sdwa v65, v69, v85 dst_sel:DWORD dst_unused:UNUSED_PAD src0_sel:DWORD src1_sel:WORD_1
	global_store_dwordx2 v[62:63], v[64:65], off offset:512
	s_waitcnt lgkmcnt(0)
	v_mov_b32_e32 v64, v82
	v_mov_b32_e32 v83, v82
	s_nop 1
	v_permlane32_swap_b32_e32 v64, v83
	v_add_f32_e32 v64, v64, v83
	v_fmamk_f32 v64, v64, 0x3a800000, v96
	v_mul_f32_e32 v65, 0x4f800000, v64
	v_cmp_gt_f32_e32 vcc, s47, v64
	s_nop 1
	v_cndmask_b32_e32 v82, v64, v65, vcc
	v_sqrt_f32_e32 v83, v82
	v_or_b32_sdwa v64, v77, v86 dst_sel:DWORD dst_unused:UNUSED_PAD src0_sel:DWORD src1_sel:WORD_1
	v_or_b32_sdwa v65, v67, v87 dst_sel:DWORD dst_unused:UNUSED_PAD src0_sel:DWORD src1_sel:WORD_1
	global_store_dwordx2 v[62:63], v[64:65], off offset:1024
	v_add_u32_e32 v64, -1, v83
	v_fma_f32 v65, -v64, v83, v82
	v_cmp_ge_f32_e64 s[10:11], 0, v65
	v_add_u32_e32 v65, 1, v83
	v_mov_b32_e32 v86, 0
	v_cndmask_b32_e64 v64, v83, v64, s[10:11]
	v_fma_f32 v83, -v65, v83, v82
	v_cmp_lt_f32_e64 s[10:11], 0, v83
	s_nop 1
	v_cndmask_b32_e64 v64, v64, v65, s[10:11]
	v_mul_f32_e32 v65, 0x37800000, v64
	v_cndmask_b32_e32 v64, v64, v65, vcc
	v_cmp_class_f32_e32 vcc, v82, v97
	v_or_b32_sdwa v65, v81, v102 dst_sel:DWORD dst_unused:UNUSED_PAD src0_sel:DWORD src1_sel:WORD_1
	s_nop 0
	v_cndmask_b32_e32 v82, v64, v82, vcc
	v_div_scale_f32 v83, s[10:11], v82, v82, 1.0
	v_rcp_f32_e32 v84, v83
	v_or_b32_sdwa v64, v79, v101 dst_sel:DWORD dst_unused:UNUSED_PAD src0_sel:DWORD src1_sel:WORD_1
	global_store_dwordx2 v[62:63], v[64:65], off offset:1536
	v_fma_f32 v62, -v83, v84, 1.0
	v_fmac_f32_e32 v84, v62, v84
	v_div_scale_f32 v62, vcc, 1.0, v82, 1.0
	v_mul_f32_e32 v63, v62, v84
	v_fma_f32 v64, -v83, v63, v62
	v_fmac_f32_e32 v63, v64, v84
	v_fma_f32 v62, -v83, v63, v62
	v_div_fmas_f32 v62, v62, v84, v63
	v_div_fixup_f32 v82, v62, v82, 1.0
	v_pk_mul_f32 v[64:65], v[82:83], v[72:73] op_sel_hi:[0,1]
	v_pk_mul_f32 v[62:63], v[82:83], v[70:71] op_sel_hi:[0,1]
	v_pk_fma_f32 v[70:71], v[48:49], v[64:65], v[4:5]
	v_pk_mul_f32 v[64:65], v[82:83], v[68:69] op_sel_hi:[0,1]
	v_pk_mul_f32 v[68:69], v[82:83], v[76:77] op_sel_hi:[0,1]
	v_pk_mul_f32 v[72:73], v[82:83], v[74:75] op_sel_hi:[0,1]
	v_pk_fma_f32 v[74:75], v[56:57], v[68:69], v[16:17]
	v_pk_mul_f32 v[68:69], v[82:83], v[80:81] op_sel_hi:[0,1]
	v_bfe_u32 v80, v70, 16, 1
	v_add3_u32 v80, v70, v80, s46
	v_bfe_u32 v81, v71, 16, 1
	v_pk_fma_f32 v[62:63], v[46:47], v[62:63], v[6:7]
	v_lshrrev_b32_e32 v80, 16, v80
	v_add3_u32 v81, v71, v81, s46
	v_and_or_b32 v80, v81, s44, v80
	v_bfe_u32 v81, v62, 16, 1
	v_pk_mul_f32 v[66:67], v[82:83], v[66:67] op_sel_hi:[0,1]
	v_pk_mul_f32 v[76:77], v[82:83], v[78:79] op_sel_hi:[0,1]
	v_add3_u32 v81, v62, v81, s46
	v_bfe_u32 v82, v63, 16, 1
	v_lshrrev_b32_e32 v81, 16, v81
	v_add3_u32 v82, v63, v82, s46
	v_pk_fma_f32 v[72:73], v[52:53], v[72:73], v[8:9]
	v_lshl_add_u64 v[78:79], v[38:39], 0, s[22:23]
	v_and_or_b32 v81, v82, s44, v81
	global_store_dwordx2 v[78:79], v[80:81], off
	v_bfe_u32 v80, v72, 16, 1
	v_add3_u32 v80, v72, v80, s46
	v_bfe_u32 v81, v73, 16, 1
	v_pk_fma_f32 v[64:65], v[50:51], v[64:65], v[10:11]
	v_lshrrev_b32_e32 v80, 16, v80
	v_add3_u32 v81, v73, v81, s46
	v_and_or_b32 v80, v81, s44, v80
	v_bfe_u32 v81, v64, 16, 1
	v_add3_u32 v81, v64, v81, s46
	v_bfe_u32 v82, v65, 16, 1
	v_lshrrev_b32_e32 v81, 16, v81
	v_add3_u32 v82, v65, v82, s46
	v_and_or_b32 v81, v82, s44, v81
	global_store_dwordx2 v[78:79], v[80:81], off offset:512
	v_bfe_u32 v80, v74, 16, 1
	v_add3_u32 v80, v74, v80, s46
	v_bfe_u32 v81, v75, 16, 1
	v_pk_fma_f32 v[66:67], v[54:55], v[66:67], v[18:19]
	v_lshrrev_b32_e32 v80, 16, v80
	v_add3_u32 v81, v75, v81, s46
	v_and_or_b32 v80, v81, s44, v80
	v_bfe_u32 v81, v66, 16, 1
	v_add3_u32 v81, v66, v81, s46
	v_bfe_u32 v82, v67, 16, 1
	v_lshrrev_b32_e32 v81, 16, v81
	v_add3_u32 v82, v67, v82, s46
	v_pk_fma_f32 v[76:77], v[60:61], v[76:77], v[20:21]
	v_and_or_b32 v81, v82, s44, v81
	global_store_dwordx2 v[78:79], v[80:81], off offset:1024
	v_bfe_u32 v80, v76, 16, 1
	v_add3_u32 v80, v76, v80, s46
	v_bfe_u32 v81, v77, 16, 1
	v_pk_fma_f32 v[68:69], v[58:59], v[68:69], v[22:23]
	v_lshrrev_b32_e32 v80, 16, v80
	v_add3_u32 v81, v77, v81, s46
	v_mul_f32_e32 v83, 0x41000000, v70
	v_mul_f32_e32 v84, 0x41000000, v71
	v_and_or_b32 v80, v81, s44, v80
	v_bfe_u32 v81, v68, 16, 1
	v_med3_f32 v83, v83, s48, v100
	v_med3_f32 v84, v84, s48, v100
	v_add3_u32 v81, v68, v81, s46
	v_bfe_u32 v82, v69, 16, 1
	v_cvt_pk_fp8_f32 v86, v83, v84
	v_lshrrev_b32_e32 v81, 16, v81
	v_add3_u32 v82, v69, v82, s46
	v_mul_f32_e32 v85, 0x41000000, v62
	v_mul_f32_e32 v83, 0x41000000, v63
	v_and_or_b32 v81, v82, s44, v81
	v_med3_f32 v84, v85, s48, v100
	v_med3_f32 v83, v83, s48, v100
	global_store_dwordx2 v[78:79], v[80:81], off offset:1536
	v_mul_f32_e32 v78, 0x41000000, v72
	v_mul_f32_e32 v79, 0x41000000, v73
	v_cvt_pk_fp8_f32 v86, v84, v83 op_sel:[0,0,1]
	v_med3_f32 v78, v78, s48, v100
	v_med3_f32 v79, v79, s48, v100
	v_mov_b32_e32 v84, 0
	v_cvt_pk_fp8_f32 v84, v78, v79
	v_mul_f32_e32 v80, 0x41000000, v64
	v_mul_f32_e32 v78, 0x41000000, v65
	v_med3_f32 v79, v80, s48, v100
	v_med3_f32 v78, v78, s48, v100
	v_cvt_pk_fp8_f32 v84, v79, v78 op_sel:[0,0,1]
	v_mul_f32_e32 v78, 0x41000000, v74
	v_mul_f32_e32 v79, 0x41000000, v75
	v_med3_f32 v78, v78, s48, v100
	v_med3_f32 v79, v79, s48, v100
	v_mov_b32_e32 v85, 0
	v_cvt_pk_fp8_f32 v85, v78, v79
	v_mul_f32_e32 v80, 0x41000000, v66
	v_mul_f32_e32 v78, 0x41000000, v67
	v_med3_f32 v79, v80, s48, v100
	v_med3_f32 v78, v78, s48, v100
	v_lshl_add_u64 v[82:83], v[40:41], 0, s[24:25]
	v_cvt_pk_fp8_f32 v85, v79, v78 op_sel:[0,0,1]
	v_mul_f32_e32 v78, 0x41000000, v76
	v_mul_f32_e32 v79, 0x41000000, v77
	global_store_dword v[82:83], v86, off
	v_med3_f32 v78, v78, s48, v100
	v_med3_f32 v79, v79, s48, v100
	v_mov_b32_e32 v86, 0
	v_cvt_pk_fp8_f32 v86, v78, v79
	v_mul_f32_e32 v80, 0x41000000, v68
	v_mul_f32_e32 v78, 0x41000000, v69
	v_med3_f32 v79, v80, s48, v100
	v_med3_f32 v78, v78, s48, v100
	v_cvt_pk_fp8_f32 v86, v79, v78 op_sel:[0,0,1]
	ds_read_b128 v[78:81], v94
	global_store_dword v[82:83], v84, off offset:256
	global_store_dword v[82:83], v85, off offset:512
	global_store_dword v[82:83], v86, off offset:768
	ds_read_b128 v[82:85], v94 offset:1024
	ds_read_b128 v[102:105], v94 offset:2048
	s_waitcnt lgkmcnt(2)
	v_pk_fma_f32 v[78:79], v[70:71], v[78:79], 0 op_sel_hi:[1,1,0]
	s_nop 0
	v_pk_fma_f32 v[86:87], v[62:63], v[80:81], v[78:79]
	ds_read_b128 v[78:81], v94 offset:3072
	s_waitcnt lgkmcnt(2)
	v_pk_fma_f32 v[82:83], v[72:73], v[82:83], v[86:87]
	s_nop 0
	v_pk_fma_f32 v[82:83], v[64:65], v[84:85], v[82:83]
	s_waitcnt lgkmcnt(1)
	v_pk_fma_f32 v[82:83], v[74:75], v[102:103], v[82:83]
	s_nop 0
	v_pk_fma_f32 v[82:83], v[66:67], v[104:105], v[82:83]
	s_waitcnt lgkmcnt(0)
	v_pk_fma_f32 v[78:79], v[76:77], v[78:79], v[82:83]
	ds_read_b128 v[82:85], v94 offset:5120
	ds_read_b128 v[102:105], v94 offset:4096
	v_pk_fma_f32 v[78:79], v[68:69], v[80:81], v[78:79]
	s_waitcnt lgkmcnt(0)
	v_pk_fma_f32 v[86:87], v[70:71], v[102:103], 0 op_sel_hi:[1,1,0]
	v_add_f32_e32 v101, v78, v79
	ds_read_b128 v[78:81], v94 offset:7168
	ds_read_b128 v[106:109], v94 offset:6144
	v_pk_fma_f32 v[86:87], v[62:63], v[104:105], v[86:87]
	s_nop 0
	v_pk_fma_f32 v[82:83], v[72:73], v[82:83], v[86:87]
	s_nop 0
	v_pk_fma_f32 v[82:83], v[64:65], v[84:85], v[82:83]
	s_waitcnt lgkmcnt(0)
	v_pk_fma_f32 v[82:83], v[74:75], v[106:107], v[82:83]
	s_nop 0
	v_pk_fma_f32 v[82:83], v[66:67], v[108:109], v[82:83]
	s_nop 0
	v_pk_fma_f32 v[78:79], v[76:77], v[78:79], v[82:83]
	s_nop 0
	v_pk_fma_f32 v[78:79], v[68:69], v[80:81], v[78:79]
	s_nop 0
	v_add_f32_e32 v110, v78, v79
	ds_read_b128 v[78:81], v94 offset:8192
	ds_read_b128 v[82:85], v94 offset:9216
	ds_read_b128 v[102:105], v94 offset:10240
	ds_read_b128 v[106:109], v94 offset:11264
	s_waitcnt lgkmcnt(3)
	v_pk_fma_f32 v[78:79], v[70:71], v[78:79], 0 op_sel_hi:[1,1,0]
	s_nop 0
	v_pk_fma_f32 v[78:79], v[62:63], v[80:81], v[78:79]
	s_waitcnt lgkmcnt(2)
	v_pk_fma_f32 v[78:79], v[72:73], v[82:83], v[78:79]
	s_nop 0
	v_pk_fma_f32 v[78:79], v[64:65], v[84:85], v[78:79]
	s_waitcnt lgkmcnt(1)
	v_pk_fma_f32 v[78:79], v[74:75], v[102:103], v[78:79]
	s_nop 0
	v_pk_fma_f32 v[78:79], v[66:67], v[104:105], v[78:79]
	s_waitcnt lgkmcnt(0)
	v_pk_fma_f32 v[86:87], v[76:77], v[106:107], v[78:79]
	ds_read_b128 v[78:81], v94 offset:13312
	ds_read_b128 v[82:85], v94 offset:12288
	v_pk_fma_f32 v[86:87], v[68:69], v[108:109], v[86:87]
	ds_read_b128 v[102:105], v94 offset:15360
	ds_read_b128 v[106:109], v94 offset:14336
	v_add_f32_e32 v111, v86, v87
	s_waitcnt lgkmcnt(2)
	v_pk_fma_f32 v[82:83], v[70:71], v[82:83], 0 op_sel_hi:[1,1,0]
	s_nop 0
	v_pk_fma_f32 v[82:83], v[62:63], v[84:85], v[82:83]
	s_nop 0
	v_pk_fma_f32 v[78:79], v[72:73], v[78:79], v[82:83]
	s_nop 0
	v_pk_fma_f32 v[78:79], v[64:65], v[80:81], v[78:79]
	s_waitcnt lgkmcnt(0)
	v_pk_fma_f32 v[78:79], v[74:75], v[106:107], v[78:79]
	s_nop 0
	v_pk_fma_f32 v[78:79], v[66:67], v[108:109], v[78:79]
	s_nop 0
	v_pk_fma_f32 v[78:79], v[76:77], v[102:103], v[78:79]
	s_nop 0
	v_pk_fma_f32 v[78:79], v[68:69], v[104:105], v[78:79]
	s_nop 0
	v_add_f32_e32 v112, v78, v79
	ds_read_b128 v[78:81], v94 offset:16384
	ds_read_b128 v[82:85], v94 offset:17408
	ds_read_b128 v[102:105], v94 offset:18432
	ds_read_b128 v[106:109], v94 offset:19456
	s_waitcnt lgkmcnt(3)
	v_pk_fma_f32 v[78:79], v[70:71], v[78:79], 0 op_sel_hi:[1,1,0]
	s_nop 0
	v_pk_fma_f32 v[78:79], v[62:63], v[80:81], v[78:79]
	s_waitcnt lgkmcnt(2)
	v_pk_fma_f32 v[78:79], v[72:73], v[82:83], v[78:79]
	s_nop 0
	v_pk_fma_f32 v[78:79], v[64:65], v[84:85], v[78:79]
	s_waitcnt lgkmcnt(1)
	v_pk_fma_f32 v[78:79], v[74:75], v[102:103], v[78:79]
	s_nop 0
	v_pk_fma_f32 v[78:79], v[66:67], v[104:105], v[78:79]
	s_waitcnt lgkmcnt(0)
	v_pk_fma_f32 v[86:87], v[76:77], v[106:107], v[78:79]
	ds_read_b128 v[78:81], v94 offset:21504
	ds_read_b128 v[82:85], v94 offset:20480
	v_pk_fma_f32 v[86:87], v[68:69], v[108:109], v[86:87]
	ds_read_b128 v[102:105], v94 offset:23552
	ds_read_b128 v[106:109], v94 offset:22528
	v_add_f32_e32 v113, v86, v87
	s_waitcnt lgkmcnt(2)
	v_pk_fma_f32 v[82:83], v[70:71], v[82:83], 0 op_sel_hi:[1,1,0]
	s_nop 0
	v_pk_fma_f32 v[82:83], v[62:63], v[84:85], v[82:83]
	s_nop 0
	v_pk_fma_f32 v[78:79], v[72:73], v[78:79], v[82:83]
	s_nop 0
	v_pk_fma_f32 v[78:79], v[64:65], v[80:81], v[78:79]
	s_waitcnt lgkmcnt(0)
	v_pk_fma_f32 v[78:79], v[74:75], v[106:107], v[78:79]
	s_nop 0
	v_pk_fma_f32 v[78:79], v[66:67], v[108:109], v[78:79]
	s_nop 0
	v_pk_fma_f32 v[78:79], v[76:77], v[102:103], v[78:79]
	s_nop 0
	v_pk_fma_f32 v[78:79], v[68:69], v[104:105], v[78:79]
	s_nop 0
	v_add_f32_e32 v114, v78, v79
	ds_read_b128 v[78:81], v94 offset:24576
	ds_read_b128 v[82:85], v94 offset:25600
	ds_read_b128 v[102:105], v94 offset:26624
	ds_read_b128 v[106:109], v94 offset:27648
	s_waitcnt lgkmcnt(3)
	v_pk_fma_f32 v[78:79], v[70:71], v[78:79], 0 op_sel_hi:[1,1,0]
	s_nop 0
	v_pk_fma_f32 v[78:79], v[62:63], v[80:81], v[78:79]
	s_waitcnt lgkmcnt(2)
	v_pk_fma_f32 v[78:79], v[72:73], v[82:83], v[78:79]
	s_nop 0
	v_pk_fma_f32 v[78:79], v[64:65], v[84:85], v[78:79]
	s_waitcnt lgkmcnt(1)
	v_pk_fma_f32 v[78:79], v[74:75], v[102:103], v[78:79]
	s_nop 0
	v_pk_fma_f32 v[78:79], v[66:67], v[104:105], v[78:79]
	s_waitcnt lgkmcnt(0)
	v_pk_fma_f32 v[86:87], v[76:77], v[106:107], v[78:79]
	ds_read_b128 v[78:81], v94 offset:29696
	ds_read_b128 v[82:85], v94 offset:28672
	v_pk_fma_f32 v[86:87], v[68:69], v[108:109], v[86:87]
	ds_read_b128 v[102:105], v94 offset:31744
	ds_read_b128 v[106:109], v94 offset:30720
	v_add_f32_e32 v86, v86, v87
	s_waitcnt lgkmcnt(2)
	v_pk_fma_f32 v[70:71], v[70:71], v[82:83], 0 op_sel_hi:[1,1,0]
	s_nop 0
	v_pk_fma_f32 v[62:63], v[62:63], v[84:85], v[70:71]
	s_nop 0
	v_pk_fma_f32 v[62:63], v[72:73], v[78:79], v[62:63]
	s_nop 0
	v_pk_fma_f32 v[62:63], v[64:65], v[80:81], v[62:63]
	s_waitcnt lgkmcnt(0)
	v_pk_fma_f32 v[62:63], v[74:75], v[106:107], v[62:63]
	s_nop 0
	v_pk_fma_f32 v[62:63], v[66:67], v[108:109], v[62:63]
	s_nop 0
	v_pk_fma_f32 v[62:63], v[76:77], v[102:103], v[62:63]
	s_nop 0
	v_pk_fma_f32 v[62:63], v[68:69], v[104:105], v[62:63]
	s_nop 0
	v_add_f32_e32 v62, v62, v63
	v_cndmask_b32_e64 v63, v101, v113, s[2:3]
	ds_bpermute_b32 v63, v93, v63
	v_cndmask_b32_e64 v64, v113, v101, s[2:3]
	v_cndmask_b32_e64 v65, v110, v114, s[2:3]
	ds_bpermute_b32 v65, v93, v65
	v_cndmask_b32_e64 v67, v112, v62, s[2:3]
	s_waitcnt lgkmcnt(1)
	v_add_f32_e32 v63, v64, v63
	v_cndmask_b32_e64 v64, v111, v86, s[2:3]
	ds_bpermute_b32 v64, v93, v64
	ds_bpermute_b32 v67, v93, v67
	v_cndmask_b32_e64 v66, v114, v110, s[2:3]
	s_waitcnt lgkmcnt(2)
	v_add_f32_e32 v65, v66, v65
	v_cndmask_b32_e64 v66, v86, v111, s[2:3]
	v_cndmask_b32_e64 v62, v62, v112, s[2:3]
	s_waitcnt lgkmcnt(1)
	v_add_f32_e32 v64, v66, v64
	s_waitcnt lgkmcnt(0)
	v_add_f32_e32 v62, v62, v67
	v_cndmask_b32_e64 v66, v63, v64, s[4:5]
	v_cndmask_b32_e64 v67, v65, v62, s[4:5]
	ds_bpermute_b32 v66, v92, v66
	ds_bpermute_b32 v67, v92, v67
	v_cndmask_b32_e64 v63, v64, v63, s[4:5]
	v_cndmask_b32_e64 v62, v62, v65, s[4:5]
	s_waitcnt lgkmcnt(1)
	v_add_f32_e32 v63, v63, v66
	s_waitcnt lgkmcnt(0)
	v_add_f32_e32 v62, v62, v67
	v_cndmask_b32_e64 v64, v63, v62, s[6:7]
	ds_bpermute_b32 v64, v91, v64
	v_cndmask_b32_e64 v62, v62, v63, s[6:7]
	s_waitcnt lgkmcnt(0)
	v_add_f32_e32 v62, v62, v64
	ds_bpermute_b32 v63, v90, v62
	s_waitcnt lgkmcnt(0)
	v_add_f32_e32 v62, v62, v63
	ds_bpermute_b32 v63, v89, v62
	s_waitcnt lgkmcnt(0)
	v_add_f32_e32 v62, v62, v63
	ds_bpermute_b32 v63, v88, v62
	s_and_saveexec_b64 s[10:11], s[8:9]
	s_cbranch_execz .LBB0_747
	s_lshl_b64 s[20:21], s[20:21], 5
	v_lshl_add_u64 v[64:65], v[42:43], 0, s[20:21]
	s_waitcnt lgkmcnt(0)
	v_add_f32_e32 v62, v62, v63
	global_store_dword v[64:65], v62, off
	s_branch .LBB0_747

.LBB0_1099:
	v_lshl_add_u64 v[8:9], s[44:45], 0, v[6:7]
	v_add_co_u32_e32 v8, vcc, 0x22c00000, v8
	v_lshl_add_u64 v[10:11], s[44:45], 0, v[4:5]
	s_nop 0
	v_addc_co_u32_e32 v9, vcc, 0, v9, vcc
	global_load_dwordx2 v[24:25], v[8:9], off
	global_load_dwordx2 v[26:27], v[8:9], off offset:512
	global_load_dwordx2 v[28:29], v[8:9], off offset:1024
	global_load_dwordx2 v[30:31], v[8:9], off offset:1536
	v_add_co_u32_e64 v10, s[2:3], s17, v10
	v_mov_b32_e32 v22, 0
	s_nop 0
	v_addc_co_u32_e64 v11, s[2:3], 0, v11, s[2:3]
	v_mov_b32_e32 v23, 0
	v_mov_b32_e32 v54, 0
	v_mov_b32_e32 v55, 0
	s_add_i32 s16, s16, s18
	v_lshl_add_u64 v[4:5], v[4:5], 0, s[20:21]
	v_lshl_add_u64 v[6:7], v[6:7], 0, s[22:23]
	s_cmp_lt_i32 s16, 0x8000
	s_waitcnt vmcnt(3)
	v_lshlrev_b32_e32 v9, 16, v25
	v_lshlrev_b32_e32 v8, 16, v24
	v_and_b32_e32 v25, 0xffff0000, v25
	v_and_b32_e32 v24, 0xffff0000, v24
	s_waitcnt vmcnt(2)
	v_lshlrev_b32_e32 v33, 16, v27
	v_lshlrev_b32_e32 v32, 16, v26
	v_and_b32_e32 v27, 0xffff0000, v27
	v_and_b32_e32 v26, 0xffff0000, v26
	s_waitcnt vmcnt(1)
	v_lshlrev_b32_e32 v35, 16, v29
	v_lshlrev_b32_e32 v34, 16, v28
	v_and_b32_e32 v29, 0xffff0000, v29
	v_and_b32_e32 v28, 0xffff0000, v28
	v_pk_mul_f32 v[38:39], v[24:25], v[24:25]
	s_waitcnt vmcnt(0)
	v_lshlrev_b32_e32 v37, 16, v31
	v_lshlrev_b32_e32 v36, 16, v30
	v_and_b32_e32 v31, 0xffff0000, v31
	v_and_b32_e32 v30, 0xffff0000, v30
	v_mov_b32_e32 v40, v8
	v_mov_b32_e32 v41, v24
	v_mov_b32_e32 v24, v9
	v_pk_mul_f32 v[42:43], v[26:27], v[26:27]
	v_pk_mul_f32 v[46:47], v[28:29], v[28:29]
	v_pk_fma_f32 v[8:9], v[8:9], v[8:9], v[38:39]
	v_mov_b32_e32 v44, v32
	v_mov_b32_e32 v45, v26
	v_mov_b32_e32 v26, v33
	v_mov_b32_e32 v48, v34
	v_mov_b32_e32 v49, v28
	v_mov_b32_e32 v28, v35
	v_pk_mul_f32 v[50:51], v[30:31], v[30:31]
	v_pk_fma_f32 v[32:33], v[32:33], v[32:33], v[42:43]
	v_pk_fma_f32 v[34:35], v[34:35], v[34:35], v[46:47]
	v_add_f32_e32 v8, v8, v9
	v_mov_b32_e32 v52, v36
	v_mov_b32_e32 v53, v30
	v_mov_b32_e32 v30, v37
	v_pk_fma_f32 v[36:37], v[36:37], v[36:37], v[50:51]
	v_add_f32_e32 v9, v32, v33
	v_add_f32_e32 v32, v34, v35
	v_add_f32_e32 v33, v36, v37
	s_waitcnt lgkmcnt(0)
	s_nop 1
	v_add_f32_dpp v8, v8, v8 quad_perm:[1,0,3,2] row_mask:0xf bank_mask:0xf
	s_waitcnt lgkmcnt(0)
	s_nop 1
	v_add_f32_dpp v9, v9, v9 quad_perm:[1,0,3,2] row_mask:0xf bank_mask:0xf
	s_waitcnt lgkmcnt(0)
	s_nop 1
	v_add_f32_dpp v32, v32, v32 quad_perm:[1,0,3,2] row_mask:0xf bank_mask:0xf
	s_waitcnt lgkmcnt(0)
	s_nop 1
	v_add_f32_dpp v33, v33, v33 quad_perm:[1,0,3,2] row_mask:0xf bank_mask:0xf
	s_waitcnt lgkmcnt(0)
	s_nop 1
	v_add_f32_dpp v8, v8, v8 quad_perm:[2,3,0,1] row_mask:0xf bank_mask:0xf
	s_waitcnt lgkmcnt(0)
	s_nop 1
	v_add_f32_dpp v9, v9, v9 quad_perm:[2,3,0,1] row_mask:0xf bank_mask:0xf
	s_waitcnt lgkmcnt(0)
	s_nop 1
	v_add_f32_dpp v32, v32, v32 quad_perm:[2,3,0,1] row_mask:0xf bank_mask:0xf
	s_waitcnt lgkmcnt(0)
	s_nop 1
	v_add_f32_dpp v33, v33, v33 quad_perm:[2,3,0,1] row_mask:0xf bank_mask:0xf
	s_waitcnt lgkmcnt(0)
	s_nop 1
	v_add_f32_dpp v8, v8, v8 row_half_mirror row_mask:0xf bank_mask:0xf
	s_waitcnt lgkmcnt(0)
	s_nop 1
	v_add_f32_dpp v9, v9, v9 row_half_mirror row_mask:0xf bank_mask:0xf
	s_waitcnt lgkmcnt(0)
	s_nop 1
	v_add_f32_dpp v32, v32, v32 row_half_mirror row_mask:0xf bank_mask:0xf
	s_waitcnt lgkmcnt(0)
	s_nop 1
	v_add_f32_dpp v33, v33, v33 row_half_mirror row_mask:0xf bank_mask:0xf
	s_waitcnt lgkmcnt(0)
	s_nop 1
	v_add_f32_dpp v8, v8, v8 row_mirror row_mask:0xf bank_mask:0xf
	s_waitcnt lgkmcnt(0)
	s_nop 1
	v_add_f32_dpp v9, v9, v9 row_mirror row_mask:0xf bank_mask:0xf
	s_waitcnt lgkmcnt(0)
	s_nop 1
	v_add_f32_dpp v32, v32, v32 row_mirror row_mask:0xf bank_mask:0xf
	s_waitcnt lgkmcnt(0)
	s_nop 1
	v_add_f32_dpp v33, v33, v33 row_mirror row_mask:0xf bank_mask:0xf
	s_waitcnt lgkmcnt(0)
	v_mov_b32_e32 v34, v8
	s_nop 1
	v_permlane16_swap_b32_e32 v8, v34
	v_add_f32_e32 v8, v8, v34
	s_waitcnt lgkmcnt(0)
	v_mov_b32_e32 v35, v9
	s_nop 1
	v_permlane16_swap_b32_e32 v9, v35
	v_add_f32_e32 v9, v9, v35
	s_waitcnt lgkmcnt(0)
	v_mov_b32_e32 v36, v32
	s_nop 1
	v_permlane16_swap_b32_e32 v32, v36
	v_add_f32_e32 v32, v32, v36
	s_waitcnt lgkmcnt(0)
	v_mov_b32_e32 v37, v33
	s_nop 1
	v_permlane16_swap_b32_e32 v33, v37
	v_add_f32_e32 v33, v33, v37
	s_waitcnt lgkmcnt(0)
	v_mov_b32_e32 v34, v8
	s_nop 1
	v_permlane32_swap_b32_e32 v8, v34
	v_add_f32_e32 v8, v8, v34
	v_fmamk_f32 v8, v8, 0x3b800000, v19
	s_waitcnt lgkmcnt(0)
	v_mov_b32_e32 v35, v9
	s_nop 1
	v_permlane32_swap_b32_e32 v9, v35
	v_add_f32_e32 v9, v9, v35
	s_waitcnt lgkmcnt(0)
	v_mov_b32_e32 v36, v32
	s_nop 1
	v_permlane32_swap_b32_e32 v32, v36
	v_add_f32_e32 v32, v32, v36
	s_waitcnt lgkmcnt(0)
	v_mov_b32_e32 v37, v33
	s_nop 1
	v_permlane32_swap_b32_e32 v33, v37
	v_add_f32_e32 v33, v33, v37
	v_fmamk_f32 v9, v9, 0x3b800000, v19
	v_fmamk_f32 v32, v32, 0x3b800000, v19
	v_mul_f32_e32 v34, 0x4f800000, v8
	v_cmp_gt_f32_e64 s[6:7], s0, v8
	v_fmamk_f32 v33, v33, 0x3b800000, v19
	v_mul_f32_e32 v35, 0x4f800000, v9
	v_cmp_gt_f32_e32 vcc, s0, v9
	v_mul_f32_e32 v36, 0x4f800000, v32
	v_cmp_gt_f32_e64 s[2:3], s0, v32
	v_cndmask_b32_e64 v8, v8, v34, s[6:7]
	v_mul_f32_e32 v37, 0x4f800000, v33
	v_cmp_gt_f32_e64 s[4:5], s0, v33
	v_cndmask_b32_e32 v9, v9, v35, vcc
	v_cndmask_b32_e64 v32, v32, v36, s[2:3]
	v_sqrt_f32_e32 v34, v8
	v_cndmask_b32_e64 v33, v33, v37, s[4:5]
	v_sqrt_f32_e32 v35, v9
	v_sqrt_f32_e32 v36, v32
	v_sqrt_f32_e32 v37, v33
	v_add_u32_e32 v38, -1, v34
	v_add_u32_e32 v39, 1, v34
	v_add_u32_e32 v42, -1, v35
	v_add_u32_e32 v46, -1, v36
	v_fma_f32 v56, -v38, v34, v8
	v_add_u32_e32 v43, 1, v35
	v_add_u32_e32 v47, 1, v36
	v_add_u32_e32 v50, -1, v37
	v_fma_f32 v57, -v39, v34, v8
	v_fma_f32 v58, -v42, v35, v9
	v_fma_f32 v60, -v46, v36, v32
	v_cmp_ge_f32_e64 s[8:9], 0, v56
	v_add_u32_e32 v51, 1, v37
	v_fma_f32 v59, -v43, v35, v9
	v_fma_f32 v61, -v47, v36, v32
	v_fma_f32 v62, -v50, v37, v33
	v_cndmask_b32_e64 v34, v34, v38, s[8:9]
	v_cmp_ge_f32_e64 s[8:9], 0, v58
	v_cmp_ge_f32_e64 s[10:11], 0, v60
	v_cmp_lt_f32_e64 s[14:15], 0, v57
	v_fma_f32 v63, -v51, v37, v33
	v_cndmask_b32_e64 v35, v35, v42, s[8:9]
	v_cmp_lt_f32_e64 s[8:9], 0, v59
	v_cndmask_b32_e64 v36, v36, v46, s[10:11]
	v_cmp_lt_f32_e64 s[10:11], 0, v61
	v_cmp_ge_f32_e64 s[12:13], 0, v62
	v_cndmask_b32_e64 v34, v34, v39, s[14:15]
	v_cndmask_b32_e64 v35, v35, v43, s[8:9]
	v_cndmask_b32_e64 v37, v37, v50, s[12:13]
	v_cmp_lt_f32_e64 s[12:13], 0, v63
	v_cndmask_b32_e64 v36, v36, v47, s[10:11]
	v_mul_f32_e32 v38, 0x37800000, v34
	v_cndmask_b32_e64 v37, v37, v51, s[12:13]
	v_mul_f32_e32 v39, 0x37800000, v35
	v_mul_f32_e32 v42, 0x37800000, v36
	v_cndmask_b32_e64 v34, v34, v38, s[6:7]
	v_cmp_class_f32_e64 s[6:7], v8, v20
	v_mul_f32_e32 v43, 0x37800000, v37
	v_cndmask_b32_e32 v35, v35, v39, vcc
	v_cmp_class_f32_e32 vcc, v9, v20
	v_cndmask_b32_e64 v36, v36, v42, s[2:3]
	v_cmp_class_f32_e64 s[2:3], v32, v20
	v_cndmask_b32_e64 v8, v34, v8, s[6:7]
	v_cndmask_b32_e64 v37, v37, v43, s[4:5]
	v_cmp_class_f32_e64 s[4:5], v33, v20
	v_cndmask_b32_e32 v34, v35, v9, vcc
	v_cndmask_b32_e64 v36, v36, v32, s[2:3]
	v_div_scale_f32 v9, s[2:3], v8, v8, 1.0
	v_cndmask_b32_e64 v37, v37, v33, s[4:5]
	v_div_scale_f32 v33, s[2:3], v34, v34, 1.0
	v_rcp_f32_e32 v46, v9
	v_div_scale_f32 v38, s[4:5], v36, v36, 1.0
	v_rcp_f32_e32 v47, v33
	v_div_scale_f32 v42, s[6:7], v37, v37, 1.0
	v_rcp_f32_e32 v50, v38
	v_rcp_f32_e32 v51, v42
	v_fma_f32 v56, -v9, v46, 1.0
	v_div_scale_f32 v32, vcc, 1.0, v8, 1.0
	v_fma_f32 v57, -v33, v47, 1.0
	v_fmac_f32_e32 v46, v56, v46
	v_div_scale_f32 v35, s[2:3], 1.0, v34, 1.0
	v_fma_f32 v58, -v38, v50, 1.0
	v_fmac_f32_e32 v47, v57, v47
	v_mul_f32_e32 v56, v32, v46
	v_div_scale_f32 v39, s[4:5], 1.0, v36, 1.0
	v_fma_f32 v59, -v42, v51, 1.0
	v_fmac_f32_e32 v50, v58, v50
	v_mul_f32_e32 v57, v35, v47
	v_fma_f32 v60, -v9, v56, v32
	v_div_scale_f32 v43, s[6:7], 1.0, v37, 1.0
	v_fmac_f32_e32 v51, v59, v51
	v_mul_f32_e32 v58, v39, v50
	v_fma_f32 v61, -v33, v57, v35
	v_fmac_f32_e32 v56, v60, v46
	v_mul_f32_e32 v59, v43, v51
	v_fma_f32 v62, -v38, v58, v39
	v_fmac_f32_e32 v57, v61, v47
	v_fma_f32 v9, -v9, v56, v32
	v_fma_f32 v63, -v42, v59, v43
	v_fmac_f32_e32 v58, v62, v50
	v_fma_f32 v32, -v33, v57, v35
	v_div_fmas_f32 v9, v9, v46, v56
	s_mov_b64 vcc, s[2:3]
	v_fmac_f32_e32 v59, v63, v51
	v_fma_f32 v35, -v38, v58, v39
	v_div_fixup_f32 v8, v9, v8, 1.0
	v_div_fmas_f32 v39, v32, v47, v57
	s_mov_b64 vcc, s[4:5]
	v_fma_f32 v38, -v42, v59, v43
	v_pk_mul_f32 v[32:33], v[8:9], v[40:41] op_sel_hi:[0,1]
	v_pk_mul_f32 v[8:9], v[8:9], v[24:25] op_sel_hi:[0,1]
	v_div_fixup_f32 v24, v39, v34, 1.0
	v_div_fmas_f32 v39, v35, v50, v58
	s_mov_b64 vcc, s[6:7]
	v_pk_mul_f32 v[8:9], v[2:3], v[8:9]
	v_pk_mul_f32 v[32:33], v[0:1], v[32:33]
	v_pk_mul_f32 v[34:35], v[24:25], v[44:45] op_sel_hi:[0,1]
	v_pk_mul_f32 v[24:25], v[24:25], v[26:27] op_sel_hi:[0,1]
	v_div_fixup_f32 v26, v39, v36, 1.0
	v_div_fmas_f32 v36, v38, v51, v59
	v_mul_f32_e32 v38, 0x41800000, v32
	v_mul_f32_e32 v39, 0x41800000, v33
	v_mul_f32_e32 v40, 0x41800000, v8
	v_mul_f32_e32 v41, 0x41800000, v9
	v_pk_mul_f32 v[8:9], v[2:3], v[24:25]
	v_pk_mul_f32 v[24:25], v[0:1], v[34:35]
	v_pk_mul_f32 v[32:33], v[26:27], v[48:49] op_sel_hi:[0,1]
	v_pk_mul_f32 v[26:27], v[26:27], v[28:29] op_sel_hi:[0,1]
	v_div_fixup_f32 v28, v36, v37, 1.0
	v_med3_f32 v34, v38, s1, v21
	v_med3_f32 v35, v39, s1, v21
	v_med3_f32 v36, v40, s1, v21
	v_med3_f32 v37, v41, s1, v21
	v_mul_f32_e32 v38, 0x41800000, v24
	v_mul_f32_e32 v39, 0x41800000, v25
	v_mul_f32_e32 v40, 0x41800000, v8
	v_mul_f32_e32 v41, 0x41800000, v9
	v_pk_mul_f32 v[8:9], v[2:3], v[26:27]
	v_pk_mul_f32 v[24:25], v[0:1], v[32:33]
	v_pk_mul_f32 v[26:27], v[28:29], v[52:53] op_sel_hi:[0,1]
	v_pk_mul_f32 v[28:29], v[28:29], v[30:31] op_sel_hi:[0,1]
	v_cvt_pk_fp8_f32 v22, v34, v35
	v_med3_f32 v30, v38, s1, v21
	v_med3_f32 v31, v39, s1, v21
	v_mul_f32_e32 v34, 0x41800000, v24
	v_mul_f32_e32 v35, 0x41800000, v25
	v_pk_mul_f32 v[24:25], v[0:1], v[26:27]
	v_cvt_pk_fp8_f32 v23, v30, v31
	v_med3_f32 v26, v34, s1, v21
	v_med3_f32 v27, v35, s1, v21
	v_mul_f32_e32 v24, 0x41800000, v24
	v_mul_f32_e32 v25, 0x41800000, v25
	v_cvt_pk_fp8_f32 v54, v26, v27
	v_med3_f32 v24, v24, s1, v21
	v_med3_f32 v25, v25, s1, v21
	v_cvt_pk_fp8_f32 v55, v24, v25
	v_med3_f32 v32, v40, s1, v21
	v_med3_f32 v33, v41, s1, v21
	v_mul_f32_e32 v38, 0x41800000, v8
	v_mul_f32_e32 v39, 0x41800000, v9
	v_pk_mul_f32 v[8:9], v[2:3], v[28:29]
	v_cvt_pk_fp8_f32 v22, v36, v37 op_sel:[0,0,1]
	v_med3_f32 v28, v38, s1, v21
	v_med3_f32 v29, v39, s1, v21
	v_mul_f32_e32 v8, 0x41800000, v8
	v_mul_f32_e32 v9, 0x41800000, v9
	v_cvt_pk_fp8_f32 v23, v32, v33 op_sel:[0,0,1]
	v_med3_f32 v8, v8, s1, v21
	v_med3_f32 v9, v9, s1, v21
	v_cvt_pk_fp8_f32 v54, v28, v29 op_sel:[0,0,1]
	v_cvt_pk_fp8_f32 v55, v8, v9 op_sel:[0,0,1]
	global_store_dword v[10:11], v22, off
	global_store_dword v[10:11], v23, off offset:256
	global_store_dword v[10:11], v54, off offset:512
	global_store_dword v[10:11], v55, off offset:768
	s_cbranch_scc1 .LBB0_1099

.LBB0_1862:
	s_add_i32 s0, s19, s23
	s_add_i32 s10, s6, -7
	s_add_i32 s8, s0, 2
	s_add_i32 s0, s0, 3
	s_ashr_i32 s11, s10, 31
	s_ashr_i32 s9, s8, 31
	s_ashr_i32 s1, s0, 31
	s_lshl_b64 s[10:11], s[10:11], 2
	s_lshl_b64 s[24:25], s[8:9], 11
	s_lshl_b64 s[26:27], s[0:1], 11
	v_lshl_add_u64 v[58:59], v[36:37], 0, s[24:25]
	s_add_u32 s24, s12, s10
	s_addc_u32 s25, s13, s11
	s_add_u32 s10, s14, s10
	s_addc_u32 s11, s15, s11
	v_lshl_add_u64 v[60:61], v[36:37], 0, s[26:27]
	global_load_dwordx2 v[56:57], v[58:59], off nt
	global_load_dwordx2 v[54:55], v[58:59], off offset:512 nt
	global_load_dwordx2 v[52:53], v[58:59], off offset:1024 nt
	global_load_dwordx2 v[50:51], v[58:59], off offset:1536 nt
	global_load_dwordx2 v[48:49], v[60:61], off nt
	global_load_dwordx2 v[46:47], v[60:61], off offset:512 nt
	global_load_dwordx2 v[44:45], v[60:61], off offset:1024 nt
	global_load_dwordx2 v[42:43], v[60:61], off offset:1536 nt
	global_load_dword v72, v68, s[24:25]
	global_load_dword v73, v68, s[10:11]
	s_add_i32 s24, s6, -6
	s_ashr_i32 s25, s24, 31
	s_lshl_b64 s[10:11], s[24:25], 2
	s_add_u32 s24, s12, s10
	s_addc_u32 s25, s13, s11
	s_add_u32 s10, s14, s10
	s_addc_u32 s11, s15, s11
	global_load_dword v74, v68, s[24:25]
	global_load_dword v76, v68, s[10:11]
	s_add_i32 s24, s6, -5
	s_ashr_i32 s25, s24, 31
	s_lshl_b64 s[10:11], s[24:25], 2
	s_add_u32 s24, s12, s10
	s_addc_u32 s25, s13, s11
	s_add_u32 s10, s14, s10
	s_addc_u32 s11, s15, s11
	global_load_dword v75, v68, s[24:25]
	global_load_dword v78, v68, s[10:11]
	s_add_i32 s24, s6, -4
	s_ashr_i32 s25, s24, 31
	s_lshl_b64 s[10:11], s[24:25], 2
	s_add_u32 s24, s12, s10
	s_addc_u32 s25, s13, s11
	s_add_u32 s10, s14, s10
	s_addc_u32 s11, s15, s11
	global_load_dword v77, v68, s[24:25]
	global_load_dword v80, v68, s[10:11]
	s_add_i32 s24, s6, -3
	s_ashr_i32 s25, s24, 31
	s_lshl_b64 s[10:11], s[24:25], 2
	s_add_u32 s24, s12, s10
	s_addc_u32 s25, s13, s11
	s_add_u32 s10, s14, s10
	s_addc_u32 s11, s15, s11
	global_load_dword v79, v68, s[24:25]
	global_load_dword v82, v68, s[10:11]
	s_add_i32 s24, s6, -2
	s_ashr_i32 s25, s24, 31
	s_lshl_b64 s[10:11], s[24:25], 2
	s_add_u32 s24, s12, s10
	s_addc_u32 s25, s13, s11
	s_add_u32 s10, s14, s10
	s_addc_u32 s11, s15, s11
	global_load_dword v81, v68, s[24:25]
	global_load_dword v84, v68, s[10:11]
	s_add_i32 s24, s6, -1
	s_ashr_i32 s25, s24, 31
	s_lshl_b64 s[10:11], s[24:25], 2
	s_add_u32 s24, s12, s10
	s_addc_u32 s25, s13, s11
	global_load_dword v83, v68, s[24:25]
	s_add_u32 s10, s14, s10
	s_addc_u32 s11, s15, s11
	s_ashr_i32 s7, s6, 31
	global_load_dword v85, v68, s[10:11]
	s_lshl_b64 s[10:11], s[6:7], 2
	s_add_u32 s24, s12, s10
	s_addc_u32 s25, s13, s11
	global_load_dword v86, v68, s[24:25]
	s_add_u32 s10, s14, s10
	s_addc_u32 s11, s15, s11
	global_load_dword v87, v68, s[10:11]
	s_lshl_b64 s[0:1], s[0:1], 12
	v_lshl_add_u64 v[58:59], v[40:41], 0, s[0:1]
	s_lshl_b64 s[8:9], s[8:9], 12
	v_lshl_add_u64 v[60:61], v[40:41], 0, s[8:9]
	s_add_i32 s23, s23, 2
	s_add_i32 s6, s6, 8
	s_cmp_gt_u32 s23, 13
	s_waitcnt vmcnt(23)
	v_lshlrev_b32_e32 v88, 16, v56
	v_and_b32_e32 v89, 0xffff0000, v56
	v_lshlrev_b32_e32 v56, 16, v57
	v_and_b32_e32 v57, 0xffff0000, v57
	s_waitcnt vmcnt(22)
	v_lshlrev_b32_e32 v90, 16, v54
	v_and_b32_e32 v91, 0xffff0000, v54
	v_lshlrev_b32_e32 v54, 16, v55
	v_and_b32_e32 v55, 0xffff0000, v55
	s_waitcnt vmcnt(15)
	v_lshlrev_b32_sdwa v104, v71, v72 dst_sel:DWORD dst_unused:UNUSED_PAD src0_sel:DWORD src1_sel:BYTE_3
	v_and_b32_e32 v105, 0xffffff, v72
	v_add_u32_e32 v72, s21, v104
	ds_read_b32 v104, v72
	s_waitcnt vmcnt(14)
	v_mul_f32_e32 v72, 0x3d000000, v73
	v_lshlrev_b32_e32 v92, 16, v52
	v_and_b32_e32 v93, 0xffff0000, v52
	v_lshlrev_b32_e32 v52, 16, v53
	s_waitcnt lgkmcnt(0)
	v_add_u32_e32 v104, v104, v105
	s_waitcnt vmcnt(13)
	v_lshlrev_b32_sdwa v73, v71, v74 dst_sel:DWORD dst_unused:UNUSED_PAD src0_sel:DWORD src1_sel:BYTE_3
	v_add_u32_e32 v73, s21, v73
	ds_read_b32 v73, v73
	v_ashrrev_i32_e32 v105, 31, v104
	v_lshlrev_b64 v[104:105], 10, v[104:105]
	v_and_b32_e32 v106, 0xffffff, v74
	s_waitcnt vmcnt(12)
	v_mul_f32_e32 v74, 0x3d000000, v76
	v_lshl_add_u64 v[104:105], v[38:39], 0, v[104:105]
	global_load_dword v107, v[104:105], off nt
	global_load_dword v110, v[104:105], off offset:256 nt
	global_load_dword v114, v[104:105], off offset:512 nt
	global_load_dword v118, v[104:105], off offset:768 nt
	s_waitcnt vmcnt(15)
	v_lshlrev_b32_sdwa v76, v71, v75 dst_sel:DWORD dst_unused:UNUSED_PAD src0_sel:DWORD src1_sel:BYTE_3
	v_add_u32_e32 v76, s21, v76
	ds_read_b32 v108, v76
	s_waitcnt lgkmcnt(1)
	v_add_u32_e32 v104, v73, v106
	v_ashrrev_i32_e32 v105, 31, v104
	v_lshlrev_b64 v[104:105], 10, v[104:105]
	v_lshl_add_u64 v[104:105], v[38:39], 0, v[104:105]
	v_and_b32_e32 v75, 0xffffff, v75
	global_load_dword v120, v[104:105], off nt
	global_load_dword v121, v[104:105], off offset:256 nt
	global_load_dword v122, v[104:105], off offset:512 nt
	global_load_dword v123, v[104:105], off offset:768 nt
	s_waitcnt vmcnt(17)
	v_lshlrev_b32_sdwa v73, v71, v77 dst_sel:DWORD dst_unused:UNUSED_PAD src0_sel:DWORD src1_sel:BYTE_3
	v_add_u32_e32 v73, s21, v73
	s_waitcnt lgkmcnt(0)
	v_add_u32_e32 v104, v108, v75
	ds_read_b32 v73, v73
	v_ashrrev_i32_e32 v105, 31, v104
	v_lshlrev_b64 v[104:105], 10, v[104:105]
	v_lshl_add_u64 v[104:105], v[38:39], 0, v[104:105]
	global_load_dword v124, v[104:105], off nt
	global_load_dword v125, v[104:105], off offset:256 nt
	global_load_dword v126, v[104:105], off offset:512 nt
	global_load_dword v127, v[104:105], off offset:768 nt
	v_and_b32_e32 v77, 0xffffff, v77
	s_waitcnt vmcnt(19)
	v_lshlrev_b32_sdwa v75, v71, v79 dst_sel:DWORD dst_unused:UNUSED_PAD src0_sel:DWORD src1_sel:BYTE_3
	s_waitcnt lgkmcnt(0)
	v_add_u32_e32 v104, v73, v77
	v_add_u32_e32 v75, s21, v75
	v_ashrrev_i32_e32 v105, 31, v104
	ds_read_b32 v75, v75
	v_lshlrev_b64 v[104:105], 10, v[104:105]
	v_lshl_add_u64 v[104:105], v[38:39], 0, v[104:105]
	global_load_dword v128, v[104:105], off nt
	global_load_dword v129, v[104:105], off offset:256 nt
	global_load_dword v130, v[104:105], off offset:512 nt
	global_load_dword v131, v[104:105], off offset:768 nt
	v_and_b32_e32 v79, 0xffffff, v79
	s_waitcnt vmcnt(21)
	v_lshlrev_b32_sdwa v73, v71, v81 dst_sel:DWORD dst_unused:UNUSED_PAD src0_sel:DWORD src1_sel:BYTE_3
	v_add_u32_e32 v73, s21, v73
	ds_read_b32 v73, v73
	s_waitcnt lgkmcnt(1)
	v_add_u32_e32 v104, v75, v79
	v_ashrrev_i32_e32 v105, 31, v104
	v_lshlrev_b64 v[104:105], 10, v[104:105]
	v_lshl_add_u64 v[104:105], v[38:39], 0, v[104:105]
	s_waitcnt vmcnt(19)
	v_lshlrev_b32_sdwa v75, v71, v83 dst_sel:DWORD dst_unused:UNUSED_PAD src0_sel:DWORD src1_sel:BYTE_3
	v_and_b32_e32 v77, 0xffffff, v81
	global_load_dword v81, v[104:105], off nt
	global_load_dword v132, v[104:105], off offset:256 nt
	global_load_dword v133, v[104:105], off offset:512 nt
	global_load_dword v134, v[104:105], off offset:768 nt
	v_add_u32_e32 v75, s21, v75
	v_mul_f32_e32 v76, 0x3d000000, v78
	v_mul_f32_e32 v78, 0x3d000000, v80
	v_mul_f32_e32 v80, 0x3d000000, v82
	v_mul_f32_e32 v82, 0x3d000000, v84
	ds_read_b32 v75, v75
	s_waitcnt lgkmcnt(1)
	v_add_u32_e32 v84, v73, v77
	s_waitcnt vmcnt(22)
	v_mul_f32_e32 v104, 0x3d000000, v85
	v_ashrrev_i32_e32 v85, 31, v84
	v_lshlrev_b64 v[84:85], 10, v[84:85]
	v_lshl_add_u64 v[84:85], v[38:39], 0, v[84:85]
	s_waitcnt vmcnt(21)
	v_lshlrev_b32_sdwa v73, v71, v86 dst_sel:DWORD dst_unused:UNUSED_PAD src0_sel:DWORD src1_sel:BYTE_3
	v_and_b32_e32 v79, 0xffffff, v83
	global_load_dword v83, v[84:85], off nt
	global_load_dword v105, v[84:85], off offset:256 nt
	global_load_dword v135, v[84:85], off offset:512 nt
	global_load_dword v136, v[84:85], off offset:768 nt
	v_add_u32_e32 v73, s21, v73
	ds_read_b32 v73, v73
	s_waitcnt lgkmcnt(1)
	v_add_u32_e32 v84, v75, v79
	v_ashrrev_i32_e32 v85, 31, v84
	v_lshlrev_b64 v[84:85], 10, v[84:85]
	v_lshl_add_u64 v[84:85], v[38:39], 0, v[84:85]
	v_and_b32_e32 v77, 0xffffff, v86
	s_waitcnt vmcnt(24)
	v_mul_f32_e32 v86, 0x3d000000, v87
	global_load_dword v87, v[84:85], off nt
	global_load_dword v137, v[84:85], off offset:256 nt
	global_load_dword v138, v[84:85], off offset:512 nt
	global_load_dword v139, v[84:85], off offset:768 nt
	s_waitcnt lgkmcnt(0)
	v_add_u32_e32 v84, v73, v77
	v_ashrrev_i32_e32 v85, 31, v84
	v_lshlrev_b64 v[84:85], 10, v[84:85]
	v_lshl_add_u64 v[84:85], v[38:39], 0, v[84:85]
	global_load_dword v140, v[84:85], off nt
	global_load_dword v141, v[84:85], off offset:256 nt
	global_load_dword v142, v[84:85], off offset:512 nt
	global_load_dword v143, v[84:85], off offset:768 nt
	v_and_b32_e32 v53, 0xffff0000, v53
	v_lshlrev_b32_e32 v94, 16, v50
	v_and_b32_e32 v95, 0xffff0000, v50
	v_lshlrev_b32_e32 v50, 16, v51
	v_and_b32_e32 v51, 0xffff0000, v51
	v_lshlrev_b32_e32 v96, 16, v48
	v_and_b32_e32 v97, 0xffff0000, v48
	v_lshlrev_b32_e32 v48, 16, v49
	v_and_b32_e32 v49, 0xffff0000, v49
	v_lshlrev_b32_e32 v98, 16, v46
	v_and_b32_e32 v99, 0xffff0000, v46
	s_waitcnt vmcnt(31)
	v_cvt_pk_f32_fp8_e32 v[84:85], v107
	v_cvt_pk_f32_fp8_sdwa v[106:107], v107 src0_sel:WORD_1
	s_waitcnt vmcnt(30)
	v_cvt_pk_f32_fp8_e32 v[108:109], v110
	v_cvt_pk_f32_fp8_sdwa v[110:111], v110 src0_sel:WORD_1
	s_waitcnt vmcnt(29)
	v_cvt_pk_f32_fp8_e32 v[112:113], v114
	v_cvt_pk_f32_fp8_sdwa v[114:115], v114 src0_sel:WORD_1
	s_waitcnt vmcnt(28)
	v_cvt_pk_f32_fp8_e32 v[116:117], v118
	v_cvt_pk_f32_fp8_sdwa v[118:119], v118 src0_sel:WORD_1
	v_pk_mul_f32 v[106:107], v[72:73], v[106:107] op_sel_hi:[0,1]
	v_pk_mul_f32 v[84:85], v[72:73], v[84:85] op_sel_hi:[0,1]
	v_pk_mul_f32 v[110:111], v[72:73], v[110:111] op_sel_hi:[0,1]
	v_pk_mul_f32 v[108:109], v[72:73], v[108:109] op_sel_hi:[0,1]
	v_pk_mul_f32 v[114:115], v[72:73], v[114:115] op_sel_hi:[0,1]
	v_pk_mul_f32 v[112:113], v[72:73], v[112:113] op_sel_hi:[0,1]
	v_pk_mul_f32 v[118:119], v[72:73], v[118:119] op_sel_hi:[0,1]
	v_pk_mul_f32 v[72:73], v[72:73], v[116:117] op_sel_hi:[0,1]
	v_pk_fma_f32 v[84:85], v[24:25], v[84:85], v[88:89]
	v_pk_fma_f32 v[56:57], v[26:27], v[106:107], v[56:57]
	v_pk_fma_f32 v[88:89], v[8:9], v[108:109], v[90:91]
	v_pk_fma_f32 v[54:55], v[10:11], v[110:111], v[54:55]
	v_pk_fma_f32 v[90:91], v[12:13], v[112:113], v[92:93]
	v_pk_fma_f32 v[52:53], v[14:15], v[114:115], v[52:53]
	v_pk_fma_f32 v[72:73], v[28:29], v[72:73], v[94:95]
	s_waitcnt vmcnt(27)
	v_cvt_pk_f32_fp8_e32 v[92:93], v120
	v_cvt_pk_f32_fp8_sdwa v[94:95], v120 src0_sel:WORD_1
	s_waitcnt vmcnt(26)
	v_cvt_pk_f32_fp8_e32 v[106:107], v121
	v_cvt_pk_f32_fp8_sdwa v[108:109], v121 src0_sel:WORD_1
	s_waitcnt vmcnt(25)
	v_cvt_pk_f32_fp8_e32 v[110:111], v122
	v_cvt_pk_f32_fp8_sdwa v[112:113], v122 src0_sel:WORD_1
	s_waitcnt vmcnt(24)
	v_cvt_pk_f32_fp8_e32 v[114:115], v123
	v_cvt_pk_f32_fp8_sdwa v[116:117], v123 src0_sel:WORD_1
	v_pk_fma_f32 v[50:51], v[30:31], v[118:119], v[50:51]
	v_pk_mul_f32 v[92:93], v[74:75], v[92:93] op_sel_hi:[0,1]
	v_pk_mul_f32 v[94:95], v[74:75], v[94:95] op_sel_hi:[0,1]
	v_pk_mul_f32 v[106:107], v[74:75], v[106:107] op_sel_hi:[0,1]
	v_pk_mul_f32 v[108:109], v[74:75], v[108:109] op_sel_hi:[0,1]
	v_pk_mul_f32 v[110:111], v[74:75], v[110:111] op_sel_hi:[0,1]
	v_pk_mul_f32 v[112:113], v[74:75], v[112:113] op_sel_hi:[0,1]
	v_pk_mul_f32 v[114:115], v[74:75], v[114:115] op_sel_hi:[0,1]
	v_pk_mul_f32 v[74:75], v[74:75], v[116:117] op_sel_hi:[0,1]
	v_pk_fma_f32 v[56:57], v[26:27], v[94:95], v[56:57]
	v_pk_fma_f32 v[84:85], v[24:25], v[92:93], v[84:85]
	v_pk_fma_f32 v[54:55], v[10:11], v[108:109], v[54:55]
	v_pk_fma_f32 v[88:89], v[8:9], v[106:107], v[88:89]
	v_pk_fma_f32 v[52:53], v[14:15], v[112:113], v[52:53]
	v_pk_fma_f32 v[90:91], v[12:13], v[110:111], v[90:91]
	v_pk_fma_f32 v[50:51], v[30:31], v[74:75], v[50:51]
	v_pk_fma_f32 v[72:73], v[28:29], v[114:115], v[72:73]
	s_waitcnt vmcnt(23)
	v_cvt_pk_f32_fp8_e32 v[74:75], v124
	v_cvt_pk_f32_fp8_sdwa v[92:93], v124 src0_sel:WORD_1
	s_waitcnt vmcnt(22)
	v_cvt_pk_f32_fp8_e32 v[94:95], v125
	v_cvt_pk_f32_fp8_sdwa v[106:107], v125 src0_sel:WORD_1
	s_waitcnt vmcnt(21)
	v_cvt_pk_f32_fp8_e32 v[108:109], v126
	v_cvt_pk_f32_fp8_sdwa v[110:111], v126 src0_sel:WORD_1
	s_waitcnt vmcnt(20)
	v_cvt_pk_f32_fp8_e32 v[112:113], v127
	v_cvt_pk_f32_fp8_sdwa v[114:115], v127 src0_sel:WORD_1
	v_pk_mul_f32 v[92:93], v[76:77], v[92:93] op_sel_hi:[0,1]
	v_pk_mul_f32 v[74:75], v[76:77], v[74:75] op_sel_hi:[0,1]
	v_pk_mul_f32 v[106:107], v[76:77], v[106:107] op_sel_hi:[0,1]
	v_pk_mul_f32 v[94:95], v[76:77], v[94:95] op_sel_hi:[0,1]
	v_pk_mul_f32 v[110:111], v[76:77], v[110:111] op_sel_hi:[0,1]
	v_pk_mul_f32 v[108:109], v[76:77], v[108:109] op_sel_hi:[0,1]
	v_pk_mul_f32 v[114:115], v[76:77], v[114:115] op_sel_hi:[0,1]
	v_pk_mul_f32 v[76:77], v[76:77], v[112:113] op_sel_hi:[0,1]
	v_pk_fma_f32 v[72:73], v[28:29], v[76:77], v[72:73]
	s_waitcnt vmcnt(19)
	v_cvt_pk_f32_fp8_e32 v[76:77], v128
	v_pk_fma_f32 v[74:75], v[24:25], v[74:75], v[84:85]
	v_pk_fma_f32 v[56:57], v[26:27], v[92:93], v[56:57]
	v_pk_fma_f32 v[84:85], v[8:9], v[94:95], v[88:89]
	v_pk_fma_f32 v[54:55], v[10:11], v[106:107], v[54:55]
	v_pk_fma_f32 v[88:89], v[12:13], v[108:109], v[90:91]
	v_pk_fma_f32 v[52:53], v[14:15], v[110:111], v[52:53]
	v_cvt_pk_f32_fp8_sdwa v[90:91], v128 src0_sel:WORD_1
	s_waitcnt vmcnt(18)
	v_cvt_pk_f32_fp8_e32 v[92:93], v129
	v_cvt_pk_f32_fp8_sdwa v[94:95], v129 src0_sel:WORD_1
	s_waitcnt vmcnt(17)
	v_cvt_pk_f32_fp8_e32 v[106:107], v130
	v_cvt_pk_f32_fp8_sdwa v[108:109], v130 src0_sel:WORD_1
	s_waitcnt vmcnt(16)
	v_cvt_pk_f32_fp8_e32 v[110:111], v131
	v_cvt_pk_f32_fp8_sdwa v[112:113], v131 src0_sel:WORD_1
	v_pk_mul_f32 v[76:77], v[78:79], v[76:77] op_sel_hi:[0,1]
	v_pk_fma_f32 v[50:51], v[30:31], v[114:115], v[50:51]
	v_pk_mul_f32 v[90:91], v[78:79], v[90:91] op_sel_hi:[0,1]
	v_pk_mul_f32 v[92:93], v[78:79], v[92:93] op_sel_hi:[0,1]
	v_pk_mul_f32 v[94:95], v[78:79], v[94:95] op_sel_hi:[0,1]
	v_pk_mul_f32 v[106:107], v[78:79], v[106:107] op_sel_hi:[0,1]
	v_pk_mul_f32 v[108:109], v[78:79], v[108:109] op_sel_hi:[0,1]
	v_pk_mul_f32 v[110:111], v[78:79], v[110:111] op_sel_hi:[0,1]
	v_pk_mul_f32 v[78:79], v[78:79], v[112:113] op_sel_hi:[0,1]
	v_pk_fma_f32 v[74:75], v[24:25], v[76:77], v[74:75]
	v_pk_fma_f32 v[56:57], v[26:27], v[90:91], v[56:57]
	v_pk_fma_f32 v[50:51], v[30:31], v[78:79], v[50:51]
	v_pk_fma_f32 v[78:79], v[74:75], v[74:75], 0 op_sel_hi:[1,1,0]
	v_pk_fma_f32 v[76:77], v[8:9], v[92:93], v[84:85]
	v_pk_fma_f32 v[78:79], v[56:57], v[56:57], v[78:79]
	v_pk_fma_f32 v[54:55], v[10:11], v[94:95], v[54:55]
	v_pk_fma_f32 v[52:53], v[14:15], v[108:109], v[52:53]
	v_pk_fma_f32 v[84:85], v[12:13], v[106:107], v[88:89]
	v_pk_fma_f32 v[72:73], v[28:29], v[110:111], v[72:73]
	s_waitcnt vmcnt(15)
	v_cvt_pk_f32_fp8_e32 v[88:89], v81
	v_cvt_pk_f32_fp8_sdwa v[90:91], v81 src0_sel:WORD_1
	s_waitcnt vmcnt(14)
	v_cvt_pk_f32_fp8_e32 v[92:93], v132
	v_cvt_pk_f32_fp8_sdwa v[94:95], v132 src0_sel:WORD_1
	s_waitcnt vmcnt(13)
	v_cvt_pk_f32_fp8_e32 v[106:107], v133
	v_cvt_pk_f32_fp8_sdwa v[108:109], v133 src0_sel:WORD_1
	s_waitcnt vmcnt(12)
	v_cvt_pk_f32_fp8_e32 v[110:111], v134
	v_cvt_pk_f32_fp8_sdwa v[112:113], v134 src0_sel:WORD_1
	v_pk_fma_f32 v[78:79], v[76:77], v[76:77], v[78:79]
	v_lshlrev_b32_e32 v46, 16, v47
	v_pk_fma_f32 v[78:79], v[54:55], v[54:55], v[78:79]
	v_and_b32_e32 v47, 0xffff0000, v47
	v_pk_fma_f32 v[78:79], v[84:85], v[84:85], v[78:79]
	v_lshlrev_b32_e32 v100, 16, v44
	v_pk_fma_f32 v[78:79], v[52:53], v[52:53], v[78:79]
	v_and_b32_e32 v101, 0xffff0000, v44
	v_lshlrev_b32_e32 v44, 16, v45
	v_and_b32_e32 v45, 0xffff0000, v45
	v_lshlrev_b32_e32 v102, 16, v42
	v_and_b32_e32 v103, 0xffff0000, v42
	v_pk_mul_f32 v[90:91], v[80:81], v[90:91] op_sel_hi:[0,1]
	v_pk_mul_f32 v[88:89], v[80:81], v[88:89] op_sel_hi:[0,1]
	v_pk_mul_f32 v[94:95], v[80:81], v[94:95] op_sel_hi:[0,1]
	v_pk_mul_f32 v[92:93], v[80:81], v[92:93] op_sel_hi:[0,1]
	v_pk_mul_f32 v[108:109], v[80:81], v[108:109] op_sel_hi:[0,1]
	v_pk_mul_f32 v[106:107], v[80:81], v[106:107] op_sel_hi:[0,1]
	v_pk_mul_f32 v[112:113], v[80:81], v[112:113] op_sel_hi:[0,1]
	v_pk_mul_f32 v[80:81], v[80:81], v[110:111] op_sel_hi:[0,1]
	v_pk_fma_f32 v[78:79], v[72:73], v[72:73], v[78:79]
	v_pk_fma_f32 v[88:89], v[24:25], v[88:89], v[96:97]
	v_pk_fma_f32 v[48:49], v[26:27], v[90:91], v[48:49]
	v_pk_fma_f32 v[90:91], v[8:9], v[92:93], v[98:99]
	v_pk_fma_f32 v[46:47], v[10:11], v[94:95], v[46:47]
	v_pk_fma_f32 v[92:93], v[12:13], v[106:107], v[100:101]
	v_pk_fma_f32 v[44:45], v[14:15], v[108:109], v[44:45]
	v_pk_fma_f32 v[80:81], v[28:29], v[80:81], v[102:103]
	s_waitcnt vmcnt(11)
	v_cvt_pk_f32_fp8_e32 v[94:95], v83
	v_cvt_pk_f32_fp8_sdwa v[96:97], v83 src0_sel:WORD_1
	s_waitcnt vmcnt(10)
	v_cvt_pk_f32_fp8_e32 v[98:99], v105
	v_cvt_pk_f32_fp8_sdwa v[100:101], v105 src0_sel:WORD_1
	s_waitcnt vmcnt(9)
	v_cvt_pk_f32_fp8_e32 v[102:103], v135
	v_cvt_pk_f32_fp8_sdwa v[106:107], v135 src0_sel:WORD_1
	s_waitcnt vmcnt(8)
	v_cvt_pk_f32_fp8_e32 v[108:109], v136
	v_cvt_pk_f32_fp8_sdwa v[110:111], v136 src0_sel:WORD_1
	v_pk_fma_f32 v[78:79], v[50:51], v[50:51], v[78:79]
	v_lshlrev_b32_e32 v42, 16, v43
	v_and_b32_e32 v43, 0xffff0000, v43
	v_add_f32_e32 v105, v78, v79
	v_pk_fma_f32 v[42:43], v[30:31], v[112:113], v[42:43]
	v_pk_mul_f32 v[78:79], v[82:83], v[94:95] op_sel_hi:[0,1]
	v_pk_mul_f32 v[94:95], v[82:83], v[96:97] op_sel_hi:[0,1]
	v_pk_mul_f32 v[96:97], v[82:83], v[98:99] op_sel_hi:[0,1]
	v_pk_mul_f32 v[98:99], v[82:83], v[100:101] op_sel_hi:[0,1]
	v_pk_mul_f32 v[100:101], v[82:83], v[102:103] op_sel_hi:[0,1]
	v_pk_mul_f32 v[102:103], v[82:83], v[106:107] op_sel_hi:[0,1]
	v_pk_mul_f32 v[106:107], v[82:83], v[108:109] op_sel_hi:[0,1]
	v_pk_mul_f32 v[82:83], v[82:83], v[110:111] op_sel_hi:[0,1]
	v_pk_fma_f32 v[48:49], v[26:27], v[94:95], v[48:49]
	v_pk_fma_f32 v[78:79], v[24:25], v[78:79], v[88:89]
	v_pk_fma_f32 v[46:47], v[10:11], v[98:99], v[46:47]
	v_pk_fma_f32 v[88:89], v[8:9], v[96:97], v[90:91]
	v_pk_fma_f32 v[44:45], v[14:15], v[102:103], v[44:45]
	v_pk_fma_f32 v[90:91], v[12:13], v[100:101], v[92:93]
	v_pk_fma_f32 v[42:43], v[30:31], v[82:83], v[42:43]
	s_waitcnt vmcnt(7)
	v_cvt_pk_f32_fp8_e32 v[82:83], v87
	v_cvt_pk_f32_fp8_sdwa v[92:93], v87 src0_sel:WORD_1
	s_waitcnt vmcnt(6)
	v_cvt_pk_f32_fp8_e32 v[94:95], v137
	v_cvt_pk_f32_fp8_sdwa v[96:97], v137 src0_sel:WORD_1
	s_waitcnt vmcnt(5)
	v_cvt_pk_f32_fp8_e32 v[98:99], v138
	v_cvt_pk_f32_fp8_sdwa v[100:101], v138 src0_sel:WORD_1
	s_waitcnt vmcnt(4)
	v_cvt_pk_f32_fp8_e32 v[102:103], v139
	v_pk_fma_f32 v[80:81], v[28:29], v[106:107], v[80:81]
	v_cvt_pk_f32_fp8_sdwa v[106:107], v139 src0_sel:WORD_1
	s_waitcnt lgkmcnt(0)
	s_nop 1
	v_add_f32_dpp v87, v105, v105 quad_perm:[1,0,3,2] row_mask:0xf bank_mask:0xf
	v_pk_mul_f32 v[92:93], v[104:105], v[92:93] op_sel_hi:[0,1]
	v_pk_mul_f32 v[82:83], v[104:105], v[82:83] op_sel_hi:[0,1]
	v_pk_mul_f32 v[96:97], v[104:105], v[96:97] op_sel_hi:[0,1]
	v_pk_mul_f32 v[94:95], v[104:105], v[94:95] op_sel_hi:[0,1]
	v_pk_mul_f32 v[100:101], v[104:105], v[100:101] op_sel_hi:[0,1]
	v_pk_mul_f32 v[98:99], v[104:105], v[98:99] op_sel_hi:[0,1]
	v_pk_mul_f32 v[102:103], v[104:105], v[102:103] op_sel_hi:[0,1]
	v_pk_mul_f32 v[106:107], v[104:105], v[106:107] op_sel_hi:[0,1]
	v_pk_fma_f32 v[78:79], v[24:25], v[82:83], v[78:79]
	v_pk_fma_f32 v[48:49], v[26:27], v[92:93], v[48:49]
	v_pk_fma_f32 v[82:83], v[8:9], v[94:95], v[88:89]
	v_pk_fma_f32 v[46:47], v[10:11], v[96:97], v[46:47]
	v_pk_fma_f32 v[88:89], v[12:13], v[98:99], v[90:91]
	v_pk_fma_f32 v[44:45], v[14:15], v[100:101], v[44:45]
	v_pk_fma_f32 v[80:81], v[28:29], v[102:103], v[80:81]
	s_waitcnt vmcnt(3)
	v_cvt_pk_f32_fp8_e32 v[90:91], v140
	v_cvt_pk_f32_fp8_sdwa v[92:93], v140 src0_sel:WORD_1
	s_waitcnt vmcnt(2)
	v_cvt_pk_f32_fp8_e32 v[94:95], v141
	v_cvt_pk_f32_fp8_sdwa v[96:97], v141 src0_sel:WORD_1
	s_waitcnt vmcnt(1)
	v_cvt_pk_f32_fp8_e32 v[98:99], v142
	v_cvt_pk_f32_fp8_sdwa v[100:101], v142 src0_sel:WORD_1
	s_waitcnt vmcnt(0)
	v_cvt_pk_f32_fp8_e32 v[102:103], v143
	v_cvt_pk_f32_fp8_sdwa v[104:105], v143 src0_sel:WORD_1
	v_pk_fma_f32 v[42:43], v[30:31], v[106:107], v[42:43]
	s_waitcnt lgkmcnt(0)
	s_nop 1
	v_add_f32_dpp v106, v87, v87 quad_perm:[2,3,0,1] row_mask:0xf bank_mask:0xf
	v_pk_mul_f32 v[90:91], v[86:87], v[90:91] op_sel_hi:[0,1]
	v_pk_mul_f32 v[92:93], v[86:87], v[92:93] op_sel_hi:[0,1]
	v_pk_mul_f32 v[94:95], v[86:87], v[94:95] op_sel_hi:[0,1]
	v_pk_mul_f32 v[96:97], v[86:87], v[96:97] op_sel_hi:[0,1]
	v_pk_mul_f32 v[98:99], v[86:87], v[98:99] op_sel_hi:[0,1]
	v_pk_mul_f32 v[100:101], v[86:87], v[100:101] op_sel_hi:[0,1]
	v_pk_mul_f32 v[102:103], v[86:87], v[102:103] op_sel_hi:[0,1]
	v_pk_mul_f32 v[86:87], v[86:87], v[104:105] op_sel_hi:[0,1]
	v_pk_fma_f32 v[78:79], v[24:25], v[90:91], v[78:79]
	v_pk_fma_f32 v[92:93], v[26:27], v[92:93], v[48:49]
	v_pk_fma_f32 v[86:87], v[30:31], v[86:87], v[42:43]
	v_pk_fma_f32 v[42:43], v[78:79], v[78:79], 0 op_sel_hi:[1,1,0]
	v_pk_fma_f32 v[82:83], v[8:9], v[94:95], v[82:83]
	v_pk_fma_f32 v[42:43], v[92:93], v[92:93], v[42:43]
	v_pk_fma_f32 v[90:91], v[10:11], v[96:97], v[46:47]
	v_pk_fma_f32 v[42:43], v[82:83], v[82:83], v[42:43]
	v_pk_fma_f32 v[94:95], v[14:15], v[100:101], v[44:45]
	v_pk_fma_f32 v[88:89], v[12:13], v[98:99], v[88:89]
	v_pk_fma_f32 v[42:43], v[90:91], v[90:91], v[42:43]
	s_waitcnt lgkmcnt(0)
	s_nop 1
	v_add_f32_dpp v44, v106, v106 row_half_mirror row_mask:0xf bank_mask:0xf
	v_pk_fma_f32 v[42:43], v[88:89], v[88:89], v[42:43]
	v_pk_fma_f32 v[80:81], v[28:29], v[102:103], v[80:81]
	v_pk_fma_f32 v[42:43], v[94:95], v[94:95], v[42:43]
	s_waitcnt lgkmcnt(0)
	s_nop 1
	v_add_f32_dpp v44, v44, v44 row_mirror row_mask:0xf bank_mask:0xf
	v_pk_fma_f32 v[42:43], v[80:81], v[80:81], v[42:43]
	v_pk_fma_f32 v[42:43], v[86:87], v[86:87], v[42:43]
	s_waitcnt lgkmcnt(0)
	v_mov_b32_e32 v45, v44
	s_nop 1
	v_permlane16_swap_b32_e32 v44, v45
	v_add_f32_e32 v44, v44, v45
	v_add_f32_e32 v42, v42, v43
	s_waitcnt lgkmcnt(0)
	s_nop 1
	v_add_f32_dpp v42, v42, v42 quad_perm:[1,0,3,2] row_mask:0xf bank_mask:0xf
	s_waitcnt lgkmcnt(0)
	v_mov_b32_e32 v45, v44
	s_nop 1
	v_permlane32_swap_b32_e32 v44, v45
	v_add_f32_e32 v44, v44, v45
	v_fmamk_f32 v44, v44, 0x3a800000, v69
	v_mul_f32_e32 v45, 0x4f800000, v44
	v_cmp_gt_f32_e32 vcc, s22, v44
	s_waitcnt lgkmcnt(0)
	s_nop 1
	v_add_f32_dpp v42, v42, v42 quad_perm:[2,3,0,1] row_mask:0xf bank_mask:0xf
	v_cndmask_b32_e32 v44, v44, v45, vcc
	v_sqrt_f32_e32 v45, v44
	s_waitcnt lgkmcnt(0)
	s_nop 1
	v_add_f32_dpp v42, v42, v42 row_half_mirror row_mask:0xf bank_mask:0xf
	v_add_u32_e32 v46, -1, v45
	v_add_u32_e32 v47, 1, v45
	v_fma_f32 v48, -v46, v45, v44
	v_fma_f32 v49, -v47, v45, v44
	v_cmp_ge_f32_e64 s[0:1], 0, v48
	s_waitcnt lgkmcnt(0)
	s_nop 1
	v_add_f32_dpp v42, v42, v42 row_mirror row_mask:0xf bank_mask:0xf
	v_cndmask_b32_e64 v45, v45, v46, s[0:1]
	v_cmp_lt_f32_e64 s[0:1], 0, v49
	s_nop 1
	v_cndmask_b32_e64 v43, v45, v47, s[0:1]
	v_mul_f32_e32 v46, 0x37800000, v43
	v_cndmask_b32_e32 v43, v43, v46, vcc
	v_cmp_class_f32_e32 vcc, v44, v70
	s_waitcnt lgkmcnt(0)
	v_mov_b32_e32 v45, v42
	s_nop 1
	v_permlane16_swap_b32_e32 v42, v45
	v_add_f32_e32 v42, v42, v45
	v_cndmask_b32_e32 v43, v43, v44, vcc
	v_div_scale_f32 v44, s[0:1], v43, v43, 1.0
	v_rcp_f32_e32 v47, v44
	v_div_scale_f32 v46, vcc, 1.0, v43, 1.0
	v_fma_f32 v48, -v44, v47, 1.0
	v_fmac_f32_e32 v47, v48, v47
	v_mul_f32_e32 v48, v46, v47
	s_waitcnt lgkmcnt(0)
	v_mov_b32_e32 v45, v42
	s_nop 1
	v_permlane32_swap_b32_e32 v42, v45
	v_add_f32_e32 v42, v42, v45
	v_fma_f32 v45, -v44, v48, v46
	v_fmamk_f32 v42, v42, 0x3a800000, v69
	v_fmac_f32_e32 v48, v45, v47
	v_mul_f32_e32 v45, 0x4f800000, v42
	v_cmp_gt_f32_e64 s[0:1], s22, v42
	v_fma_f32 v44, -v44, v48, v46
	s_nop 0
	v_cndmask_b32_e64 v96, v42, v45, s[0:1]
	v_div_fmas_f32 v42, v44, v47, v48
	v_sqrt_f32_e32 v97, v96
	v_div_fixup_f32 v42, v42, v43, 1.0
	v_pk_mul_f32 v[46:47], v[74:75], v[42:43] op_sel_hi:[1,0]
	v_pk_mul_f32 v[44:45], v[56:57], v[42:43] op_sel_hi:[1,0]
	v_pk_mul_f32 v[56:57], v[76:77], v[42:43] op_sel_hi:[1,0]
	v_pk_mul_f32 v[48:49], v[54:55], v[42:43] op_sel_hi:[1,0]
	v_pk_mul_f32 v[54:55], v[84:85], v[42:43] op_sel_hi:[1,0]
	v_pk_mul_f32 v[52:53], v[52:53], v[42:43] op_sel_hi:[1,0]
	v_pk_mul_f32 v[72:73], v[72:73], v[42:43] op_sel_hi:[1,0]
	v_pk_mul_f32 v[74:75], v[50:51], v[42:43] op_sel_hi:[1,0]
	v_pk_fma_f32 v[44:45], v[2:3], v[44:45], 0 op_sel_hi:[1,1,0]
	v_pk_fma_f32 v[42:43], v[0:1], v[46:47], 0 op_sel_hi:[1,1,0]
	v_pk_fma_f32 v[48:49], v[6:7], v[48:49], 0 op_sel_hi:[1,1,0]
	v_pk_fma_f32 v[46:47], v[4:5], v[56:57], 0 op_sel_hi:[1,1,0]
	v_pk_fma_f32 v[52:53], v[18:19], v[52:53], 0 op_sel_hi:[1,1,0]
	v_pk_fma_f32 v[50:51], v[16:17], v[54:55], 0 op_sel_hi:[1,1,0]
	v_pk_fma_f32 v[56:57], v[22:23], v[74:75], 0 op_sel_hi:[1,1,0]
	v_pk_fma_f32 v[54:55], v[20:21], v[72:73], 0 op_sel_hi:[1,1,0]
	global_store_dwordx4 v[60:61], v[42:45], off nt
	global_store_dwordx4 v[60:61], v[46:49], off offset:1024 nt
	global_store_dwordx4 v[60:61], v[50:53], off offset:2048 nt
	global_store_dwordx4 v[60:61], v[54:57], off offset:3072 nt
	v_add_u32_e32 v42, -1, v97
	v_add_u32_e32 v43, 1, v97
	v_fma_f32 v44, -v42, v97, v96
	v_fma_f32 v45, -v43, v97, v96
	v_cmp_ge_f32_e32 vcc, 0, v44
	s_nop 1
	v_cndmask_b32_e32 v42, v97, v42, vcc
	v_cmp_lt_f32_e32 vcc, 0, v45
	s_nop 1
	v_cndmask_b32_e32 v42, v42, v43, vcc
	v_mul_f32_e32 v43, 0x37800000, v42
	v_cndmask_b32_e64 v42, v42, v43, s[0:1]
	v_cmp_class_f32_e32 vcc, v96, v70
	s_nop 1
	v_cndmask_b32_e32 v42, v42, v96, vcc
	v_div_scale_f32 v43, s[0:1], v42, v42, 1.0
	v_rcp_f32_e32 v45, v43
	v_div_scale_f32 v44, vcc, 1.0, v42, 1.0
	v_fma_f32 v46, -v43, v45, 1.0
	v_fmac_f32_e32 v45, v46, v45
	v_mul_f32_e32 v46, v44, v45
	v_fma_f32 v47, -v43, v46, v44
	v_fmac_f32_e32 v46, v47, v45
	v_fma_f32 v43, -v43, v46, v44
	v_div_fmas_f32 v43, v43, v45, v46
	v_div_fixup_f32 v42, v43, v42, 1.0
	v_pk_mul_f32 v[46:47], v[78:79], v[42:43] op_sel_hi:[1,0]
	v_pk_mul_f32 v[44:45], v[92:93], v[42:43] op_sel_hi:[1,0]
	v_pk_mul_f32 v[50:51], v[82:83], v[42:43] op_sel_hi:[1,0]
	v_pk_mul_f32 v[48:49], v[90:91], v[42:43] op_sel_hi:[1,0]
	v_pk_mul_f32 v[54:55], v[88:89], v[42:43] op_sel_hi:[1,0]
	v_pk_mul_f32 v[52:53], v[94:95], v[42:43] op_sel_hi:[1,0]
	v_pk_mul_f32 v[60:61], v[80:81], v[42:43] op_sel_hi:[1,0]
	v_pk_mul_f32 v[56:57], v[86:87], v[42:43] op_sel_hi:[1,0]
	v_pk_fma_f32 v[44:45], v[2:3], v[44:45], 0 op_sel_hi:[1,1,0]
	v_pk_fma_f32 v[42:43], v[0:1], v[46:47], 0 op_sel_hi:[1,1,0]
	v_pk_fma_f32 v[48:49], v[6:7], v[48:49], 0 op_sel_hi:[1,1,0]
	v_pk_fma_f32 v[46:47], v[4:5], v[50:51], 0 op_sel_hi:[1,1,0]
	v_pk_fma_f32 v[52:53], v[18:19], v[52:53], 0 op_sel_hi:[1,1,0]
	v_pk_fma_f32 v[50:51], v[16:17], v[54:55], 0 op_sel_hi:[1,1,0]
	v_pk_fma_f32 v[56:57], v[22:23], v[56:57], 0 op_sel_hi:[1,1,0]
	v_pk_fma_f32 v[54:55], v[20:21], v[60:61], 0 op_sel_hi:[1,1,0]
	global_store_dwordx4 v[58:59], v[42:45], off nt
	global_store_dwordx4 v[58:59], v[46:49], off offset:1024 nt
	global_store_dwordx4 v[58:59], v[50:53], off offset:2048 nt
	global_store_dwordx4 v[58:59], v[54:57], off offset:3072 nt
	s_cbranch_scc0 .LBB0_1862
	s_add_i32 s92, s92, s96
	s_add_i32 s17, s17, s18
	s_add_i32 s19, s19, s20
	s_cmpk_gt_i32 s92, 0xff
	s_cbranch_scc0 .LBB0_1861
